# speedup vs baseline: 1.0259x; 1.0259x over previous
_Z10pre_kernelPKfS0_S0_S0_S0_S0_S0_S0_S0_S0_S0_PtPfS0_S0_S0_S0_S0_S0_S2_S2_S2_S0_S0_S0_S1_:
	s_cmpk_lt_u32 s2, 0x80
	s_cbranch_scc1 .Lpre_orig
	s_cmpk_lt_u32 s2, 0xa0
	s_cbranch_scc1 .Lpre_roleBC
	s_cmpk_lg_u32 s2, 0xa0
	s_cbranch_scc1 .Lpre_not160
	s_endpgm
.Lpre_not160:
	s_cmpk_lt_u32 s2, 0xad
	s_cbranch_scc1 .Lpre_roleD
.Lpre_orig:
	s_load_dwordx2 s[24:25], s[0:1], 0x58
	s_load_dwordx4 s[20:23], s[0:1], 0x0
	s_cmpk_gt_i32 s2, 0x7f
	s_mov_b64 s[4:5], -1
	s_cbranch_scc0 .LBB0_95
	s_load_dwordx2 s[26:27], s[0:1], 0x38
	s_cmpk_gt_u32 s2, 0x9f
	s_cbranch_scc0 .LBB0_28
	s_cmpk_lg_i32 s2, 0xa0
	s_cbranch_scc0 .LBB0_17
	s_cmpk_gt_u32 s2, 0xac
	v_and_b32_e32 v24, 15, v0
	s_cbranch_scc0 .LBB0_13
	s_add_i32 s12, s2, 0xffffff53
	s_mul_hi_u32 s3, s12, 0xaaaaaaab
	s_lshr_b32 s3, s3, 3
	s_mul_i32 s13, s3, 12
	s_sub_i32 s13, s12, s13
	s_load_dwordx2 s[16:17], s[0:1], 0x88
	s_load_dwordx8 s[4:11], s[0:1], 0x68
	s_lshl_b32 s14, s13, 6
	s_lshr_b32 s12, s13, 2
	s_and_b32 s14, s14, 0xc0
	s_cmp_lt_u32 s13, 8
	s_cselect_b64 s[18:19], -1, 0
	s_lshl_b32 s28, s12, 8
	s_mov_b32 s29, 0
	s_lshl_b64 s[28:29], s[28:29], 2
	s_waitcnt lgkmcnt(0)
	s_add_u32 s15, s10, s28
	s_addc_u32 s28, s11, s29
	s_and_b64 s[10:11], s[18:19], exec
	s_cselect_b32 s10, s28, s17
	s_cselect_b32 s11, s15, s16
	s_lshl_b32 s15, s14, 2
	s_add_u32 s16, s11, s15
	s_addc_u32 s17, s10, 0
	v_bfe_u32 v25, v0, 4, 2
	s_and_b64 s[10:11], s[18:19], exec
	v_lshlrev_b32_e32 v6, 3, v25
	v_mov_b32_e32 v7, 0
	s_cselect_b32 s10, 9, 8
	v_lshlrev_b64 v[2:3], s10, v[6:7]
	v_lshl_add_u64 v[2:3], v[2:3], 2, s[16:17]
	v_and_b32_e32 v6, 0xc0, v0
	v_lshl_add_u64 v[2:3], v[2:3], 0, v[6:7]
	v_lshlrev_b32_e32 v6, 2, v24
	v_lshl_add_u64 v[2:3], v[2:3], 0, v[6:7]
	s_lshl_b64 s[16:17], 1, s10
	v_lshl_add_u64 v[4:5], s[16:17], 2, v[2:3]
	s_lshl_b64 s[16:17], 2, s10
	v_lshl_add_u64 v[8:9], s[16:17], 2, v[2:3]
	s_lshl_b64 s[16:17], 3, s10
	v_lshl_add_u64 v[10:11], s[16:17], 2, v[2:3]
	s_lshl_b64 s[16:17], 4, s10
	v_lshl_add_u64 v[12:13], s[16:17], 2, v[2:3]
	s_lshl_b64 s[16:17], 5, s10
	v_lshl_add_u64 v[14:15], s[16:17], 2, v[2:3]
	s_lshl_b64 s[16:17], 6, s10
	v_lshl_add_u64 v[16:17], s[16:17], 2, v[2:3]
	s_lshl_b64 s[16:17], 7, s10
	v_lshl_add_u64 v[18:19], s[16:17], 2, v[2:3]
	s_lshl_b64 s[16:17], 32, s10
	global_load_dword v48, v[2:3], off
	global_load_dword v49, v[4:5], off
	global_load_dword v50, v[8:9], off
	global_load_dword v51, v[10:11], off
	global_load_dword v52, v[12:13], off
	global_load_dword v53, v[14:15], off
	global_load_dword v54, v[16:17], off
	global_load_dword v55, v[18:19], off
	v_lshl_add_u64 v[4:5], s[16:17], 2, v[2:3]
	s_lshl_b64 s[16:17], 33, s10
	v_lshl_add_u64 v[8:9], s[16:17], 2, v[2:3]
	s_lshl_b64 s[16:17], 34, s10
	v_lshl_add_u64 v[10:11], s[16:17], 2, v[2:3]
	s_lshl_b64 s[16:17], 35, s10
	v_lshl_add_u64 v[12:13], s[16:17], 2, v[2:3]
	s_lshl_b64 s[16:17], 36, s10
	v_lshl_add_u64 v[14:15], s[16:17], 2, v[2:3]
	s_lshl_b64 s[16:17], 37, s10
	v_lshl_add_u64 v[16:17], s[16:17], 2, v[2:3]
	s_lshl_b64 s[16:17], 38, s10
	v_lshl_add_u64 v[18:19], s[16:17], 2, v[2:3]
	s_lshl_b64 s[16:17], 39, s10
	v_lshl_add_u64 v[20:21], s[16:17], 2, v[2:3]
	s_lshl_b64 s[16:17], 64, s10
	global_load_dword v56, v[4:5], off
	global_load_dword v57, v[8:9], off
	global_load_dword v58, v[10:11], off
	global_load_dword v59, v[12:13], off
	global_load_dword v60, v[14:15], off
	global_load_dword v61, v[16:17], off
	global_load_dword v62, v[18:19], off
	global_load_dword v63, v[20:21], off
	v_lshl_add_u64 v[4:5], s[16:17], 2, v[2:3]
	s_lshl_b64 s[16:17], 0x41, s10
	v_lshl_add_u64 v[8:9], s[16:17], 2, v[2:3]
	s_lshl_b64 s[16:17], 0x42, s10
	v_lshl_add_u64 v[10:11], s[16:17], 2, v[2:3]
	s_lshl_b64 s[16:17], 0x43, s10
	v_lshl_add_u64 v[12:13], s[16:17], 2, v[2:3]
	s_lshl_b64 s[16:17], 0x44, s10
	v_lshl_add_u64 v[14:15], s[16:17], 2, v[2:3]
	s_lshl_b64 s[16:17], 0x45, s10
	v_lshl_add_u64 v[16:17], s[16:17], 2, v[2:3]
	s_lshl_b64 s[16:17], 0x46, s10
	v_lshl_add_u64 v[18:19], s[16:17], 2, v[2:3]
	s_lshl_b64 s[16:17], 0x47, s10
	v_lshl_add_u64 v[20:21], s[16:17], 2, v[2:3]
	s_lshl_b64 s[16:17], 0x60, s10
	global_load_dword v64, v[4:5], off
	global_load_dword v65, v[8:9], off
	global_load_dword v66, v[10:11], off
	global_load_dword v67, v[12:13], off
	global_load_dword v68, v[14:15], off
	global_load_dword v69, v[16:17], off
	global_load_dword v70, v[18:19], off
	global_load_dword v71, v[20:21], off
	v_lshl_add_u64 v[4:5], s[16:17], 2, v[2:3]
	s_lshl_b64 s[16:17], 0x61, s10
	v_lshl_add_u64 v[8:9], s[16:17], 2, v[2:3]
	s_lshl_b64 s[16:17], 0x62, s10
	v_lshl_add_u64 v[10:11], s[16:17], 2, v[2:3]
	s_lshl_b64 s[16:17], 0x63, s10
	v_lshl_add_u64 v[12:13], s[16:17], 2, v[2:3]
	s_lshl_b64 s[16:17], 0x64, s10
	v_lshl_add_u64 v[14:15], s[16:17], 2, v[2:3]
	s_lshl_b64 s[16:17], 0x65, s10
	v_lshl_add_u64 v[16:17], s[16:17], 2, v[2:3]
	s_lshl_b64 s[16:17], 0x66, s10
	v_lshrrev_b32_e32 v1, 6, v0
	v_lshl_add_u64 v[18:19], s[16:17], 2, v[2:3]
	s_lshl_b64 s[16:17], 0x67, s10
	v_and_b32_e32 v80, 63, v0
	v_lshl_add_u64 v[20:21], s[16:17], 2, v[2:3]
	global_load_dword v72, v[4:5], off
	global_load_dword v73, v[8:9], off
	global_load_dword v74, v[10:11], off
	global_load_dword v75, v[12:13], off
	global_load_dword v76, v[14:15], off
	global_load_dword v77, v[16:17], off
	global_load_dword v78, v[18:19], off
	global_load_dword v79, v[20:21], off
	v_lshlrev_b32_e32 v10, 10, v1
	v_lshlrev_b32_e32 v6, 4, v80
	v_lshl_or_b32 v22, s3, 12, v10
	v_lshl_add_u64 v[20:21], s[4:5], 0, v[6:7]
	v_ashrrev_i32_e32 v23, 31, v22
	v_lshl_add_u64 v[10:11], v[22:23], 2, v[20:21]
	global_load_dwordx4 v[10:13], v[10:11], off
	s_lshl_b64 s[16:17], 0x80, s10
	v_lshl_add_u64 v[4:5], s[16:17], 2, v[2:3]
	s_lshl_b64 s[16:17], 0x81, s10
	v_lshl_add_u64 v[8:9], s[16:17], 2, v[2:3]
	s_lshl_b64 s[16:17], 0x82, s10
	v_lshl_add_u64 v[14:15], s[16:17], 2, v[2:3]
	s_lshl_b64 s[16:17], 0x83, s10
	v_lshl_add_u64 v[16:17], s[16:17], 2, v[2:3]
	s_lshl_b64 s[16:17], 0x84, s10
	v_lshl_add_u64 v[18:19], s[16:17], 2, v[2:3]
	s_lshl_b64 s[16:17], 0x85, s10
	v_lshl_add_u64 v[26:27], s[16:17], 2, v[2:3]
	s_lshl_b64 s[16:17], 0x86, s10
	v_lshl_add_u64 v[28:29], s[16:17], 2, v[2:3]
	s_lshl_b64 s[16:17], 0x87, s10
	s_lshl_b64 s[4:5], 0xa0, s10
	v_lshl_add_u64 v[30:31], s[16:17], 2, v[2:3]
	global_load_dword v81, v[4:5], off
	global_load_dword v82, v[8:9], off
	global_load_dword v83, v[14:15], off
	global_load_dword v84, v[16:17], off
	global_load_dword v85, v[18:19], off
	global_load_dword v86, v[26:27], off
	global_load_dword v87, v[28:29], off
	global_load_dword v88, v[30:31], off
	v_lshl_add_u64 v[4:5], s[4:5], 2, v[2:3]
	s_lshl_b64 s[4:5], 0xa1, s10
	v_lshl_add_u64 v[8:9], s[4:5], 2, v[2:3]
	s_lshl_b64 s[4:5], 0xa2, s10
	v_lshl_add_u64 v[18:19], s[4:5], 2, v[2:3]
	s_lshl_b64 s[4:5], 0xa3, s10
	v_lshl_add_u64 v[26:27], s[4:5], 2, v[2:3]
	s_lshl_b64 s[4:5], 0xa4, s10
	v_lshl_add_u64 v[28:29], s[4:5], 2, v[2:3]
	s_lshl_b64 s[4:5], 0xa5, s10
	v_or_b32_e32 v14, 0x100, v22
	v_lshl_add_u64 v[30:31], s[4:5], 2, v[2:3]
	s_lshl_b64 s[4:5], 0xa6, s10
	v_ashrrev_i32_e32 v15, 31, v14
	v_lshl_add_u64 v[32:33], s[4:5], 2, v[2:3]
	s_lshl_b64 s[4:5], 0xa7, s10
	v_lshl_add_u64 v[14:15], v[14:15], 2, v[20:21]
	v_lshl_add_u64 v[34:35], s[4:5], 2, v[2:3]
	global_load_dwordx4 v[14:17], v[14:15], off
	s_nop 0
	global_load_dword v89, v[4:5], off
	global_load_dword v90, v[8:9], off
	global_load_dword v91, v[18:19], off
	global_load_dword v92, v[26:27], off
	global_load_dword v93, v[28:29], off
	global_load_dword v94, v[30:31], off
	global_load_dword v95, v[32:33], off
	global_load_dword v96, v[34:35], off
	s_lshl_b64 s[4:5], 0xc0, s10
	v_lshl_add_u64 v[4:5], s[4:5], 2, v[2:3]
	s_lshl_b64 s[4:5], 0xc1, s10
	v_lshl_add_u64 v[8:9], s[4:5], 2, v[2:3]
	s_lshl_b64 s[4:5], 0xc2, s10
	v_lshl_add_u64 v[18:19], s[4:5], 2, v[2:3]
	s_lshl_b64 s[4:5], 0xc3, s10
	v_lshl_add_u64 v[26:27], s[4:5], 2, v[2:3]
	s_lshl_b64 s[4:5], 0xc4, s10
	v_lshl_add_u64 v[28:29], s[4:5], 2, v[2:3]
	s_lshl_b64 s[4:5], 0xc5, s10
	v_lshl_add_u64 v[30:31], s[4:5], 2, v[2:3]
	s_lshl_b64 s[4:5], 0xc6, s10
	v_lshl_add_u64 v[32:33], s[4:5], 2, v[2:3]
	s_lshl_b64 s[4:5], 0xc7, s10
	v_lshl_add_u64 v[34:35], s[4:5], 2, v[2:3]
	global_load_dword v97, v[4:5], off
	global_load_dword v98, v[8:9], off
	global_load_dword v99, v[18:19], off
	global_load_dword v100, v[26:27], off
	global_load_dword v101, v[28:29], off
	global_load_dword v102, v[30:31], off
	global_load_dword v103, v[32:33], off
	global_load_dword v104, v[34:35], off
	s_lshl_b64 s[4:5], 0xe0, s10
	v_lshl_add_u64 v[26:27], s[4:5], 2, v[2:3]
	s_lshl_b64 s[4:5], 0xe1, s10
	v_lshl_add_u64 v[28:29], s[4:5], 2, v[2:3]
	s_lshl_b64 s[4:5], 0xe2, s10
	v_lshl_add_u64 v[30:31], s[4:5], 2, v[2:3]
	s_lshl_b64 s[4:5], 0xe3, s10
	v_lshl_add_u64 v[32:33], s[4:5], 2, v[2:3]
	s_lshl_b64 s[4:5], 0xe4, s10
	v_lshl_add_u64 v[34:35], s[4:5], 2, v[2:3]
	s_lshl_b64 s[4:5], 0xe5, s10
	v_lshl_add_u64 v[36:37], s[4:5], 2, v[2:3]
	s_lshl_b64 s[4:5], 0xe6, s10
	v_lshl_add_u64 v[38:39], s[4:5], 2, v[2:3]
	s_lshl_b64 s[4:5], 0xe7, s10
	v_lshl_add_u64 v[40:41], s[4:5], 2, v[2:3]
	global_load_dwordx4 v[2:5], v6, s[6:7]
	s_nop 0
	global_load_dwordx4 v[6:9], v6, s[8:9]
	s_mov_b32 s6, 0x3727c5ac
	s_mov_b32 s4, 0x3b800000
	s_cmp_gt_u32 s13, 3
	s_waitcnt vmcnt(27)
	v_add_f32_e32 v18, v10, v11
	v_add_f32_e32 v18, v12, v18
	v_add_f32_e32 v18, v13, v18
	s_nop 1
	v_add_f32_dpp v18, v18, v18 quad_perm:[1,0,3,2] row_mask:0xf bank_mask:0xf bound_ctrl:1
	s_nop 1
	v_add_f32_dpp v18, v18, v18 quad_perm:[2,3,0,1] row_mask:0xf bank_mask:0xf bound_ctrl:1
	s_nop 1
	v_add_f32_dpp v18, v18, v18 row_half_mirror row_mask:0xf bank_mask:0xf bound_ctrl:1
	s_nop 1
	v_add_f32_dpp v18, v18, v18 row_mirror row_mask:0xf bank_mask:0xf bound_ctrl:1
	v_mov_b32_e32 v19, v18
	s_nop 1
	v_permlane16_swap_b32_e32 v18, v19
	v_add_f32_e32 v18, v18, v19
	v_mov_b32_e32 v19, v18
	s_nop 1
	v_permlane32_swap_b32_e32 v18, v19
	v_add_f32_e32 v18, v18, v19
	v_fmac_f32_e32 v11, 0xbb800000, v18
	v_fmamk_f32 v13, v18, 0xbb800000, v13
	v_fmamk_f32 v12, v18, 0xbb800000, v12
	v_fmamk_f32 v10, v18, 0xbb800000, v10
	v_mul_f32_e32 v18, v11, v11
	v_fmac_f32_e32 v18, v10, v10
	v_fmac_f32_e32 v18, v12, v12
	v_fmac_f32_e32 v18, v13, v13
	s_nop 1
	v_add_f32_dpp v18, v18, v18 quad_perm:[1,0,3,2] row_mask:0xf bank_mask:0xf bound_ctrl:1
	s_nop 1
	v_add_f32_dpp v18, v18, v18 quad_perm:[2,3,0,1] row_mask:0xf bank_mask:0xf bound_ctrl:1
	s_nop 1
	v_add_f32_dpp v18, v18, v18 row_half_mirror row_mask:0xf bank_mask:0xf bound_ctrl:1
	s_nop 1
	v_add_f32_dpp v18, v18, v18 row_mirror row_mask:0xf bank_mask:0xf bound_ctrl:1
	v_mov_b32_e32 v19, v18
	s_nop 1
	v_permlane16_swap_b32_e32 v18, v19
	v_add_f32_e32 v45, v18, v19
	s_waitcnt vmcnt(18)
	v_add_f32_e32 v18, v14, v15
	v_add_f32_e32 v18, v16, v18
	v_add_f32_e32 v18, v17, v18
	v_mov_b32_e32 v47, v45
	s_nop 1
	v_permlane32_swap_b32_e32 v45, v47
	v_add_f32_dpp v18, v18, v18 quad_perm:[1,0,3,2] row_mask:0xf bank_mask:0xf bound_ctrl:1
	s_nop 1
	v_add_f32_dpp v18, v18, v18 quad_perm:[2,3,0,1] row_mask:0xf bank_mask:0xf bound_ctrl:1
	s_nop 1
	v_add_f32_dpp v18, v18, v18 row_half_mirror row_mask:0xf bank_mask:0xf bound_ctrl:1
	s_nop 1
	v_add_f32_dpp v18, v18, v18 row_mirror row_mask:0xf bank_mask:0xf bound_ctrl:1
	v_mov_b32_e32 v19, v18
	s_nop 1
	v_permlane16_swap_b32_e32 v18, v19
	v_add_f32_e32 v18, v18, v19
	v_mov_b32_e32 v19, v18
	s_nop 1
	v_permlane32_swap_b32_e32 v18, v19
	v_add_f32_e32 v18, v18, v19
	v_fmamk_f32 v42, v18, 0xbb800000, v16
	v_or_b32_e32 v16, 0x200, v22
	v_fmamk_f32 v43, v18, 0xbb800000, v17
	v_ashrrev_i32_e32 v17, 31, v16
	v_lshl_add_u64 v[16:17], v[16:17], 2, v[20:21]
	v_fmamk_f32 v14, v18, 0xbb800000, v14
	v_fmac_f32_e32 v15, 0xbb800000, v18
	global_load_dwordx4 v[16:19], v[16:17], off
	v_mul_f32_e32 v23, v15, v15
	v_fmac_f32_e32 v23, v14, v14
	v_fmac_f32_e32 v23, v42, v42
	v_fmac_f32_e32 v23, v43, v43
	v_or_b32_e32 v22, 0x300, v22
	s_nop 0
	v_add_f32_dpp v23, v23, v23 quad_perm:[1,0,3,2] row_mask:0xf bank_mask:0xf bound_ctrl:1
	s_nop 1
	v_add_f32_dpp v23, v23, v23 quad_perm:[2,3,0,1] row_mask:0xf bank_mask:0xf bound_ctrl:1
	s_nop 1
	v_add_f32_dpp v23, v23, v23 row_half_mirror row_mask:0xf bank_mask:0xf bound_ctrl:1
	s_nop 1
	v_add_f32_dpp v23, v23, v23 row_mirror row_mask:0xf bank_mask:0xf bound_ctrl:1
	v_mov_b32_e32 v44, v23
	s_nop 1
	v_permlane16_swap_b32_e32 v23, v44
	v_add_f32_e32 v44, v23, v44
	v_mov_b32_e32 v46, v44
	s_nop 1
	v_permlane32_swap_b32_e32 v44, v46
	v_pk_add_f32 v[46:47], v[44:45], v[46:47]
	v_mov_b64_e32 v[44:45], s[6:7]
	v_pk_fma_f32 v[46:47], v[46:47], s[4:5], v[44:45] op_sel_hi:[1,0,0]
	s_mov_b32 s5, 0x800000
	v_mul_f32_e32 v23, 0x4b800000, v47
	v_cmp_gt_f32_e32 vcc, s5, v47
	s_movk_i32 s6, 0x7fff
	s_nop 0
	v_cndmask_b32_e32 v23, v47, v23, vcc
	v_rsq_f32_e32 v47, v23
	v_ashrrev_i32_e32 v23, 31, v22
	v_lshl_add_u64 v[20:21], v[22:23], 2, v[20:21]
	global_load_dwordx4 v[20:23], v[20:21], off
	s_nop 0
	global_load_dword v26, v[26:27], off
	s_nop 0
	global_load_dword v27, v[28:29], off
	s_nop 0
	global_load_dword v28, v[30:31], off
	global_load_dword v29, v[32:33], off
	s_nop 0
	global_load_dword v30, v[34:35], off
	global_load_dword v31, v[36:37], off
	global_load_dword v32, v[38:39], off
	global_load_dword v33, v[40:41], off
	v_lshlrev_b32_e32 v34, 11, v1
	v_lshl_or_b32 v36, v80, 3, v34
	v_mul_f32_e32 v34, 0x45800000, v47
	v_cndmask_b32_e32 v34, v47, v34, vcc
	v_pk_mul_f32 v[12:13], v[12:13], v[34:35] op_sel_hi:[1,0]
	v_mov_b32_e32 v37, 1
	s_waitcnt vmcnt(10)
	v_pk_fma_f32 v[12:13], v[4:5], v[12:13], v[8:9]
	v_pk_mul_f32 v[10:11], v[10:11], v[34:35] op_sel_hi:[1,0]
	v_and_b32_sdwa v34, v12, v37 dst_sel:DWORD dst_unused:UNUSED_PAD src0_sel:WORD_1 src1_sel:DWORD
	v_add3_u32 v12, v12, v34, s6
	v_and_b32_sdwa v34, v13, v37 dst_sel:DWORD dst_unused:UNUSED_PAD src0_sel:WORD_1 src1_sel:DWORD
	v_add3_u32 v13, v13, v34, s6
	v_mul_f32_e32 v34, 0x4b800000, v46
	v_cmp_gt_f32_e32 vcc, s5, v46
	v_pk_fma_f32 v[10:11], v[2:3], v[10:11], v[6:7]
	v_and_b32_e32 v13, 0xffff0000, v13
	v_cndmask_b32_e32 v34, v46, v34, vcc
	v_rsq_f32_e32 v34, v34
	v_and_b32_sdwa v35, v10, v37 dst_sel:DWORD dst_unused:UNUSED_PAD src0_sel:WORD_1 src1_sel:DWORD
	v_add3_u32 v10, v10, v35, s6
	v_and_b32_sdwa v35, v11, v37 dst_sel:DWORD dst_unused:UNUSED_PAD src0_sel:WORD_1 src1_sel:DWORD
	v_add3_u32 v11, v11, v35, s6
	v_and_b32_e32 v35, 0xffff0000, v11
	v_or_b32_sdwa v11, v13, v12 dst_sel:DWORD dst_unused:UNUSED_PAD src0_sel:DWORD src1_sel:WORD_1
	v_mul_f32_e32 v12, 0x45800000, v34
	v_cndmask_b32_e32 v12, v34, v12, vcc
	v_or_b32_sdwa v10, v35, v10 dst_sel:DWORD dst_unused:UNUSED_PAD src0_sel:DWORD src1_sel:WORD_1
	v_pk_mul_f32 v[34:35], v[42:43], v[12:13] op_sel_hi:[1,0]
	v_pk_mul_f32 v[12:13], v[14:15], v[12:13] op_sel_hi:[1,0]
	v_pk_fma_f32 v[14:15], v[4:5], v[34:35], v[8:9]
	v_pk_fma_f32 v[12:13], v[2:3], v[12:13], v[6:7]
	v_and_b32_sdwa v34, v14, v37 dst_sel:DWORD dst_unused:UNUSED_PAD src0_sel:WORD_1 src1_sel:DWORD
	v_and_b32_sdwa v35, v12, v37 dst_sel:DWORD dst_unused:UNUSED_PAD src0_sel:WORD_1 src1_sel:DWORD
	v_add3_u32 v35, v12, v35, s6
	v_and_b32_sdwa v12, v15, v37 dst_sel:DWORD dst_unused:UNUSED_PAD src0_sel:WORD_1 src1_sel:DWORD
	v_add3_u32 v12, v15, v12, s6
	v_and_b32_e32 v38, 0xffff0000, v12
	v_add3_u32 v34, v14, v34, s6
	v_and_b32_sdwa v14, v13, v37 dst_sel:DWORD dst_unused:UNUSED_PAD src0_sel:WORD_1 src1_sel:DWORD
	v_add3_u32 v13, v13, v14, s6
	v_and_b32_e32 v39, 0xffff0000, v13
	s_waitcnt vmcnt(9)
	v_add_f32_e32 v12, v16, v17
	v_add_f32_e32 v12, v18, v12
	v_add_f32_e32 v12, v19, v12
	s_nop 1
	v_add_f32_dpp v12, v12, v12 quad_perm:[1,0,3,2] row_mask:0xf bank_mask:0xf bound_ctrl:1
	s_nop 1
	v_add_f32_dpp v12, v12, v12 quad_perm:[2,3,0,1] row_mask:0xf bank_mask:0xf bound_ctrl:1
	s_nop 1
	v_add_f32_dpp v12, v12, v12 row_half_mirror row_mask:0xf bank_mask:0xf bound_ctrl:1
	s_nop 1
	v_add_f32_dpp v12, v12, v12 row_mirror row_mask:0xf bank_mask:0xf bound_ctrl:1
	v_mov_b32_e32 v13, v12
	s_nop 1
	v_permlane16_swap_b32_e32 v12, v13
	v_add_f32_e32 v12, v12, v13
	v_mov_b32_e32 v13, v12
	s_nop 1
	v_permlane32_swap_b32_e32 v12, v13
	v_add_f32_e32 v14, v12, v13
	v_fmac_f32_e32 v17, 0xbb800000, v14
	v_fmamk_f32 v13, v14, 0xbb800000, v19
	v_fmamk_f32 v12, v14, 0xbb800000, v18
	v_fmamk_f32 v16, v14, 0xbb800000, v16
	v_mul_f32_e32 v14, v17, v17
	v_fmac_f32_e32 v14, v16, v16
	v_fmac_f32_e32 v14, v12, v12
	v_fmac_f32_e32 v14, v13, v13
	s_nop 1
	v_add_f32_dpp v14, v14, v14 quad_perm:[1,0,3,2] row_mask:0xf bank_mask:0xf bound_ctrl:1
	s_nop 1
	v_add_f32_dpp v14, v14, v14 quad_perm:[2,3,0,1] row_mask:0xf bank_mask:0xf bound_ctrl:1
	s_nop 1
	v_add_f32_dpp v14, v14, v14 row_half_mirror row_mask:0xf bank_mask:0xf bound_ctrl:1
	s_nop 1
	v_add_f32_dpp v14, v14, v14 row_mirror row_mask:0xf bank_mask:0xf bound_ctrl:1
	v_mov_b32_e32 v15, v14
	s_nop 1
	v_permlane16_swap_b32_e32 v14, v15
	v_add_f32_e32 v15, v14, v15
	s_waitcnt vmcnt(8)
	v_add_f32_e32 v14, v20, v21
	v_add_f32_e32 v14, v22, v14
	v_add_f32_e32 v14, v23, v14
	v_mov_b32_e32 v19, v15
	s_nop 1
	v_permlane32_swap_b32_e32 v15, v19
	v_add_f32_dpp v14, v14, v14 quad_perm:[1,0,3,2] row_mask:0xf bank_mask:0xf bound_ctrl:1
	s_nop 1
	v_add_f32_dpp v14, v14, v14 quad_perm:[2,3,0,1] row_mask:0xf bank_mask:0xf bound_ctrl:1
	s_nop 1
	v_add_f32_dpp v14, v14, v14 row_half_mirror row_mask:0xf bank_mask:0xf bound_ctrl:1
	s_nop 1
	v_add_f32_dpp v14, v14, v14 row_mirror row_mask:0xf bank_mask:0xf bound_ctrl:1
	v_mov_b32_e32 v18, v14
	s_nop 1
	v_permlane16_swap_b32_e32 v14, v18
	v_add_f32_e32 v14, v14, v18
	v_mov_b32_e32 v18, v14
	s_nop 1
	v_permlane32_swap_b32_e32 v14, v18
	v_add_f32_e32 v14, v14, v18
	v_fmac_f32_e32 v21, 0xbb800000, v14
	v_fmamk_f32 v23, v14, 0xbb800000, v23
	v_fmamk_f32 v22, v14, 0xbb800000, v22
	v_fmamk_f32 v20, v14, 0xbb800000, v20
	v_mul_f32_e32 v14, v21, v21
	v_fmac_f32_e32 v14, v20, v20
	v_fmac_f32_e32 v14, v22, v22
	v_fmac_f32_e32 v14, v23, v23
	s_nop 1
	v_add_f32_dpp v14, v14, v14 quad_perm:[1,0,3,2] row_mask:0xf bank_mask:0xf bound_ctrl:1
	s_nop 1
	v_add_f32_dpp v14, v14, v14 quad_perm:[2,3,0,1] row_mask:0xf bank_mask:0xf bound_ctrl:1
	s_nop 1
	v_add_f32_dpp v14, v14, v14 row_half_mirror row_mask:0xf bank_mask:0xf bound_ctrl:1
	s_nop 1
	v_add_f32_dpp v14, v14, v14 row_mirror row_mask:0xf bank_mask:0xf bound_ctrl:1
	v_mov_b32_e32 v18, v14
	s_nop 1
	v_permlane16_swap_b32_e32 v14, v18
	v_add_f32_e32 v14, v14, v18
	v_mov_b32_e32 v18, v14
	s_nop 1
	v_permlane32_swap_b32_e32 v14, v18
	v_pk_add_f32 v[14:15], v[14:15], v[18:19]
	v_or_b32_sdwa v19, v38, v34 dst_sel:DWORD dst_unused:UNUSED_PAD src0_sel:DWORD src1_sel:WORD_1
	v_pk_fma_f32 v[14:15], v[14:15], s[4:5], v[44:45] op_sel_hi:[1,0,0]
	s_nop 0
	v_mul_f32_e32 v18, 0x4b800000, v15
	v_cmp_gt_f32_e32 vcc, s5, v15
	s_nop 1
	v_cndmask_b32_e32 v15, v15, v18, vcc
	v_rsq_f32_e32 v15, v15
	v_or_b32_sdwa v18, v39, v35 dst_sel:DWORD dst_unused:UNUSED_PAD src0_sel:DWORD src1_sel:WORD_1
	ds_write2st64_b64 v36, v[10:11], v[18:19] offset0:64 offset1:65
	v_mul_f32_e32 v10, 0x45800000, v15
	v_cndmask_b32_e32 v10, v15, v10, vcc
	v_pk_mul_f32 v[12:13], v[12:13], v[10:11] op_sel_hi:[1,0]
	v_cmp_gt_f32_e32 vcc, s5, v14
	v_pk_fma_f32 v[12:13], v[4:5], v[12:13], v[8:9]
	v_pk_mul_f32 v[10:11], v[16:17], v[10:11] op_sel_hi:[1,0]
	v_and_b32_sdwa v15, v12, v37 dst_sel:DWORD dst_unused:UNUSED_PAD src0_sel:WORD_1 src1_sel:DWORD
	v_add3_u32 v12, v12, v15, s6
	v_and_b32_sdwa v15, v13, v37 dst_sel:DWORD dst_unused:UNUSED_PAD src0_sel:WORD_1 src1_sel:DWORD
	v_add3_u32 v13, v13, v15, s6
	v_mul_f32_e32 v15, 0x4b800000, v14
	v_cndmask_b32_e32 v14, v14, v15, vcc
	v_pk_fma_f32 v[10:11], v[2:3], v[10:11], v[6:7]
	v_rsq_f32_e32 v14, v14
	v_and_b32_sdwa v16, v10, v37 dst_sel:DWORD dst_unused:UNUSED_PAD src0_sel:WORD_1 src1_sel:DWORD
	v_add3_u32 v10, v10, v16, s6
	v_and_b32_sdwa v16, v11, v37 dst_sel:DWORD dst_unused:UNUSED_PAD src0_sel:WORD_1 src1_sel:DWORD
	v_add3_u32 v11, v11, v16, s6
	v_and_b32_e32 v13, 0xffff0000, v13
	v_and_b32_e32 v15, 0xffff0000, v11
	v_or_b32_sdwa v11, v13, v12 dst_sel:DWORD dst_unused:UNUSED_PAD src0_sel:DWORD src1_sel:WORD_1
	v_mul_f32_e32 v12, 0x45800000, v14
	v_cndmask_b32_e32 v12, v14, v12, vcc
	v_or_b32_sdwa v10, v15, v10 dst_sel:DWORD dst_unused:UNUSED_PAD src0_sel:DWORD src1_sel:WORD_1
	v_pk_mul_f32 v[14:15], v[22:23], v[12:13] op_sel_hi:[1,0]
	v_pk_mul_f32 v[12:13], v[20:21], v[12:13] op_sel_hi:[1,0]
	v_pk_fma_f32 v[4:5], v[4:5], v[14:15], v[8:9]
	v_pk_fma_f32 v[2:3], v[2:3], v[12:13], v[6:7]
	v_and_b32_sdwa v6, v4, v37 dst_sel:DWORD dst_unused:UNUSED_PAD src0_sel:WORD_1 src1_sel:DWORD
	v_and_b32_sdwa v7, v2, v37 dst_sel:DWORD dst_unused:UNUSED_PAD src0_sel:WORD_1 src1_sel:DWORD
	v_add3_u32 v2, v2, v7, s6
	v_add3_u32 v4, v4, v6, s6
	v_and_b32_sdwa v6, v5, v37 dst_sel:DWORD dst_unused:UNUSED_PAD src0_sel:WORD_1 src1_sel:DWORD
	v_and_b32_sdwa v7, v3, v37 dst_sel:DWORD dst_unused:UNUSED_PAD src0_sel:WORD_1 src1_sel:DWORD
	v_add3_u32 v5, v5, v6, s6
	v_add3_u32 v3, v3, v7, s6
	v_and_b32_e32 v5, 0xffff0000, v5
	v_and_b32_e32 v6, 0xffff0000, v3
	v_or_b32_sdwa v3, v5, v4 dst_sel:DWORD dst_unused:UNUSED_PAD src0_sel:DWORD src1_sel:WORD_1
	v_or_b32_sdwa v2, v6, v2 dst_sel:DWORD dst_unused:UNUSED_PAD src0_sel:DWORD src1_sel:WORD_1
	ds_write2st64_b64 v36, v[10:11], v[2:3] offset0:66 offset1:67
	v_and_b32_e32 v2, 48, v0
	v_lshl_or_b32 v18, v24, 9, v2
	v_cvt_pk_bf16_f32 v5, v54, v55
	v_cvt_pk_bf16_f32 v4, v52, v53
	v_cvt_pk_bf16_f32 v3, v50, v51
	v_cvt_pk_bf16_f32 v2, v48, v49
	s_waitcnt lgkmcnt(0)
	s_barrier
	ds_read_b128 v[6:9], v18 offset:32768
	ds_read_b128 v[10:13], v18 offset:32832
	s_waitcnt lgkmcnt(1)
	v_mfma_f32_16x16x32_bf16 v[2:5], v[2:5], v[6:9], 0
	v_cvt_pk_bf16_f32 v9, v62, v63
	v_cvt_pk_bf16_f32 v8, v60, v61
	v_cvt_pk_bf16_f32 v7, v58, v59
	v_cvt_pk_bf16_f32 v6, v56, v57
	s_mov_b64 s[4:5], -1
	s_waitcnt lgkmcnt(0)
	v_mfma_f32_16x16x32_bf16 v[2:5], v[6:9], v[10:13], v[2:5]
	v_cvt_pk_bf16_f32 v9, v70, v71
	v_cvt_pk_bf16_f32 v8, v68, v69
	v_cvt_pk_bf16_f32 v7, v66, v67
	v_cvt_pk_bf16_f32 v6, v64, v65
	ds_read_b128 v[10:13], v18 offset:32896
	ds_read_b128 v[14:17], v18 offset:32960
	s_waitcnt lgkmcnt(1)
	v_mfma_f32_16x16x32_bf16 v[2:5], v[6:9], v[10:13], v[2:5]
	v_cvt_pk_bf16_f32 v9, v78, v79
	v_cvt_pk_bf16_f32 v8, v76, v77
	v_cvt_pk_bf16_f32 v7, v74, v75
	v_cvt_pk_bf16_f32 v6, v72, v73
	s_waitcnt lgkmcnt(0)
	s_nop 0
	v_mfma_f32_16x16x32_bf16 v[2:5], v[6:9], v[14:17], v[2:5]
	v_cvt_pk_bf16_f32 v9, v87, v88
	v_cvt_pk_bf16_f32 v8, v85, v86
	v_cvt_pk_bf16_f32 v7, v83, v84
	v_cvt_pk_bf16_f32 v6, v81, v82
	ds_read_b128 v[10:13], v18 offset:33024
	ds_read_b128 v[14:17], v18 offset:33088
	s_waitcnt lgkmcnt(1)
	v_mfma_f32_16x16x32_bf16 v[2:5], v[6:9], v[10:13], v[2:5]
	v_cvt_pk_bf16_f32 v9, v95, v96
	v_cvt_pk_bf16_f32 v8, v93, v94
	v_cvt_pk_bf16_f32 v7, v91, v92
	v_cvt_pk_bf16_f32 v6, v89, v90
	s_waitcnt lgkmcnt(0)
	s_nop 0
	v_mfma_f32_16x16x32_bf16 v[2:5], v[6:9], v[14:17], v[2:5]
	v_cvt_pk_bf16_f32 v9, v103, v104
	v_cvt_pk_bf16_f32 v8, v101, v102
	v_cvt_pk_bf16_f32 v7, v99, v100
	v_cvt_pk_bf16_f32 v6, v97, v98
	ds_read_b128 v[10:13], v18 offset:33152
	ds_read_b128 v[14:17], v18 offset:33216
	s_waitcnt lgkmcnt(1)
	v_mfma_f32_16x16x32_bf16 v[2:5], v[6:9], v[10:13], v[2:5]
	s_waitcnt vmcnt(0)
	v_cvt_pk_bf16_f32 v9, v32, v33
	v_cvt_pk_bf16_f32 v8, v30, v31
	v_cvt_pk_bf16_f32 v7, v28, v29
	v_cvt_pk_bf16_f32 v6, v26, v27
	s_waitcnt lgkmcnt(0)
	s_nop 0
	v_mfma_f32_16x16x32_bf16 v[2:5], v[6:9], v[14:17], v[2:5]
	v_lshl_or_b32 v8, v1, 4, s14
	v_lshlrev_b32_e32 v7, 2, v25
	v_lshl_or_b32 v6, s3, 4, v24
	v_or_b32_e32 v1, v8, v7
	s_cbranch_scc0 .LBB0_10
	s_cmp_lg_u32 s12, 2
	s_cbranch_scc0 .LBB0_7
	s_load_dwordx2 s[4:5], s[0:1], 0xa0
	v_and_b32_e32 v9, 31, v6
	s_lshl_b32 s6, s3, 9
	s_and_b32 s6, s6, 0x1ffffc00
	v_lshlrev_b32_e32 v10, 2, v8
	v_and_or_b32 v9, v0, 32, v9
	v_or3_b32 v9, v10, s6, v9
	v_and_b32_e32 v14, 4, v7
	v_lshlrev_b32_e32 v10, 3, v9
	v_mov_b32_e32 v11, 0
	s_waitcnt lgkmcnt(0)
	v_lshl_add_u64 v[12:13], v[10:11], 1, s[4:5]
	v_lshlrev_b32_e32 v10, 1, v14
	v_mov_b32_e32 v9, 1
	v_lshl_add_u64 v[10:11], v[12:13], 0, v[10:11]
	v_and_b32_sdwa v13, v2, v9 dst_sel:DWORD dst_unused:UNUSED_PAD src0_sel:WORD_1 src1_sel:DWORD
	s_movk_i32 s4, 0x7fff
	v_and_b32_sdwa v12, v4, v9 dst_sel:DWORD dst_unused:UNUSED_PAD src0_sel:WORD_1 src1_sel:DWORD
	v_add3_u32 v14, v2, v13, s4
	v_and_b32_sdwa v13, v5, v9 dst_sel:DWORD dst_unused:UNUSED_PAD src0_sel:WORD_1 src1_sel:DWORD
	v_and_b32_sdwa v9, v3, v9 dst_sel:DWORD dst_unused:UNUSED_PAD src0_sel:WORD_1 src1_sel:DWORD
	v_add3_u32 v13, v5, v13, s4
	v_add3_u32 v9, v3, v9, s4
	v_add3_u32 v12, v4, v12, s4
	v_and_b32_e32 v13, 0xffff0000, v13
	v_and_b32_e32 v9, 0xffff0000, v9
	v_or_b32_sdwa v13, v13, v12 dst_sel:DWORD dst_unused:UNUSED_PAD src0_sel:DWORD src1_sel:WORD_1
	v_or_b32_sdwa v12, v9, v14 dst_sel:DWORD dst_unused:UNUSED_PAD src0_sel:DWORD src1_sel:WORD_1
	global_store_dwordx2 v[10:11], v[12:13], off
	s_mov_b64 s[4:5], 0

.Lpre_roleBC:
	s_load_dwordx16 s[4:19], s[0:1], 0x0
	s_load_dwordx8 s[20:27], s[0:1], 0x40
	s_load_dwordx2 s[28:29], s[0:1], 0x60
	s_load_dwordx2 s[30:31], s[0:1], 0xa0
	s_sub_u32 s3, s2, 0x80
	v_lshrrev_b32_e32 v1, 6, v0
	v_and_b32_e32 v2, 63, v0
	v_and_b32_e32 v3, 31, v0
	v_bfe_u32 v4, v0, 5, 1
	v_lshlrev_b32_e32 v30, 4, v0
	v_lshlrev_b32_e32 v5, 7, v1
	v_lshl_or_b32 v5, v3, 2, v5
	s_waitcnt lgkmcnt(0)
	s_lshl_b32 s44, s3, 12
	s_add_u32 s44, s44, 0xa000
	s_add_u32 s26, s26, s44
	s_addc_u32 s27, s27, 0
	s_cmp_lt_u32 s3, 8
	s_cbranch_scc0 .Lpre_B_only
	v_lshrrev_b32_e32 v6, 3, v0
	v_and_b32_e32 v7, 7, v0
	v_lshlrev_b32_e32 v8, 12, v6
	v_lshl_or_b32 v8, v7, 4, v8
	v_lshlrev_b32_e32 v9, 4, v6
	v_lshrrev_b32_e32 v10, 5, v0
	v_lshlrev_b32_e32 v11, 11, v10
	v_lshl_or_b32 v11, v3, 4, v11
	v_lshlrev_b32_e32 v12, 10, v10
	v_lshl_or_b32 v12, v3, 4, v12
	v_lshlrev_b32_e32 v13, 3, v10
	v_and_b32_e32 v14, 0x7f, v0
	v_lshlrev_b32_e32 v14, 2, v14
	s_lshl_b32 s45, s3, 7
	s_add_u32 s36, s4, s45
	s_addc_u32 s37, s5, 0
	s_lshl_b32 s45, s3, 14
	s_add_u32 s38, s6, s45
	s_addc_u32 s39, s7, 0
	s_lshl_b32 s45, s3, 13
	s_add_u32 s40, s18, s45
	s_addc_u32 s41, s19, 0
	s_add_u32 s32, s6, s45
	s_addc_u32 s33, s7, 0
	s_lshl_b32 s45, s3, 6
	s_add_u32 s42, s16, s45
	s_addc_u32 s43, s17, 0
	v_lshl_add_u32 v15, v4, 12, v5
	global_load_dwordx4 v[32:35], v8, s[36:37]
	global_load_dwordx4 v[36:39], v8, s[36:37] offset:1024
	global_load_dwordx4 v[40:43], v8, s[36:37] offset:2048
	global_load_dwordx4 v[44:47], v8, s[36:37] offset:3072
	global_load_dwordx4 v[48:51], v9, s[12:13]
	global_load_dwordx4 v[52:55], v11, s[38:39]
	global_load_dwordx4 v[56:59], v11, s[38:39] offset:512
	global_load_dwordx4 v[60:63], v11, s[38:39] offset:1024
	global_load_dwordx4 v[64:67], v11, s[38:39] offset:1536
	global_load_dwordx4 v[68:71], v12, s[40:41]
	global_load_dwordx4 v[72:75], v12, s[40:41] offset:512
	global_load_dwordx2 v[76:77], v13, s[42:43]
	global_load_dword v78, v14, s[8:9]
	global_load_dword v79, v14, s[20:21]
	global_load_dword v80, v14, s[24:25]
	global_load_dword v16, v15, s[32:33]
	global_load_dword v17, v15, s[32:33] offset:512
	global_load_dword v18, v15, s[32:33] offset:1024
	global_load_dword v19, v15, s[32:33] offset:1536
	global_load_dword v20, v15, s[32:33] offset:2048
	global_load_dword v21, v15, s[32:33] offset:2560
	global_load_dword v22, v15, s[32:33] offset:3072
	global_load_dword v23, v15, s[32:33] offset:3584
	s_waitcnt vmcnt(18)
	v_mul_f32_e32 v84, v48, v32
	v_mul_f32_e32 v85, v48, v33
	v_mul_f32_e32 v86, v48, v34
	v_mul_f32_e32 v87, v48, v35
	v_fmac_f32_e32 v84, v49, v36
	v_fmac_f32_e32 v85, v49, v37
	v_fmac_f32_e32 v86, v49, v38
	v_fmac_f32_e32 v87, v49, v39
	v_fmac_f32_e32 v84, v50, v40
	v_fmac_f32_e32 v85, v50, v41
	v_fmac_f32_e32 v86, v50, v42
	v_fmac_f32_e32 v87, v50, v43
	v_fmac_f32_e32 v84, v51, v44
	v_fmac_f32_e32 v85, v51, v45
	v_fmac_f32_e32 v86, v51, v46
	v_fmac_f32_e32 v87, v51, v47
	ds_write_b128 v30, v[84:87]
	v_lshlrev_b32_e32 v31, 2, v3
	s_waitcnt lgkmcnt(0)
	s_barrier
	ds_read_b32 v88, v31 offset:0
	ds_read_b32 v89, v31 offset:128
	ds_read_b32 v90, v31 offset:256
	ds_read_b32 v91, v31 offset:384
	ds_read_b32 v92, v31 offset:512
	ds_read_b32 v93, v31 offset:640
	ds_read_b32 v94, v31 offset:768
	ds_read_b32 v95, v31 offset:896
	ds_read_b32 v96, v31 offset:1024
	ds_read_b32 v97, v31 offset:1152
	ds_read_b32 v98, v31 offset:1280
	ds_read_b32 v99, v31 offset:1408
	ds_read_b32 v100, v31 offset:1536
	ds_read_b32 v101, v31 offset:1664
	ds_read_b32 v102, v31 offset:1792
	ds_read_b32 v103, v31 offset:1920
	s_waitcnt lgkmcnt(0)
	ds_read_b32 v104, v31 offset:2048
	ds_read_b32 v105, v31 offset:2176
	ds_read_b32 v106, v31 offset:2304
	ds_read_b32 v107, v31 offset:2432
	ds_read_b32 v108, v31 offset:2560
	ds_read_b32 v109, v31 offset:2688
	ds_read_b32 v110, v31 offset:2816
	ds_read_b32 v111, v31 offset:2944
	ds_read_b32 v112, v31 offset:3072
	ds_read_b32 v113, v31 offset:3200
	ds_read_b32 v114, v31 offset:3328
	ds_read_b32 v115, v31 offset:3456
	ds_read_b32 v116, v31 offset:3584
	ds_read_b32 v117, v31 offset:3712
	ds_read_b32 v118, v31 offset:3840
	ds_read_b32 v119, v31 offset:3968
	s_waitcnt lgkmcnt(0)
	v_add_f32_e32 v88, v88, v104
	v_add_f32_e32 v89, v89, v105
	v_add_f32_e32 v90, v90, v106
	v_add_f32_e32 v91, v91, v107
	v_add_f32_e32 v92, v92, v108
	v_add_f32_e32 v93, v93, v109
	v_add_f32_e32 v94, v94, v110
	v_add_f32_e32 v95, v95, v111
	v_add_f32_e32 v96, v96, v112
	v_add_f32_e32 v97, v97, v113
	v_add_f32_e32 v98, v98, v114
	v_add_f32_e32 v99, v99, v115
	v_add_f32_e32 v100, v100, v116
	v_add_f32_e32 v101, v101, v117
	v_add_f32_e32 v102, v102, v118
	v_add_f32_e32 v103, v103, v119
	v_add_f32_e32 v88, v88, v96
	v_add_f32_e32 v89, v89, v97
	v_add_f32_e32 v90, v90, v98
	v_add_f32_e32 v91, v91, v99
	v_add_f32_e32 v92, v92, v100
	v_add_f32_e32 v93, v93, v101
	v_add_f32_e32 v94, v94, v102
	v_add_f32_e32 v95, v95, v103
	v_add_f32_e32 v88, v88, v92
	v_add_f32_e32 v89, v89, v93
	v_add_f32_e32 v90, v90, v94
	v_add_f32_e32 v91, v91, v95
	v_add_f32_e32 v88, v88, v90
	v_add_f32_e32 v89, v89, v91
	v_add_f32_e32 v88, v88, v89
	ds_write_b32 v31, v88 offset:4096
	v_lshlrev_b32_e32 v81, 4, v10
	v_mov_b32_e32 v82, 0
	s_waitcnt lgkmcnt(0)
	s_barrier
	ds_read_b128 v[120:123], v81 offset:4096
	s_waitcnt vmcnt(14)
	s_waitcnt lgkmcnt(0)
	v_mul_f32_e32 v84, v120, v52
	v_mul_f32_e32 v85, v120, v53
	v_mul_f32_e32 v86, v120, v54
	v_mul_f32_e32 v87, v120, v55
	v_fmac_f32_e32 v84, v121, v56
	v_fmac_f32_e32 v85, v121, v57
	v_fmac_f32_e32 v86, v121, v58
	v_fmac_f32_e32 v87, v121, v59
	v_fmac_f32_e32 v84, v122, v60
	v_fmac_f32_e32 v85, v122, v61
	v_fmac_f32_e32 v86, v122, v62
	v_fmac_f32_e32 v87, v122, v63
	v_fmac_f32_e32 v84, v123, v64
	v_fmac_f32_e32 v85, v123, v65
	v_fmac_f32_e32 v86, v123, v66
	v_fmac_f32_e32 v87, v123, v67
	ds_write_b128 v30, v[84:87] offset:8192
	ds_read_b128 v[96:99], v82 offset:4096
	ds_read_b128 v[100:103], v82 offset:4112
	ds_read_b128 v[104:107], v82 offset:4128
	ds_read_b128 v[108:111], v82 offset:4144
	ds_read_b128 v[112:115], v82 offset:4160
	ds_read_b128 v[116:119], v82 offset:4176
	ds_read_b128 v[120:123], v82 offset:4192
	ds_read_b128 v[124:127], v82 offset:4208
	s_waitcnt vmcnt(11)
	v_mul_f32_e32 v92, v76, v68
	v_mul_f32_e32 v93, v76, v69
	v_mul_f32_e32 v94, v76, v70
	v_mul_f32_e32 v95, v76, v71
	v_fmac_f32_e32 v92, v77, v72
	v_fmac_f32_e32 v93, v77, v73
	v_fmac_f32_e32 v94, v77, v74
	v_fmac_f32_e32 v95, v77, v75
	ds_write_b128 v30, v[92:95] offset:12288
	s_waitcnt lgkmcnt(1)
	v_add_f32_e32 v96, v96, v112
	v_add_f32_e32 v97, v97, v113
	v_add_f32_e32 v98, v98, v114
	v_add_f32_e32 v99, v99, v115
	v_add_f32_e32 v100, v100, v116
	v_add_f32_e32 v101, v101, v117
	v_add_f32_e32 v102, v102, v118
	v_add_f32_e32 v103, v103, v119
	v_add_f32_e32 v104, v104, v120
	v_add_f32_e32 v105, v105, v121
	v_add_f32_e32 v106, v106, v122
	v_add_f32_e32 v107, v107, v123
	v_add_f32_e32 v108, v108, v124
	v_add_f32_e32 v109, v109, v125
	v_add_f32_e32 v110, v110, v126
	v_add_f32_e32 v111, v111, v127
	v_add_f32_e32 v96, v96, v104
	v_add_f32_e32 v97, v97, v105
	v_add_f32_e32 v98, v98, v106
	v_add_f32_e32 v99, v99, v107
	v_add_f32_e32 v100, v100, v108
	v_add_f32_e32 v101, v101, v109
	v_add_f32_e32 v102, v102, v110
	v_add_f32_e32 v103, v103, v111
	v_add_f32_e32 v96, v96, v100
	v_add_f32_e32 v97, v97, v101
	v_add_f32_e32 v98, v98, v102
	v_add_f32_e32 v99, v99, v103
	v_add_f32_e32 v96, v96, v98
	v_add_f32_e32 v97, v97, v99
	v_add_f32_e32 v96, v96, v97
	v_mov_b32_e32 v112, v96
	s_waitcnt vmcnt(0)
	v_cvt_pk_bf16_f32 v24, v16, v17
	v_cvt_pk_bf16_f32 v25, v18, v19
	v_cvt_pk_bf16_f32 v26, v20, v21
	v_cvt_pk_bf16_f32 v27, v22, v23
	global_store_dwordx4 v30, v[24:27], s[26:27]
	s_waitcnt lgkmcnt(0)
	s_barrier
	v_cmp_gt_u32_e32 vcc, 0x80, v0
	s_and_saveexec_b64 s[46:47], vcc
	s_cbranch_execz .Lpre_C_done
	v_lshlrev_b32_e32 v83, 2, v0
	ds_read_b32 v96, v83 offset:8192
	ds_read_b32 v97, v83 offset:8704
	ds_read_b32 v98, v83 offset:9216
	ds_read_b32 v99, v83 offset:9728
	ds_read_b32 v100, v83 offset:10240
	ds_read_b32 v101, v83 offset:10752
	ds_read_b32 v102, v83 offset:11264
	ds_read_b32 v103, v83 offset:11776
	ds_read_b32 v104, v83 offset:12288
	ds_read_b32 v105, v83 offset:12800
	ds_read_b32 v106, v83 offset:13312
	ds_read_b32 v107, v83 offset:13824
	ds_read_b32 v108, v83 offset:14336
	ds_read_b32 v109, v83 offset:14848
	ds_read_b32 v110, v83 offset:15360
	ds_read_b32 v111, v83 offset:15872
	s_waitcnt lgkmcnt(0)
	v_add_f32_e32 v96, v96, v100
	v_add_f32_e32 v97, v97, v101
	v_add_f32_e32 v98, v98, v102
	v_add_f32_e32 v99, v99, v103
	v_add_f32_e32 v96, v96, v98
	v_add_f32_e32 v97, v97, v99
	v_add_f32_e32 v96, v96, v97
	v_add_f32_e32 v104, v104, v108
	v_add_f32_e32 v105, v105, v109
	v_add_f32_e32 v106, v106, v110
	v_add_f32_e32 v107, v107, v111
	v_add_f32_e32 v104, v104, v106
	v_add_f32_e32 v105, v105, v107
	v_add_f32_e32 v104, v104, v105
	s_add_u32 s48, s30, 0x40000
	s_addc_u32 s49, s31, 0
	s_lshl_b32 s45, s3, 10
	s_add_u32 s48, s48, s45
	s_addc_u32 s49, s49, 0
	s_cmp_lg_u32 s3, 0
	s_cbranch_scc1 .Lpre_C_nz
	v_add_f32_e32 v96, v96, v78
	v_add_f32_e32 v104, v104, v79
	global_store_dword v83, v80, s[28:29] offset:1024
.Lpre_C_nz:
	global_store_dword v83, v96, s[48:49]
	global_store_dword v83, v104, s[48:49] offset:512
	s_lshl_b32 s45, s3, 2
	s_add_u32 s50, s28, s45
	s_addc_u32 s51, s29, 0
	v_cmp_eq_u32_e32 vcc, 0, v0
	s_and_saveexec_b64 s[52:53], vcc
	s_cbranch_execz .Lpre_C_done
	global_store_dword v82, v112, s[50:51] offset:1536

.Lpre_B_only:
	s_cmp_lt_u32 s3, 16
	s_cbranch_scc0 .Lpre_B_w12
	s_lshl_b32 s45, s3, 13
	s_add_u32 s32, s6, s45
	s_addc_u32 s33, s7, 0
	v_lshl_add_u32 v15, v4, 12, v5
	global_load_dword v16, v15, s[32:33]
	global_load_dword v17, v15, s[32:33] offset:512
	global_load_dword v18, v15, s[32:33] offset:1024
	global_load_dword v19, v15, s[32:33] offset:1536
	global_load_dword v20, v15, s[32:33] offset:2048
	global_load_dword v21, v15, s[32:33] offset:2560
	global_load_dword v22, v15, s[32:33] offset:3072
	global_load_dword v23, v15, s[32:33] offset:3584
	s_waitcnt vmcnt(0)
	v_cvt_pk_bf16_f32 v24, v16, v17
	v_cvt_pk_bf16_f32 v25, v18, v19
	v_cvt_pk_bf16_f32 v26, v20, v21
	v_cvt_pk_bf16_f32 v27, v22, v23
	global_store_dwordx4 v30, v[24:27], s[26:27]
	s_endpgm
.Lpre_B_w12:
	s_sub_u32 s45, s3, 16
	s_and_b32 s46, s45, 7
	s_cmp_lt_u32 s3, 24
	s_cselect_b32 s32, s18, s22
	s_cselect_b32 s33, s19, s23
	s_lshl_b32 s47, s46, 13
	s_add_u32 s32, s32, s47
	s_addc_u32 s33, s33, 0
	v_lshl_add_u32 v15, v4, 11, v5
	v_add_u32_e32 v6, 0x1000, v15
	global_load_dword v16, v15, s[32:33]
	global_load_dword v17, v15, s[32:33] offset:512
	global_load_dword v18, v15, s[32:33] offset:1024
	global_load_dword v19, v15, s[32:33] offset:1536
	global_load_dword v20, v6, s[32:33]
	global_load_dword v21, v6, s[32:33] offset:512
	global_load_dword v22, v6, s[32:33] offset:1024
	global_load_dword v23, v6, s[32:33] offset:1536
	s_cmp_lt_u32 s3, 24
	s_cbranch_scc0 .Lpre_B_nog
	s_lshl_b32 s47, s46, 6
	s_add_u32 s34, s14, s47
	s_addc_u32 s35, s15, 0
	v_lshlrev_b32_e32 v7, 4, v4
	global_load_dwordx4 v[84:87], v7, s[34:35]
	global_load_dwordx4 v[88:91], v7, s[34:35] offset:32
	s_waitcnt vmcnt(0)
	v_mul_f32_e32 v16, v84, v16
	v_mul_f32_e32 v17, v85, v17
	v_mul_f32_e32 v18, v86, v18
	v_mul_f32_e32 v19, v87, v19
	v_mul_f32_e32 v20, v88, v20
	v_mul_f32_e32 v21, v89, v21
	v_mul_f32_e32 v22, v90, v22
	v_mul_f32_e32 v23, v91, v23
.Lpre_B_nog:
	s_waitcnt vmcnt(0)
	v_cvt_pk_bf16_f32 v24, v16, v17
	v_cvt_pk_bf16_f32 v25, v18, v19
	v_cvt_pk_bf16_f32 v26, v20, v21
	v_cvt_pk_bf16_f32 v27, v22, v23
	global_store_dwordx4 v30, v[24:27], s[26:27]
	s_endpgm
.Lpre_roleD:
	s_load_dwordx8 s[4:11], s[0:1], 0xb0
	s_sub_u32 s3, s2, 0xa1
	s_lshr_b32 s12, s3, 2
	s_and_b32 s13, s3, 3
	v_lshrrev_b32_e32 v1, 6, v0
	v_and_b32_e32 v2, 63, v0
	v_lshrrev_b32_e32 v3, 4, v2
	v_lshl_add_u32 v3, v1, 2, v3
	v_and_b32_e32 v4, 15, v2
	v_lshlrev_b32_e32 v3, 13, v3
	v_lshl_or_b32 v3, v4, 2, v3
	v_add_u32_e32 v5, 0x1000, v3
	v_lshlrev_b32_e32 v6, 4, v0
	s_lshl_b32 s13, s13, 8
	s_waitcnt lgkmcnt(0)
	s_cmp_eq_u32 s12, 1
	s_cselect_b32 s14, s6, s8
	s_cselect_b32 s15, s7, s9
	s_cmp_eq_u32 s12, 0
	s_cselect_b32 s14, s4, s14
	s_cselect_b32 s15, s5, s15
	s_add_u32 s14, s14, s13
	s_addc_u32 s15, s15, 0
	s_add_u32 s16, s14, 0x0
	s_addc_u32 s17, s15, 0
	s_add_u32 s18, s14, 0x20000
	s_addc_u32 s19, s15, 0
	s_add_u32 s20, s14, 0x40
	s_addc_u32 s21, s15, 0
	s_add_u32 s22, s14, 0x20040
	s_addc_u32 s23, s15, 0
	s_add_u32 s24, s14, 0x80
	s_addc_u32 s25, s15, 0
	s_add_u32 s26, s14, 0x20080
	s_addc_u32 s27, s15, 0
	s_add_u32 s28, s14, 0xc0
	s_addc_u32 s29, s15, 0
	s_add_u32 s30, s14, 0x200c0
	s_addc_u32 s31, s15, 0
	global_load_dword v16, v3, s[16:17]
	global_load_dword v17, v3, s[16:17] offset:1024
	global_load_dword v18, v3, s[16:17] offset:2048
	global_load_dword v19, v3, s[16:17] offset:3072
	global_load_dword v20, v5, s[16:17]
	global_load_dword v21, v5, s[16:17] offset:1024
	global_load_dword v22, v5, s[16:17] offset:2048
	global_load_dword v23, v5, s[16:17] offset:3072
	global_load_dword v24, v3, s[18:19]
	global_load_dword v25, v3, s[18:19] offset:1024
	global_load_dword v26, v3, s[18:19] offset:2048
	global_load_dword v27, v3, s[18:19] offset:3072
	global_load_dword v28, v5, s[18:19]
	global_load_dword v29, v5, s[18:19] offset:1024
	global_load_dword v30, v5, s[18:19] offset:2048
	global_load_dword v31, v5, s[18:19] offset:3072
	global_load_dword v32, v3, s[20:21]
	global_load_dword v33, v3, s[20:21] offset:1024
	global_load_dword v34, v3, s[20:21] offset:2048
	global_load_dword v35, v3, s[20:21] offset:3072
	global_load_dword v36, v5, s[20:21]
	global_load_dword v37, v5, s[20:21] offset:1024
	global_load_dword v38, v5, s[20:21] offset:2048
	global_load_dword v39, v5, s[20:21] offset:3072
	global_load_dword v40, v3, s[22:23]
	global_load_dword v41, v3, s[22:23] offset:1024
	global_load_dword v42, v3, s[22:23] offset:2048
	global_load_dword v43, v3, s[22:23] offset:3072
	global_load_dword v44, v5, s[22:23]
	global_load_dword v45, v5, s[22:23] offset:1024
	global_load_dword v46, v5, s[22:23] offset:2048
	global_load_dword v47, v5, s[22:23] offset:3072
	global_load_dword v48, v3, s[24:25]
	global_load_dword v49, v3, s[24:25] offset:1024
	global_load_dword v50, v3, s[24:25] offset:2048
	global_load_dword v51, v3, s[24:25] offset:3072
	global_load_dword v52, v5, s[24:25]
	global_load_dword v53, v5, s[24:25] offset:1024
	global_load_dword v54, v5, s[24:25] offset:2048
	global_load_dword v55, v5, s[24:25] offset:3072
	global_load_dword v56, v3, s[26:27]
	global_load_dword v57, v3, s[26:27] offset:1024
	global_load_dword v58, v3, s[26:27] offset:2048
	global_load_dword v59, v3, s[26:27] offset:3072
	global_load_dword v60, v5, s[26:27]
	global_load_dword v61, v5, s[26:27] offset:1024
	global_load_dword v62, v5, s[26:27] offset:2048
	global_load_dword v63, v5, s[26:27] offset:3072
	global_load_dword v64, v3, s[28:29]
	global_load_dword v65, v3, s[28:29] offset:1024
	global_load_dword v66, v3, s[28:29] offset:2048
	global_load_dword v67, v3, s[28:29] offset:3072
	global_load_dword v68, v5, s[28:29]
	global_load_dword v69, v5, s[28:29] offset:1024
	global_load_dword v70, v5, s[28:29] offset:2048
	global_load_dword v71, v5, s[28:29] offset:3072
	global_load_dword v72, v3, s[30:31]
	global_load_dword v73, v3, s[30:31] offset:1024
	global_load_dword v74, v3, s[30:31] offset:2048
	global_load_dword v75, v3, s[30:31] offset:3072
	global_load_dword v76, v5, s[30:31]
	global_load_dword v77, v5, s[30:31] offset:1024
	global_load_dword v78, v5, s[30:31] offset:2048
	global_load_dword v79, v5, s[30:31] offset:3072
	s_lshl_b32 s3, s3, 15
	s_add_u32 s10, s10, s3
	s_addc_u32 s11, s11, 0
	s_waitcnt vmcnt(56)
	v_cvt_pk_bf16_f32 v80, v16, v17
	v_cvt_pk_bf16_f32 v81, v18, v19
	v_cvt_pk_bf16_f32 v82, v20, v21
	v_cvt_pk_bf16_f32 v83, v22, v23
	global_store_dwordx4 v6, v[80:83], s[10:11]
	s_add_u32 s10, s10, 0x1000
	s_addc_u32 s11, s11, 0
	s_waitcnt vmcnt(49)
	v_cvt_pk_bf16_f32 v84, v24, v25
	v_cvt_pk_bf16_f32 v85, v26, v27
	v_cvt_pk_bf16_f32 v86, v28, v29
	v_cvt_pk_bf16_f32 v87, v30, v31
	global_store_dwordx4 v6, v[84:87], s[10:11]
	s_add_u32 s10, s10, 0x1000
	s_addc_u32 s11, s11, 0
	s_waitcnt vmcnt(42)
	v_cvt_pk_bf16_f32 v88, v32, v33
	v_cvt_pk_bf16_f32 v89, v34, v35
	v_cvt_pk_bf16_f32 v90, v36, v37
	v_cvt_pk_bf16_f32 v91, v38, v39
	global_store_dwordx4 v6, v[88:91], s[10:11]
	s_add_u32 s10, s10, 0x1000
	s_addc_u32 s11, s11, 0
	s_waitcnt vmcnt(35)
	v_cvt_pk_bf16_f32 v92, v40, v41
	v_cvt_pk_bf16_f32 v93, v42, v43
	v_cvt_pk_bf16_f32 v94, v44, v45
	v_cvt_pk_bf16_f32 v95, v46, v47
	global_store_dwordx4 v6, v[92:95], s[10:11]
	s_add_u32 s10, s10, 0x1000
	s_addc_u32 s11, s11, 0
	s_waitcnt vmcnt(28)
	v_cvt_pk_bf16_f32 v96, v48, v49
	v_cvt_pk_bf16_f32 v97, v50, v51
	v_cvt_pk_bf16_f32 v98, v52, v53
	v_cvt_pk_bf16_f32 v99, v54, v55
	global_store_dwordx4 v6, v[96:99], s[10:11]
	s_add_u32 s10, s10, 0x1000
	s_addc_u32 s11, s11, 0
	s_waitcnt vmcnt(21)
	v_cvt_pk_bf16_f32 v100, v56, v57
	v_cvt_pk_bf16_f32 v101, v58, v59
	v_cvt_pk_bf16_f32 v102, v60, v61
	v_cvt_pk_bf16_f32 v103, v62, v63
	global_store_dwordx4 v6, v[100:103], s[10:11]
	s_add_u32 s10, s10, 0x1000
	s_addc_u32 s11, s11, 0
	s_waitcnt vmcnt(14)
	v_cvt_pk_bf16_f32 v104, v64, v65
	v_cvt_pk_bf16_f32 v105, v66, v67
	v_cvt_pk_bf16_f32 v106, v68, v69
	v_cvt_pk_bf16_f32 v107, v70, v71
	global_store_dwordx4 v6, v[104:107], s[10:11]
	s_add_u32 s10, s10, 0x1000
	s_addc_u32 s11, s11, 0
	s_waitcnt vmcnt(7)
	v_cvt_pk_bf16_f32 v108, v72, v73
	v_cvt_pk_bf16_f32 v109, v74, v75
	v_cvt_pk_bf16_f32 v110, v76, v77
	v_cvt_pk_bf16_f32 v111, v78, v79
	global_store_dwordx4 v6, v[108:111], s[10:11]
	s_endpgm

.LBB1_5:
	s_andn2_saveexec_b64 s[8:9], s[8:9]
	s_cbranch_execz .LBB1_9
	v_cmp_eq_u32_e32 vcc, 1, v192
	s_and_saveexec_b64 s[10:11], vcc
	s_cbranch_execz .LBB1_8
	s_load_dwordx2 s[20:21], s[0:1], 0x20
	v_add_u32_e32 v194, 0x40000, v176
	v_add_u32_e32 v195, 0x41000, v176
	s_waitcnt lgkmcnt(0)
	global_load_dwordx4 v[196:199], v194, s[20:21]
	global_load_dwordx4 v[200:203], v194, s[20:21] offset:1024
	global_load_dwordx4 v[204:207], v194, s[20:21] offset:2048
	global_load_dwordx4 v[208:211], v194, s[20:21] offset:3072
	global_load_dwordx4 v[212:215], v195, s[20:21]
	global_load_dwordx4 v[216:219], v195, s[20:21] offset:1024
	global_load_dwordx4 v[220:223], v195, s[20:21] offset:2048
	global_load_dwordx4 v[224:227], v195, s[20:21] offset:3072

.LBB1_12:
	s_or_b64 exec, exec, s[12:13]
	v_lshlrev_b32_e32 v174, 12, v192
	v_mov_b32_e32 v175, 0
	v_mul_u32_u24_e32 v1, 0x1200, v192
	v_mov_b32_e32 v177, v175
	v_lshl_add_u64 v[8:9], s[10:11], 0, v[174:175]
	v_lshlrev_b32_e32 v7, 9, v192
	v_lshl_add_u64 v[180:181], v[8:9], 0, v[176:177]
	s_mov_b64 s[0:1], 0xa000
	v_sub_u32_e32 v186, v1, v7
	v_lshl_add_u64 v[8:9], v[180:181], 0, s[0:1]
	v_readfirstlane_b32 s0, v186
	s_mov_b32 m0, s0
	s_mov_b64 s[0:1], 0xe000
	v_add_u32_e32 v190, 0x5000, v186
	global_load_lds_dwordx4 v[8:9], off
	global_load_lds_dwordx4 v[8:9], off offset:1024
	global_load_lds_dwordx4 v[8:9], off offset:2048
	global_load_lds_dwordx4 v[8:9], off offset:3072
	v_lshl_add_u64 v[8:9], v[180:181], 0, s[0:1]
	v_readfirstlane_b32 s0, v190
	s_mov_b32 m0, s0
	s_mov_b64 s[0:1], 0x12000
	v_add_u32_e32 v187, 0xa000, v186
	s_mov_b32 s3, 0
	global_load_lds_dwordx4 v[8:9], off
	global_load_lds_dwordx4 v[8:9], off offset:1024
	global_load_lds_dwordx4 v[8:9], off offset:2048
	global_load_lds_dwordx4 v[8:9], off offset:3072
	v_lshl_add_u64 v[8:9], v[180:181], 0, s[0:1]
	v_readfirstlane_b32 s0, v187
	s_mov_b32 m0, s0
	s_lshl_b64 s[0:1], s[2:3], 8
	s_lshl_b32 s2, s14, 7
	s_or_b32 s0, s0, s2
	v_lshl_or_b32 v182, v192, 5, s0
	v_mov_b32_e32 v183, s1
	v_lshlrev_b64 v[178:179], 9, v[182:183]
	global_load_lds_dwordx4 v[8:9], off
	global_load_lds_dwordx4 v[8:9], off offset:1024
	global_load_lds_dwordx4 v[8:9], off offset:2048
	global_load_lds_dwordx4 v[8:9], off offset:3072
	v_lshl_add_u64 v[8:9], s[8:9], 0, v[178:179]
	v_and_b32_e32 v174, 0x70, v6
	v_lshl_add_u64 v[6:7], v[8:9], 0, v[174:175]
	v_lshlrev_b32_e32 v8, 6, v0
	v_and_b32_e32 v8, 0xe00, v8
	v_mov_b32_e32 v9, v175
	v_or_b32_e32 v12, 0x1000, v8
	v_mov_b32_e32 v13, v175
	v_or_b32_e32 v16, 0x2000, v8
	v_mov_b32_e32 v17, v175
	v_lshl_add_u64 v[10:11], v[6:7], 0, v[8:9]
	v_lshl_add_u64 v[14:15], v[6:7], 0, v[12:13]
	v_lshl_add_u64 v[18:19], v[6:7], 0, v[16:17]
	v_or_b32_e32 v8, 0x3000, v8
	s_mov_b64 s[0:1], 0x80
	global_load_dwordx4 v[134:137], v[14:15], off nt
	global_load_dwordx4 v[130:133], v[18:19], off nt
	v_lshl_add_u64 v[14:15], v[6:7], 0, v[8:9]
	v_lshl_add_u64 v[18:19], v[6:7], 0, s[0:1]
	global_load_dwordx4 v[142:145], v[10:11], off nt
	global_load_dwordx4 v[114:117], v[10:11], off offset:128 nt
	v_lshl_add_u64 v[20:21], v[18:19], 0, v[12:13]
	global_load_dwordx4 v[138:141], v[14:15], off nt
	global_load_dwordx4 v[118:121], v[20:21], off nt
	v_lshl_add_u64 v[14:15], v[18:19], 0, v[16:17]
	s_mov_b64 s[0:1], 0x100
	v_lshl_add_u64 v[18:19], v[18:19], 0, v[8:9]
	global_load_dwordx4 v[122:125], v[14:15], off nt
	global_load_dwordx4 v[126:129], v[18:19], off nt
	v_lshl_add_u64 v[14:15], v[6:7], 0, s[0:1]
	s_mov_b64 s[0:1], 0x180
	v_lshl_add_u64 v[18:19], v[14:15], 0, v[12:13]
	v_lshl_add_u64 v[6:7], v[6:7], 0, s[0:1]
	v_lshl_add_u64 v[20:21], v[14:15], 0, v[16:17]
	global_load_dwordx4 v[94:97], v[18:19], off nt
	global_load_dwordx4 v[98:101], v[20:21], off nt
	v_lshl_add_u64 v[14:15], v[14:15], 0, v[8:9]
	global_load_dwordx4 v[102:105], v[10:11], off offset:256 nt
	global_load_dwordx4 v[66:69], v[10:11], off offset:384 nt
	v_lshl_add_u64 v[10:11], v[6:7], 0, v[12:13]
	global_load_dwordx4 v[106:109], v[14:15], off nt
	global_load_dwordx4 v[70:73], v[10:11], off nt
	v_lshl_add_u64 v[10:11], v[6:7], 0, v[16:17]
	v_lshl_add_u64 v[6:7], v[6:7], 0, v[8:9]
	global_load_dwordx4 v[74:77], v[10:11], off nt
	global_load_dwordx4 v[78:81], v[6:7], off nt
	v_and_b32_e32 v189, 32, v191
	s_waitcnt vmcnt(16)
	v_readfirstlane_b32 s22, v192
	s_cmp_lg_u32 s22, 1
	s_cbranch_scc1 .Ledge_nosum
	v_pk_add_f32 v[196:197], v[196:197], v[200:201]
	v_pk_add_f32 v[198:199], v[198:199], v[202:203]
	v_pk_add_f32 v[204:205], v[204:205], v[208:209]
	v_pk_add_f32 v[206:207], v[206:207], v[210:211]
	v_pk_add_f32 v[212:213], v[212:213], v[216:217]
	v_pk_add_f32 v[214:215], v[214:215], v[218:219]
	v_pk_add_f32 v[220:221], v[220:221], v[224:225]
	v_pk_add_f32 v[222:223], v[222:223], v[226:227]
	v_pk_add_f32 v[196:197], v[196:197], v[204:205]
	v_pk_add_f32 v[198:199], v[198:199], v[206:207]
	v_pk_add_f32 v[212:213], v[212:213], v[220:221]
	v_pk_add_f32 v[214:215], v[214:215], v[222:223]
	v_pk_add_f32 v[196:197], v[196:197], v[212:213]
	v_pk_add_f32 v[198:199], v[198:199], v[214:215]
	ds_write_b128 v176, v[196:199] offset:58368
.Ledge_nosum:
	s_waitcnt lgkmcnt(0)
	s_barrier
	ds_read_b128 v[6:9], v176
	ds_read_b128 v[10:13], v176 offset:1024
	ds_read_b128 v[14:17], v176 offset:2048
	ds_read_b128 v[194:197], v176 offset:3072
	ds_read_b128 v[198:201], v189 offset:57344
	ds_read_b128 v[18:21], v189 offset:57360
	ds_read_b128 v[202:205], v176 offset:4096
	ds_read_b128 v[206:209], v176 offset:5120
	ds_read_b128 v[210:213], v176 offset:6144
	ds_read_b128 v[214:217], v176 offset:7168
	ds_read_b128 v[218:221], v189 offset:57408
	ds_read_b128 v[222:225], v189 offset:57424
	s_movk_i32 s0, 0x1200
	v_and_b32_e32 v188, 31, v0
	v_lshlrev_b32_e32 v226, 16, v2
	v_and_b32_e32 v227, 0xffff0000, v2
	v_lshlrev_b32_e32 v22, 16, v3
	v_and_b32_e32 v23, 0xffff0000, v3
	v_lshlrev_b32_e32 v2, 16, v4
	v_and_b32_e32 v3, 0xffff0000, v4
	v_lshlrev_b32_e32 v4, 16, v5
	v_and_b32_e32 v5, 0xffff0000, v5
	s_waitcnt lgkmcnt(0)
	v_pk_mul_f32 v[228:229], v[18:19], v[2:3]
	v_pk_mul_f32 v[18:19], v[20:21], v[4:5]
	v_pk_mul_f32 v[24:25], v[200:201], v[22:23]
	v_pk_mul_f32 v[26:27], v[198:199], v[226:227]
	v_cvt_pk_bf16_f32 v4, v228, v229
	v_pk_fma_f32 v[246:247], v[200:201], v[22:23], v[18:19]
	v_pk_fma_f32 v[248:249], v[198:199], v[226:227], v[228:229]
	ds_read_b128 v[198:201], v176 offset:8192
	ds_read_b128 v[226:229], v176 offset:9216
	ds_read_b128 v[230:233], v176 offset:10240
	ds_read_b128 v[234:237], v176 offset:11264
	ds_read_b128 v[238:241], v189 offset:57472
	ds_read_b128 v[242:245], v189 offset:57488
	v_cvt_pk_bf16_f32 v2, v26, v27
	v_cvt_pk_bf16_f32 v5, v18, v19
	v_cvt_pk_bf16_f32 v3, v24, v25
	s_nop 1
	v_mfma_f32_32x32x16_bf16 v[50:65], v[6:9], v[2:5], 0
	v_mfma_f32_32x32x16_bf16 v[34:49], v[10:13], v[2:5], 0
	v_mfma_f32_32x32x16_bf16 v[18:33], v[14:17], v[2:5], 0
	v_mfma_f32_32x32x16_bf16 v[2:17], v[194:197], v[2:5], 0
	v_lshlrev_b32_e32 v194, 16, v172
	v_and_b32_e32 v195, 0xffff0000, v172
	v_lshlrev_b32_e32 v172, 16, v173
	v_and_b32_e32 v173, 0xffff0000, v173
	v_lshlrev_b32_e32 v250, 16, v170
	v_and_b32_e32 v251, 0xffff0000, v170
	v_lshlrev_b32_e32 v170, 16, v171
	v_and_b32_e32 v171, 0xffff0000, v171
	v_pk_mul_f32 v[222:223], v[222:223], v[194:195]
	v_pk_mul_f32 v[172:173], v[224:225], v[172:173]
	v_pk_mul_f32 v[252:253], v[220:221], v[170:171]
	v_pk_mul_f32 v[254:255], v[218:219], v[250:251]
	v_cvt_pk_bf16_f32 v197, v172, v173
	v_pk_fma_f32 v[170:171], v[220:221], v[170:171], v[172:173]
	v_pk_fma_f32 v[172:173], v[218:219], v[250:251], v[222:223]
	v_cvt_pk_bf16_f32 v196, v222, v223
	v_cvt_pk_bf16_f32 v194, v254, v255
	v_cvt_pk_bf16_f32 v195, v252, v253
	v_pk_add_f32 v[172:173], v[248:249], v[172:173]
	v_pk_add_f32 v[170:171], v[246:247], v[170:171]
	v_mfma_f32_32x32x16_bf16 v[50:65], v[202:205], v[194:197], v[50:65]
	v_pk_mov_b32 v[202:203], v[172:173], v[170:171] op_sel:[1,0]
	v_mov_b32_e32 v173, v171
	v_pk_add_f32 v[170:171], v[202:203], v[172:173]
	s_nop 0
	v_pk_add_f32 v[170:171], v[170:171], v[170:171] op_sel:[0,1] op_sel_hi:[1,0]
	v_mfma_f32_32x32x16_bf16 v[34:49], v[206:209], v[194:197], v[34:49]
	v_mfma_f32_32x32x16_bf16 v[18:33], v[210:213], v[194:197], v[18:33]
	ds_read_b128 v[202:205], v176 offset:12288
	ds_read_b128 v[206:209], v176 offset:13312
	ds_read_b128 v[210:213], v176 offset:14336
	ds_read_b128 v[218:221], v176 offset:15360
	ds_read_b128 v[222:225], v189 offset:57536
	ds_read_b128 v[246:249], v189 offset:57552
	v_mfma_f32_32x32x16_bf16 v[2:17], v[214:217], v[194:197], v[2:17]
	v_lshlrev_b32_e32 v172, 16, v166
	v_and_b32_e32 v173, 0xffff0000, v166
	v_lshlrev_b32_e32 v194, 16, v167
	v_and_b32_e32 v195, 0xffff0000, v167
	v_lshlrev_b32_e32 v166, 16, v168
	v_and_b32_e32 v167, 0xffff0000, v168
	v_lshlrev_b32_e32 v168, 16, v169
	v_and_b32_e32 v169, 0xffff0000, v169
	s_waitcnt lgkmcnt(0)
	v_pk_mul_f32 v[196:197], v[240:241], v[194:195]
	v_pk_mul_f32 v[214:215], v[238:239], v[172:173]
	v_pk_mul_f32 v[216:217], v[242:243], v[166:167]
	v_pk_mul_f32 v[242:243], v[244:245], v[168:169]
	v_cvt_pk_bf16_f32 v168, v216, v217
	v_cvt_pk_bf16_f32 v166, v214, v215
	v_cvt_pk_bf16_f32 v169, v242, v243
	v_cvt_pk_bf16_f32 v167, v196, v197
	v_pk_fma_f32 v[194:195], v[240:241], v[194:195], v[242:243]
	v_pk_fma_f32 v[172:173], v[238:239], v[172:173], v[216:217]
	v_mfma_f32_32x32x16_bf16 v[50:65], v[198:201], v[166:169], v[50:65]
	v_mfma_f32_32x32x16_bf16 v[34:49], v[226:229], v[166:169], v[34:49]
	v_mfma_f32_32x32x16_bf16 v[18:33], v[230:233], v[166:169], v[18:33]
	v_mfma_f32_32x32x16_bf16 v[2:17], v[234:237], v[166:169], v[2:17]
	v_lshlrev_b32_e32 v166, 16, v164
	v_and_b32_e32 v167, 0xffff0000, v164
	v_lshlrev_b32_e32 v164, 16, v165
	v_and_b32_e32 v165, 0xffff0000, v165
	v_mul_f32_e64 v216, v248, v164
	v_mul_f32_e64 v217, v249, v165
	v_mul_u32_u24_e32 v164, 0x140, v192
	v_lshlrev_b32_e32 v164, 4, v164
	v_mov_b32_e32 v165, v175
	v_mul_u32_u24_e32 v171, 0x1400, v192
	v_lshl_add_u64 v[164:165], s[10:11], 0, v[164:165]
	v_readfirstlane_b32 s2, v171
	v_lshlrev_b32_e32 v196, 16, v162
	v_and_b32_e32 v197, 0xffff0000, v162
	v_lshlrev_b32_e32 v162, 16, v163
	v_and_b32_e32 v163, 0xffff0000, v163
	v_lshl_add_u64 v[164:165], v[164:165], 0, v[176:177]
	s_movk_i32 s1, 0x1400
	s_mov_b32 m0, s2
	v_mov_b32_e32 v171, 0x1000
	v_pk_mul_f32 v[198:199], v[224:225], v[162:163]
	s_waitcnt lgkmcnt(0)
	s_barrier
	global_load_lds_dwordx4 v[164:165], off
	global_load_lds_dwordx4 v[164:165], off offset:1024
	global_load_lds_dwordx4 v[164:165], off offset:2048
	global_load_lds_dwordx4 v[164:165], off offset:3072
	s_mov_b64 s[2:3], 0x1000
	v_mad_u32_u24 v171, v192, s1, v171
	v_pk_mul_f32 v[214:215], v[246:247], v[166:167]
	v_cvt_pk_bf16_f32 v167, v198, v199
	v_lshl_add_u64 v[198:199], v[164:165], 0, s[2:3]
	v_readfirstlane_b32 s2, v171
	s_mov_b32 m0, s2
	v_pk_mul_f32 v[200:201], v[222:223], v[196:197]
	global_load_lds_dwordx4 v[198:199], off
	v_pk_fma_f32 v[162:163], v[224:225], v[162:163], v[216:217]
	v_pk_fma_f32 v[196:197], v[222:223], v[196:197], v[214:215]
	v_pk_add_f32 v[162:163], v[194:195], v[162:163]
	v_pk_add_f32 v[172:173], v[172:173], v[196:197]
	v_cvt_pk_bf16_f32 v168, v214, v215
	v_cvt_pk_bf16_f32 v166, v200, v201
	v_cvt_pk_bf16_f32 v169, v216, v217
	v_pk_mov_b32 v[194:195], v[172:173], v[162:163] op_sel:[1,0]
	v_mov_b32_e32 v173, v163
	v_mfma_f32_32x32x16_bf16 v[50:65], v[202:205], v[166:169], v[50:65]
	v_add_f32_e64 v162, v194, v172
	v_add_f32_e64 v163, v195, v173
	v_pk_add_f32 v[162:163], v[162:163], v[162:163] op_sel:[0,1] op_sel_hi:[1,0]
	v_mfma_f32_32x32x16_bf16 v[34:49], v[206:209], v[166:169], v[34:49]
	v_mfma_f32_32x32x16_bf16 v[18:33], v[210:213], v[166:169], v[18:33]
	ds_read_b128 v[194:197], v176 offset:20480
	ds_read_b128 v[198:201], v176 offset:21504
	ds_read_b128 v[202:205], v176 offset:22528
	ds_read_b128 v[206:209], v176 offset:23552
	ds_read_b128 v[210:213], v189 offset:57600
	ds_read_b128 v[214:217], v189 offset:57616
	ds_read_b128 v[222:225], v176 offset:24576
	ds_read_b128 v[226:229], v176 offset:25600
	ds_read_b128 v[230:233], v176 offset:26624
	ds_read_b128 v[234:237], v176 offset:27648
	ds_read_b128 v[238:241], v189 offset:57664
	ds_read_b128 v[242:245], v189 offset:57680
	v_mfma_f32_32x32x16_bf16 v[2:17], v[218:221], v[166:169], v[2:17]
	v_lshlrev_b32_e32 v166, 16, v158
	v_and_b32_e32 v167, 0xffff0000, v158
	v_lshlrev_b32_e32 v168, 16, v159
	v_and_b32_e32 v169, 0xffff0000, v159
	v_lshlrev_b32_e32 v158, 16, v160
	v_and_b32_e32 v159, 0xffff0000, v160
	v_lshlrev_b32_e32 v160, 16, v161
	v_and_b32_e32 v161, 0xffff0000, v161
	s_waitcnt lgkmcnt(0)
	v_pk_mul_f32 v[172:173], v[212:213], v[168:169]
	v_pk_mul_f32 v[218:219], v[210:211], v[166:167]
	v_pk_mul_f32 v[214:215], v[214:215], v[158:159]
	v_pk_mul_f32 v[216:217], v[216:217], v[160:161]
	v_cvt_pk_bf16_f32 v160, v214, v215
	v_cvt_pk_bf16_f32 v158, v218, v219
	v_cvt_pk_bf16_f32 v161, v216, v217
	v_cvt_pk_bf16_f32 v159, v172, v173
	v_pk_fma_f32 v[172:173], v[212:213], v[168:169], v[216:217]
	v_pk_fma_f32 v[218:219], v[210:211], v[166:167], v[214:215]
	v_mfma_f32_32x32x16_bf16 v[50:65], v[194:197], v[158:161], v[50:65]
	v_mfma_f32_32x32x16_bf16 v[34:49], v[198:201], v[158:161], v[34:49]
	v_mfma_f32_32x32x16_bf16 v[18:33], v[202:205], v[158:161], v[18:33]
	ds_read_b128 v[166:169], v176 offset:28672
	ds_read_b128 v[194:197], v176 offset:29696
	ds_read_b128 v[198:201], v176 offset:30720
	ds_read_b128 v[202:205], v176 offset:31744
	ds_read_b128 v[210:213], v189 offset:57728
	ds_read_b128 v[214:217], v189 offset:57744
	v_mfma_f32_32x32x16_bf16 v[2:17], v[206:209], v[158:161], v[2:17]
	v_lshlrev_b32_e32 v206, 16, v154
	v_and_b32_e32 v207, 0xffff0000, v154
	v_lshlrev_b32_e32 v154, 16, v155
	v_and_b32_e32 v155, 0xffff0000, v155
	v_lshlrev_b32_e32 v158, 16, v156
	v_and_b32_e32 v159, 0xffff0000, v156
	v_lshlrev_b32_e32 v156, 16, v157
	v_and_b32_e32 v157, 0xffff0000, v157
	v_pk_mul_f32 v[208:209], v[240:241], v[154:155]
	v_pk_mul_f32 v[220:221], v[238:239], v[206:207]
	v_pk_mul_f32 v[242:243], v[242:243], v[158:159]
	v_pk_mul_f32 v[156:157], v[244:245], v[156:157]
	v_cvt_pk_bf16_f32 v160, v242, v243
	v_cvt_pk_bf16_f32 v158, v220, v221
	v_cvt_pk_bf16_f32 v161, v156, v157
	v_cvt_pk_bf16_f32 v159, v208, v209
	v_pk_fma_f32 v[154:155], v[240:241], v[154:155], v[156:157]
	v_pk_fma_f32 v[156:157], v[238:239], v[206:207], v[242:243]
	v_mfma_f32_32x32x16_bf16 v[50:65], v[222:225], v[158:161], v[50:65]
	v_add_f32_e64 v156, v218, v156
	v_add_f32_e64 v157, v219, v157
	v_add_f32_e64 v154, v172, v154
	v_add_f32_e64 v155, v173, v155
	v_pk_mov_b32 v[172:173], v[156:157], v[154:155] op_sel:[1,0]
	v_mov_b32_e32 v157, v155
	v_pk_add_f32 v[154:155], v[172:173], v[156:157]
	v_mfma_f32_32x32x16_bf16 v[34:49], v[226:229], v[158:161], v[34:49]
	v_add_f32_e64 v156, v154, v155
	v_add_f32_e64 v157, v155, v154
	v_mfma_f32_32x32x16_bf16 v[18:33], v[230:233], v[158:161], v[18:33]
	ds_read_b128 v[206:209], v176 offset:32768
	ds_read_b128 v[218:221], v176 offset:33792
	ds_read_b128 v[222:225], v176 offset:34816
	ds_read_b128 v[226:229], v176 offset:35840
	ds_read_b128 v[230:233], v189 offset:57792
	ds_read_b128 v[238:241], v189 offset:57808
	v_mfma_f32_32x32x16_bf16 v[2:17], v[234:237], v[158:161], v[2:17]
	v_lshlrev_b32_e32 v154, 16, v150
	v_and_b32_e32 v155, 0xffff0000, v150
	v_lshlrev_b32_e32 v158, 16, v151
	v_and_b32_e32 v159, 0xffff0000, v151
	v_lshlrev_b32_e32 v150, 16, v152
	v_and_b32_e32 v151, 0xffff0000, v152
	v_lshlrev_b32_e32 v152, 16, v153
	v_and_b32_e32 v153, 0xffff0000, v153
	s_waitcnt lgkmcnt(0)
	v_pk_mul_f32 v[160:161], v[212:213], v[158:159]
	v_pk_mul_f32 v[172:173], v[210:211], v[154:155]
	v_pk_mul_f32 v[214:215], v[214:215], v[150:151]
	v_pk_mul_f32 v[216:217], v[216:217], v[152:153]
	v_cvt_pk_bf16_f32 v152, v214, v215
	v_cvt_pk_bf16_f32 v150, v172, v173
	v_cvt_pk_bf16_f32 v153, v216, v217
	v_cvt_pk_bf16_f32 v151, v160, v161
	v_pk_fma_f32 v[158:159], v[212:213], v[158:159], v[216:217]
	v_pk_fma_f32 v[154:155], v[210:211], v[154:155], v[214:215]
	v_mfma_f32_32x32x16_bf16 v[50:65], v[166:169], v[150:153], v[50:65]
	v_mfma_f32_32x32x16_bf16 v[34:49], v[194:197], v[150:153], v[34:49]
	v_mfma_f32_32x32x16_bf16 v[18:33], v[198:201], v[150:153], v[18:33]
	v_mfma_f32_32x32x16_bf16 v[2:17], v[202:205], v[150:153], v[2:17]
	v_lshlrev_b32_e32 v152, 16, v146
	v_and_b32_e32 v153, 0xffff0000, v146
	v_lshlrev_b32_e32 v146, 16, v147
	v_and_b32_e32 v147, 0xffff0000, v147
	v_mov_b32_e32 v157, 0x5000
	v_lshlrev_b32_e32 v150, 16, v148
	v_and_b32_e32 v151, 0xffff0000, v148
	v_lshlrev_b32_e32 v148, 16, v149
	v_and_b32_e32 v149, 0xffff0000, v149
	v_pk_mul_f32 v[160:161], v[232:233], v[146:147]
	s_mov_b64 s[2:3], 0x5000
	v_mad_u32_u24 v157, v192, s1, v157
	v_pk_mul_f32 v[172:173], v[240:241], v[148:149]
	v_cvt_pk_bf16_f32 v149, v160, v161
	v_lshl_add_u64 v[160:161], v[164:165], 0, s[2:3]
	v_readfirstlane_b32 s2, v157
	s_mov_b32 m0, s2
	v_mov_b32_e32 v157, 0x6000
	s_waitcnt lgkmcnt(0)
	s_barrier
	global_load_lds_dwordx4 v[160:161], off
	global_load_lds_dwordx4 v[160:161], off offset:1024
	global_load_lds_dwordx4 v[160:161], off offset:2048
	global_load_lds_dwordx4 v[160:161], off offset:3072
	v_mad_u32_u24 v157, v192, s1, v157
	s_mov_b64 s[2:3], 0x6000
	v_readfirstlane_b32 s1, v157
	v_lshl_add_u64 v[160:161], v[164:165], 0, s[2:3]
	s_mov_b32 m0, s1
	v_pk_mul_f32 v[168:169], v[238:239], v[150:151]
	global_load_lds_dwordx4 v[160:161], off
	v_pk_mul_f32 v[166:167], v[230:231], v[152:153]
	v_pk_fma_f32 v[146:147], v[232:233], v[146:147], v[172:173]
	v_pk_fma_f32 v[152:153], v[230:231], v[152:153], v[168:169]
	v_pk_add_f32 v[146:147], v[158:159], v[146:147]
	v_pk_add_f32 v[152:153], v[154:155], v[152:153]
	v_cvt_pk_bf16_f32 v150, v168, v169
	v_cvt_pk_bf16_f32 v148, v166, v167
	v_cvt_pk_bf16_f32 v151, v172, v173
	v_pk_mov_b32 v[154:155], v[152:153], v[146:147] op_sel:[1,0]
	v_mov_b32_e32 v153, v147
	v_mfma_f32_32x32x16_bf16 v[50:65], v[206:209], v[148:151], v[50:65]
	v_add_f32_e64 v146, v154, v152
	v_add_f32_e64 v147, v155, v153
	v_pk_add_f32 v[146:147], v[146:147], v[146:147] op_sel:[0,1] op_sel_hi:[1,0]
	v_mfma_f32_32x32x16_bf16 v[34:49], v[218:221], v[148:151], v[34:49]
	v_mfma_f32_32x32x16_bf16 v[18:33], v[222:225], v[148:151], v[18:33]
	ds_read_b128 v[152:155], v176 offset:40960
	ds_read_b128 v[158:161], v176 offset:41984
	ds_read_b128 v[164:167], v176 offset:43008
	ds_read_b128 v[194:197], v176 offset:44032
	ds_read_b128 v[198:201], v189 offset:57856
	ds_read_b128 v[202:205], v189 offset:57872
	ds_read_b128 v[206:209], v176 offset:45056
	ds_read_b128 v[210:213], v176 offset:46080
	ds_read_b128 v[214:217], v176 offset:47104
	ds_read_b128 v[218:221], v176 offset:48128
	ds_read_b128 v[222:225], v189 offset:57920
	ds_read_b128 v[230:233], v189 offset:57936
	v_mfma_f32_32x32x16_bf16 v[2:17], v[226:229], v[148:151], v[2:17]
	v_lshlrev_b32_e32 v148, 16, v110
	v_and_b32_e32 v149, 0xffff0000, v110
	v_lshlrev_b32_e32 v150, 16, v111
	v_and_b32_e32 v151, 0xffff0000, v111
	v_lshlrev_b32_e32 v110, 16, v112
	v_and_b32_e32 v111, 0xffff0000, v112
	v_lshlrev_b32_e32 v112, 16, v113
	v_and_b32_e32 v113, 0xffff0000, v113
	s_waitcnt lgkmcnt(0)
	v_pk_mul_f32 v[168:169], v[200:201], v[150:151]
	v_pk_mul_f32 v[172:173], v[198:199], v[148:149]
	v_pk_mul_f32 v[202:203], v[202:203], v[110:111]
	v_pk_mul_f32 v[204:205], v[204:205], v[112:113]
	v_cvt_pk_bf16_f32 v112, v202, v203
	v_cvt_pk_bf16_f32 v110, v172, v173
	v_cvt_pk_bf16_f32 v113, v204, v205
	v_cvt_pk_bf16_f32 v111, v168, v169
	v_pk_fma_f32 v[148:149], v[198:199], v[148:149], v[202:203]
	s_nop 0
	v_mfma_f32_32x32x16_bf16 v[50:65], v[152:155], v[110:113], v[50:65]
	v_fma_f32 v154, v200, v150, v204
	v_fma_f32 v155, v201, v151, v205
	v_mfma_f32_32x32x16_bf16 v[34:49], v[158:161], v[110:113], v[34:49]
	v_mfma_f32_32x32x16_bf16 v[18:33], v[164:167], v[110:113], v[18:33]
	ds_read_b128 v[150:153], v176 offset:49152
	ds_read_b128 v[158:161], v176 offset:50176
	ds_read_b128 v[164:167], v176 offset:51200
	ds_read_b128 v[198:201], v176 offset:52224
	ds_read_b128 v[202:205], v189 offset:57984
	ds_read_b128 v[226:229], v189 offset:58000
	v_mfma_f32_32x32x16_bf16 v[2:17], v[194:197], v[110:113], v[2:17]
	v_lshlrev_b32_e32 v110, 16, v90
	v_and_b32_e32 v111, 0xffff0000, v90
	v_lshlrev_b32_e32 v112, 16, v91
	v_and_b32_e32 v113, 0xffff0000, v91
	v_lshlrev_b32_e32 v90, 16, v92
	v_and_b32_e32 v91, 0xffff0000, v92
	v_lshlrev_b32_e32 v92, 16, v93
	v_and_b32_e32 v93, 0xffff0000, v93
	v_pk_mul_f32 v[194:195], v[230:231], v[90:91]
	v_pk_mul_f32 v[196:197], v[232:233], v[92:93]
	v_pk_mul_f32 v[168:169], v[224:225], v[112:113]
	v_pk_mul_f32 v[172:173], v[222:223], v[110:111]
	v_pk_fma_f32 v[112:113], v[224:225], v[112:113], v[196:197]
	v_pk_fma_f32 v[110:111], v[222:223], v[110:111], v[194:195]
	v_pk_add_f32 v[112:113], v[154:155], v[112:113]
	v_pk_add_f32 v[110:111], v[148:149], v[110:111]
	v_cvt_pk_bf16_f32 v92, v194, v195
	v_pk_mov_b32 v[148:149], v[110:111], v[112:113] op_sel:[1,0]
	v_mov_b32_e32 v111, v113
	v_cvt_pk_bf16_f32 v90, v172, v173
	v_cvt_pk_bf16_f32 v93, v196, v197
	v_cvt_pk_bf16_f32 v91, v168, v169
	v_pk_add_f32 v[110:111], v[148:149], v[110:111]
	s_nop 0
	v_mfma_f32_32x32x16_bf16 v[50:65], v[206:209], v[90:93], v[50:65]
	v_add_f32_e64 v148, v110, v111
	v_add_f32_e64 v149, v111, v110
	v_mfma_f32_32x32x16_bf16 v[34:49], v[210:213], v[90:93], v[34:49]
	v_mfma_f32_32x32x16_bf16 v[18:33], v[214:217], v[90:93], v[18:33]
	ds_read_b128 v[110:113], v176 offset:53248
	ds_read_b128 v[194:197], v176 offset:54272
	ds_read_b128 v[206:209], v176 offset:55296
	ds_read_b128 v[210:213], v176 offset:56320
	ds_read_b128 v[214:217], v189 offset:58048
	ds_read_b128 v[222:225], v189 offset:58064
	v_mfma_f32_32x32x16_bf16 v[2:17], v[218:221], v[90:93], v[2:17]
	v_lshlrev_b32_e32 v90, 16, v86
	v_and_b32_e32 v91, 0xffff0000, v86
	v_lshlrev_b32_e32 v92, 16, v87
	v_and_b32_e32 v93, 0xffff0000, v87
	v_lshlrev_b32_e32 v86, 16, v88
	v_and_b32_e32 v87, 0xffff0000, v88
	v_lshlrev_b32_e32 v88, 16, v89
	v_and_b32_e32 v89, 0xffff0000, v89
	s_waitcnt lgkmcnt(0)
	v_pk_mul_f32 v[154:155], v[204:205], v[92:93]
	v_pk_mul_f32 v[168:169], v[202:203], v[90:91]
	v_pk_mul_f32 v[172:173], v[226:227], v[86:87]
	v_pk_mul_f32 v[218:219], v[228:229], v[88:89]
	v_cvt_pk_bf16_f32 v88, v172, v173
	v_cvt_pk_bf16_f32 v86, v168, v169
	v_cvt_pk_bf16_f32 v89, v218, v219
	v_cvt_pk_bf16_f32 v87, v154, v155
	v_pk_fma_f32 v[92:93], v[204:205], v[92:93], v[218:219]
	v_pk_fma_f32 v[90:91], v[202:203], v[90:91], v[172:173]
	v_mfma_f32_32x32x16_bf16 v[50:65], v[150:153], v[86:89], v[50:65]
	v_mfma_f32_32x32x16_bf16 v[34:49], v[158:161], v[86:89], v[34:49]
	v_mfma_f32_32x32x16_bf16 v[18:33], v[164:167], v[86:89], v[18:33]
	v_mfma_f32_32x32x16_bf16 v[2:17], v[198:201], v[86:89], v[2:17]
	v_lshlrev_b32_e32 v86, 16, v82
	v_and_b32_e32 v87, 0xffff0000, v82
	v_lshlrev_b32_e32 v88, 16, v83
	v_and_b32_e32 v89, 0xffff0000, v83
	v_lshlrev_b32_e32 v82, 16, v84
	v_and_b32_e32 v83, 0xffff0000, v84
	v_lshlrev_b32_e32 v84, 16, v85
	v_and_b32_e32 v85, 0xffff0000, v85
	v_pk_mul_f32 v[150:151], v[216:217], v[88:89]
	v_pk_mul_f32 v[152:153], v[214:215], v[86:87]
	v_pk_mul_f32 v[154:155], v[222:223], v[82:83]
	v_pk_mul_f32 v[158:159], v[224:225], v[84:85]
	v_cvt_pk_bf16_f32 v84, v154, v155
	v_cvt_pk_bf16_f32 v82, v152, v153
	v_cvt_pk_bf16_f32 v85, v158, v159
	v_cvt_pk_bf16_f32 v83, v150, v151
	v_pk_fma_f32 v[88:89], v[216:217], v[88:89], v[158:159]
	v_pk_fma_f32 v[86:87], v[214:215], v[86:87], v[154:155]
	s_mov_b64 s[2:3], 0x3000
	v_mfma_f32_32x32x16_bf16 v[50:65], v[110:113], v[82:85], v[50:65]
	v_add_f32_e64 v86, v90, v86
	v_add_f32_e64 v87, v91, v87
	v_add_f32_e64 v88, v92, v88
	v_add_f32_e64 v89, v93, v89
	s_waitcnt vmcnt(5)
	v_pk_mov_b32 v[90:91], v[86:87], v[88:89] op_sel:[1,0]
	v_mov_b32_e32 v87, v89
	v_pk_add_f32 v[86:87], v[90:91], v[86:87]
	v_lshrrev_b32_e32 v161, 3, v191
	v_mfma_f32_32x32x16_bf16 v[34:49], v[194:197], v[82:85], v[34:49]
	s_movk_i32 s1, 0x90
	v_or_b32_e32 v152, v1, v174
	v_add_f32_e64 v150, v86, v87
	v_add_f32_e64 v151, v87, v86
	v_mad_u32_u24 v155, v161, s1, v152
	v_mul_u32_u24_e32 v147, 0x90, v188
	v_mad_u32_u24 v149, v192, s0, v147
	v_and_b32_e32 v147, 32, v0
	v_mfma_f32_32x32x16_bf16 v[18:33], v[206:209], v[82:85], v[18:33]
	v_add_u32_e32 v151, v149, v147
	v_lshrrev_b32_e32 v147, 1, v191
	v_and_b32_e32 v154, 16, v147
	v_add_u32_e32 v160, v149, v154
	v_sub_u32_e32 v147, v189, v154
	s_mov_b64 s[8:9], 0x16000
	s_brev_b32 s0, 60
	v_mfma_f32_32x32x16_bf16 v[2:17], v[210:213], v[82:85], v[2:17]
	v_lshl_add_u64 v[82:83], v[184:185], 0, s[2:3]
	s_mov_b64 s[2:3], 0x3400
	global_load_dwordx4 v[110:113], v[82:83], off
	v_lshl_add_u64 v[82:83], v[184:185], 0, s[2:3]
	s_mov_b64 s[2:3], 0x3800
	global_load_dwordx4 v[90:93], v[82:83], off
	v_lshl_add_u64 v[82:83], v[184:185], 0, s[2:3]
	s_mov_b64 s[2:3], 0x3c00
	global_load_dwordx4 v[86:89], v[82:83], off
	v_lshl_add_u64 v[82:83], v[184:185], 0, s[2:3]
	global_load_dwordx4 v[82:85], v[82:83], off
	s_waitcnt lgkmcnt(0)
	s_barrier
	ds_write_b128 v155, v[142:145] offset:61440
	v_mov_b32_e32 v142, 0x480
	v_mad_u32_u24 v165, v161, s1, v142
	v_add_u32_e32 v157, v152, v165
	ds_write_b128 v157, v[134:137] offset:61440
	v_mov_b32_e32 v134, 0x900
	v_mad_u32_u24 v164, v161, s1, v134
	v_add_u32_e32 v171, v152, v164
	ds_write_b128 v171, v[130:133] offset:61440
	v_mov_b32_e32 v130, 0xd80
	v_mad_u32_u24 v163, v161, s1, v130
	v_add_u32_e32 v174, v152, v163
	ds_write_b128 v174, v[138:141] offset:61440
	ds_read_b128 v[142:145], v151 offset:61440
	ds_read_b128 v[138:141], v151 offset:61456
	ds_read_b128 v[134:137], v151 offset:61504
	ds_read_b128 v[130:133], v151 offset:61520
	ds_read_b128 v[166:169], v160 offset:61440
	ds_read_b128 v[192:195], v160 offset:61472
	ds_read_b128 v[196:199], v147 offset:58368
	ds_read_b128 v[200:203], v147 offset:58400
	ds_read_b128 v[204:207], v160 offset:61504
	ds_read_b128 v[208:211], v160 offset:61536
	ds_read_b128 v[212:215], v147 offset:58432
	ds_read_b128 v[216:219], v147 offset:58464
	s_waitcnt lgkmcnt(0)
	v_pk_add_f32 v[152:153], v[168:169], v[198:199]
	v_pk_add_f32 v[158:159], v[166:167], v[196:197]
	v_pk_add_f32 v[166:167], v[194:195], v[202:203]
	v_pk_add_f32 v[168:169], v[192:193], v[200:201]
	v_pk_add_f32 v[192:193], v[210:211], v[218:219]
	v_pk_add_f32 v[194:195], v[208:209], v[216:217]
	v_pk_add_f32 v[172:173], v[206:207], v[214:215]
	v_pk_add_f32 v[184:185], v[204:205], v[212:213]
	v_pk_add_f32 v[62:63], v[194:195], v[62:63]
	v_pk_add_f32 v[54:55], v[168:169], v[54:55]
	v_pk_add_f32 v[64:65], v[192:193], v[64:65]
	v_pk_add_f32 v[56:57], v[166:167], v[56:57]
	ds_write_b128 v155, v[114:117] offset:61440
	ds_write_b128 v157, v[118:121] offset:61440
	ds_write_b128 v171, v[122:125] offset:61440
	ds_write_b128 v174, v[126:129] offset:61440
	ds_read_b128 v[126:129], v151 offset:61440
	ds_read_b128 v[122:125], v151 offset:61456
	ds_read_b128 v[118:121], v151 offset:61504
	ds_read_b128 v[114:117], v151 offset:61520
	ds_read_b128 v[166:169], v160 offset:61440
	ds_read_b128 v[192:195], v160 offset:61472
	ds_read_b128 v[196:199], v147 offset:58496
	ds_read_b128 v[200:203], v147 offset:58528
	ds_read_b128 v[204:207], v160 offset:61504
	ds_read_b128 v[208:211], v160 offset:61536
	ds_read_b128 v[212:215], v147 offset:58560
	ds_read_b128 v[216:219], v147 offset:58592
	v_pk_add_f32 v[52:53], v[152:153], v[52:53]
	v_pk_add_f32 v[50:51], v[158:159], v[50:51]
	s_waitcnt lgkmcnt(0)
	v_pk_add_f32 v[152:153], v[168:169], v[198:199]
	v_pk_add_f32 v[158:159], v[166:167], v[196:197]
	v_pk_add_f32 v[166:167], v[194:195], v[202:203]
	v_pk_add_f32 v[168:169], v[192:193], v[200:201]
	v_pk_add_f32 v[192:193], v[210:211], v[218:219]
	v_pk_add_f32 v[194:195], v[208:209], v[216:217]
	v_pk_add_f32 v[58:59], v[184:185], v[58:59]
	v_pk_add_f32 v[60:61], v[172:173], v[60:61]
	v_pk_add_f32 v[172:173], v[206:207], v[214:215]
	v_pk_add_f32 v[184:185], v[204:205], v[212:213]
	v_pk_add_f32 v[46:47], v[194:195], v[46:47]
	v_pk_add_f32 v[38:39], v[168:169], v[38:39]
	v_pk_add_f32 v[48:49], v[192:193], v[48:49]
	v_pk_add_f32 v[40:41], v[166:167], v[40:41]
	ds_write_b128 v155, v[102:105] offset:61440
	ds_write_b128 v157, v[94:97] offset:61440
	ds_write_b128 v171, v[98:101] offset:61440
	ds_write_b128 v174, v[106:109] offset:61440
	ds_read_b128 v[106:109], v151 offset:61440
	ds_read_b128 v[102:105], v151 offset:61456
	ds_read_b128 v[98:101], v151 offset:61504
	ds_read_b128 v[94:97], v151 offset:61520
	ds_read_b128 v[166:169], v160 offset:61440
	ds_read_b128 v[192:195], v160 offset:61472
	ds_read_b128 v[196:199], v147 offset:58624
	ds_read_b128 v[200:203], v147 offset:58656
	ds_read_b128 v[204:207], v160 offset:61504
	ds_read_b128 v[208:211], v160 offset:61536
	ds_read_b128 v[212:215], v147 offset:58688
	ds_read_b128 v[216:219], v147 offset:58720
	v_pk_add_f32 v[36:37], v[152:153], v[36:37]
	v_pk_add_f32 v[34:35], v[158:159], v[34:35]
	s_waitcnt lgkmcnt(0)
	v_pk_add_f32 v[152:153], v[168:169], v[198:199]
	v_pk_add_f32 v[158:159], v[166:167], v[196:197]
	v_pk_add_f32 v[166:167], v[194:195], v[202:203]
	v_pk_add_f32 v[168:169], v[192:193], v[200:201]
	v_pk_add_f32 v[192:193], v[210:211], v[218:219]
	v_pk_add_f32 v[194:195], v[208:209], v[216:217]
	v_add_f32_e32 v149, 0, v142
	v_pk_add_f32 v[42:43], v[184:185], v[42:43]
	v_pk_add_f32 v[44:45], v[172:173], v[44:45]
	v_pk_add_f32 v[172:173], v[206:207], v[214:215]
	v_pk_add_f32 v[184:185], v[204:205], v[212:213]
	v_pk_add_f32 v[30:31], v[194:195], v[30:31]
	v_pk_add_f32 v[22:23], v[168:169], v[22:23]
	v_pk_add_f32 v[32:33], v[192:193], v[32:33]
	v_pk_add_f32 v[24:25], v[166:167], v[24:25]
	ds_write_b128 v155, v[66:69] offset:61440
	ds_write_b128 v157, v[70:73] offset:61440
	ds_write_b128 v171, v[74:77] offset:61440
	ds_write_b128 v174, v[78:81] offset:61440
	ds_read_b128 v[78:81], v151 offset:61440
	ds_read_b128 v[74:77], v151 offset:61456
	ds_read_b128 v[70:73], v151 offset:61504
	ds_read_b128 v[66:69], v151 offset:61520
	ds_read_b128 v[166:169], v160 offset:61440
	ds_read_b128 v[192:195], v160 offset:61472
	ds_read_b128 v[196:199], v147 offset:58752
	ds_read_b128 v[200:203], v147 offset:58784
	ds_read_b128 v[204:207], v160 offset:61504
	ds_read_b128 v[208:211], v160 offset:61536
	ds_read_b128 v[212:215], v147 offset:58816
	ds_read_b128 v[216:219], v147 offset:58848
	v_add_f32_e32 v149, v149, v143
	v_mul_f32_e32 v151, v143, v143
	v_fmac_f32_e32 v151, v142, v142
	v_add_f32_e32 v149, v149, v144
	v_fmac_f32_e32 v151, v144, v144
	v_add_f32_e32 v149, v149, v145
	v_fmac_f32_e32 v151, v145, v145
	v_add_f32_e32 v149, v149, v138
	v_fmac_f32_e32 v151, v138, v138
	v_add_f32_e32 v149, v149, v139
	v_fmac_f32_e32 v151, v139, v139
	v_add_f32_e32 v149, v149, v140
	v_fmac_f32_e32 v151, v140, v140
	v_add_f32_e32 v149, v149, v141
	v_fmac_f32_e32 v151, v141, v141
	v_add_f32_e32 v149, v149, v134
	v_fmac_f32_e32 v151, v134, v134
	v_add_f32_e32 v149, v149, v135
	v_fmac_f32_e32 v151, v135, v135
	v_add_f32_e32 v149, v149, v136
	v_fmac_f32_e32 v151, v136, v136
	v_add_f32_e32 v149, v149, v137
	v_fmac_f32_e32 v151, v137, v137
	v_add_f32_e32 v149, v149, v130
	v_fmac_f32_e32 v151, v130, v130
	v_add_f32_e32 v149, v149, v131
	v_fmac_f32_e32 v151, v131, v131
	v_add_f32_e32 v149, v149, v132
	v_fmac_f32_e32 v151, v132, v132
	v_add_f32_e32 v149, v149, v133
	v_fmac_f32_e32 v151, v133, v133
	v_add_f32_e32 v149, v149, v126
	v_fmac_f32_e32 v151, v126, v126
	v_add_f32_e32 v149, v149, v127
	v_fmac_f32_e32 v151, v127, v127
	v_add_f32_e32 v149, v149, v128
	v_fmac_f32_e32 v151, v128, v128
	v_add_f32_e32 v149, v149, v129
	v_fmac_f32_e32 v151, v129, v129
	v_add_f32_e32 v149, v149, v122
	v_fmac_f32_e32 v151, v122, v122
	v_add_f32_e32 v149, v149, v123
	v_fmac_f32_e32 v151, v123, v123
	v_add_f32_e32 v149, v149, v124
	v_fmac_f32_e32 v151, v124, v124
	v_add_f32_e32 v149, v149, v125
	v_fmac_f32_e32 v151, v125, v125
	v_add_f32_e32 v149, v149, v118
	v_fmac_f32_e32 v151, v118, v118
	v_add_f32_e32 v149, v149, v119
	v_fmac_f32_e32 v151, v119, v119
	v_add_f32_e32 v149, v149, v120
	v_fmac_f32_e32 v151, v120, v120
	v_add_f32_e32 v149, v149, v121
	v_fmac_f32_e32 v151, v121, v121
	v_add_f32_e32 v149, v149, v114
	v_fmac_f32_e32 v151, v114, v114
	v_add_f32_e32 v149, v149, v115
	v_fmac_f32_e32 v151, v115, v115
	v_add_f32_e32 v149, v149, v116
	v_fmac_f32_e32 v151, v116, v116
	v_add_f32_e32 v149, v149, v117
	v_fmac_f32_e32 v151, v117, v117
	v_add_f32_e32 v149, v149, v106
	v_fmac_f32_e32 v151, v106, v106
	v_add_f32_e32 v149, v149, v107
	v_fmac_f32_e32 v151, v107, v107
	v_add_f32_e32 v149, v149, v108
	v_fmac_f32_e32 v151, v108, v108
	v_add_f32_e32 v149, v149, v109
	v_fmac_f32_e32 v151, v109, v109
	v_add_f32_e32 v149, v149, v102
	v_fmac_f32_e32 v151, v102, v102
	v_add_f32_e32 v149, v149, v103
	v_fmac_f32_e32 v151, v103, v103
	v_add_f32_e32 v149, v149, v104
	v_fmac_f32_e32 v151, v104, v104
	v_add_f32_e32 v149, v149, v105
	v_fmac_f32_e32 v151, v105, v105
	v_add_f32_e32 v149, v149, v98
	v_fmac_f32_e32 v151, v98, v98
	v_add_f32_e32 v149, v149, v99
	v_fmac_f32_e32 v151, v99, v99
	v_add_f32_e32 v149, v149, v100
	v_fmac_f32_e32 v151, v100, v100
	v_add_f32_e32 v149, v149, v101
	v_fmac_f32_e32 v151, v101, v101
	v_add_f32_e32 v149, v149, v94
	v_fmac_f32_e32 v151, v94, v94
	v_add_f32_e32 v149, v149, v95
	v_fmac_f32_e32 v151, v95, v95
	v_add_f32_e32 v149, v149, v96
	v_fmac_f32_e32 v151, v96, v96
	v_add_f32_e32 v149, v149, v97
	v_fmac_f32_e32 v151, v97, v97
	s_waitcnt lgkmcnt(0)
	v_add_f32_e32 v149, v149, v78
	v_fmac_f32_e32 v151, v78, v78
	v_add_f32_e32 v149, v149, v79
	v_fmac_f32_e32 v151, v79, v79
	v_add_f32_e32 v149, v149, v80
	v_fmac_f32_e32 v151, v80, v80
	v_add_f32_e32 v149, v149, v81
	v_fmac_f32_e32 v151, v81, v81
	v_add_f32_e32 v149, v149, v74
	v_fmac_f32_e32 v151, v74, v74
	v_add_f32_e32 v149, v149, v75
	v_fmac_f32_e32 v151, v75, v75
	v_add_f32_e32 v149, v149, v76
	v_pk_add_f32 v[20:21], v[152:153], v[20:21]
	v_pk_add_f32 v[152:153], v[168:169], v[198:199]
	v_pk_add_f32 v[168:169], v[192:193], v[200:201]
	v_fmac_f32_e32 v151, v76, v76
	v_add_f32_e32 v149, v149, v77
	v_pk_add_f32 v[6:7], v[168:169], v[6:7]
	v_fmac_f32_e32 v151, v77, v77
	v_add_f32_e32 v149, v149, v70
	v_pk_mul_f32 v[168:169], v[70:71], v[70:71]
	v_pk_add_f32 v[18:19], v[158:159], v[18:19]
	v_pk_add_f32 v[158:159], v[166:167], v[196:197]
	v_pk_add_f32 v[166:167], v[194:195], v[202:203]
	v_add_f32_e32 v149, v149, v71
	v_add_f32_e32 v151, v151, v168
	v_pk_add_f32 v[8:9], v[166:167], v[8:9]
	v_pk_mul_f32 v[166:167], v[72:73], v[72:73]
	v_add_f32_e32 v151, v151, v169
	v_add_f32_e32 v149, v149, v72
	v_add_f32_e32 v149, v149, v73
	v_add_f32_e32 v151, v151, v166
	v_add_f32_e32 v151, v151, v167
	v_add_f32_e32 v149, v149, v66
	v_pk_mul_f32 v[168:169], v[66:67], v[66:67]
	v_add_f32_e32 v149, v149, v67
	v_add_f32_e32 v151, v151, v168
	v_pk_mul_f32 v[166:167], v[68:69], v[68:69]
	v_add_f32_e32 v151, v151, v169
	v_add_f32_e32 v149, v149, v68
	v_add_f32_e32 v169, v149, v69
	v_add_f32_e32 v149, v151, v166
	v_add_f32_e32 v168, v149, v167
	v_mov_b32_e32 v167, v169
	v_mov_b32_e32 v166, v168
	s_nop 0
	v_permlane32_swap_b32_e32 v169, v167
	v_permlane32_swap_b32_e32 v168, v166
	v_readfirstlane_b32 s3, v187
	v_pk_add_f32 v[166:167], v[168:169], v[166:167]
	v_lshl_add_u64 v[168:169], v[180:181], 0, s[8:9]
	s_mov_b32 m0, s3
	s_nop 0
	global_load_lds_dwordx4 v[168:169], off
	global_load_lds_dwordx4 v[168:169], off offset:1024
	global_load_lds_dwordx4 v[168:169], off offset:2048
	global_load_lds_dwordx4 v[168:169], off offset:3072
	v_pk_mul_f32 v[166:167], v[166:167], s[0:1] op_sel_hi:[1,0]
	s_mov_b32 s2, 0x800000
	v_fma_f32 v149, -v167, v167, v166
	v_add_f32_e32 v149, 0x3727c5ac, v149
	v_mul_f32_e32 v151, 0x4b800000, v149
	v_cmp_gt_f32_e32 vcc, s2, v149
	v_pk_add_f32 v[4:5], v[152:153], v[4:5]
	v_pk_add_f32 v[2:3], v[158:159], v[2:3]
	v_cndmask_b32_e32 v149, v149, v151, vcc
	v_rsq_f32_e32 v149, v149
	v_pk_add_f32 v[26:27], v[184:185], v[26:27]
	v_pk_add_f32 v[28:29], v[172:173], v[28:29]
	v_pk_add_f32 v[172:173], v[206:207], v[214:215]
	v_mul_f32_e32 v151, 0x45800000, v149
	v_cndmask_b32_e32 v152, v149, v151, vcc
	v_mul_f32_e64 v158, v152, -v167
	v_pk_add_f32 v[184:185], v[204:205], v[212:213]
	v_pk_add_f32 v[192:193], v[210:211], v[218:219]
	v_pk_add_f32 v[194:195], v[208:209], v[216:217]
	v_pk_fma_f32 v[142:143], v[152:153], v[142:143], v[158:159] op_sel_hi:[0,1,0]
	v_pk_fma_f32 v[144:145], v[152:153], v[144:145], v[158:159] op_sel_hi:[0,1,0]
	v_pk_fma_f32 v[138:139], v[152:153], v[138:139], v[158:159] op_sel_hi:[0,1,0]
	v_pk_fma_f32 v[140:141], v[152:153], v[140:141], v[158:159] op_sel_hi:[0,1,0]
	v_pk_fma_f32 v[134:135], v[152:153], v[134:135], v[158:159] op_sel_hi:[0,1,0]
	v_pk_fma_f32 v[136:137], v[152:153], v[136:137], v[158:159] op_sel_hi:[0,1,0]
	v_pk_fma_f32 v[130:131], v[152:153], v[130:131], v[158:159] op_sel_hi:[0,1,0]
	v_pk_fma_f32 v[132:133], v[152:153], v[132:133], v[158:159] op_sel_hi:[0,1,0]
	v_pk_fma_f32 v[126:127], v[152:153], v[126:127], v[158:159] op_sel_hi:[0,1,0]
	v_pk_fma_f32 v[128:129], v[152:153], v[128:129], v[158:159] op_sel_hi:[0,1,0]
	v_pk_fma_f32 v[122:123], v[152:153], v[122:123], v[158:159] op_sel_hi:[0,1,0]
	v_pk_fma_f32 v[124:125], v[152:153], v[124:125], v[158:159] op_sel_hi:[0,1,0]
	v_pk_fma_f32 v[118:119], v[152:153], v[118:119], v[158:159] op_sel_hi:[0,1,0]
	v_pk_fma_f32 v[120:121], v[152:153], v[120:121], v[158:159] op_sel_hi:[0,1,0]
	v_pk_fma_f32 v[114:115], v[152:153], v[114:115], v[158:159] op_sel_hi:[0,1,0]
	v_pk_fma_f32 v[116:117], v[152:153], v[116:117], v[158:159] op_sel_hi:[0,1,0]
	v_pk_fma_f32 v[106:107], v[152:153], v[106:107], v[158:159] op_sel_hi:[0,1,0]
	v_pk_fma_f32 v[108:109], v[152:153], v[108:109], v[158:159] op_sel_hi:[0,1,0]
	v_pk_fma_f32 v[102:103], v[152:153], v[102:103], v[158:159] op_sel_hi:[0,1,0]
	v_pk_fma_f32 v[104:105], v[152:153], v[104:105], v[158:159] op_sel_hi:[0,1,0]
	v_pk_fma_f32 v[98:99], v[152:153], v[98:99], v[158:159] op_sel_hi:[0,1,0]
	v_pk_fma_f32 v[100:101], v[152:153], v[100:101], v[158:159] op_sel_hi:[0,1,0]
	v_pk_fma_f32 v[94:95], v[152:153], v[94:95], v[158:159] op_sel_hi:[0,1,0]
	v_pk_fma_f32 v[96:97], v[152:153], v[96:97], v[158:159] op_sel_hi:[0,1,0]
	v_pk_fma_f32 v[78:79], v[152:153], v[78:79], v[158:159] op_sel_hi:[0,1,0]
	v_pk_fma_f32 v[80:81], v[152:153], v[80:81], v[158:159] op_sel_hi:[0,1,0]
	v_pk_fma_f32 v[74:75], v[152:153], v[74:75], v[158:159] op_sel_hi:[0,1,0]
	v_pk_fma_f32 v[76:77], v[152:153], v[76:77], v[158:159] op_sel_hi:[0,1,0]
	v_pk_add_f32 v[14:15], v[194:195], v[14:15]
	v_pk_add_f32 v[10:11], v[184:185], v[10:11]
	v_pk_add_f32 v[16:17], v[192:193], v[16:17]
	v_pk_add_f32 v[12:13], v[172:173], v[12:13]
	v_cvt_pk_bf16_f32 v141, v140, v141
	v_cvt_pk_bf16_f32 v140, v138, v139
	v_cvt_pk_bf16_f32 v139, v144, v145
	v_cvt_pk_bf16_f32 v138, v142, v143
	v_cvt_pk_bf16_f32 v133, v132, v133
	v_cvt_pk_bf16_f32 v132, v130, v131
	v_cvt_pk_bf16_f32 v131, v136, v137
	v_cvt_pk_bf16_f32 v130, v134, v135
	v_cvt_pk_bf16_f32 v125, v124, v125
	v_cvt_pk_bf16_f32 v124, v122, v123
	v_cvt_pk_bf16_f32 v123, v128, v129
	v_cvt_pk_bf16_f32 v122, v126, v127
	v_cvt_pk_bf16_f32 v117, v116, v117
	v_cvt_pk_bf16_f32 v116, v114, v115
	v_cvt_pk_bf16_f32 v115, v120, v121
	v_cvt_pk_bf16_f32 v114, v118, v119
	v_cvt_pk_bf16_f32 v105, v104, v105
	v_cvt_pk_bf16_f32 v104, v102, v103
	v_cvt_pk_bf16_f32 v103, v108, v109
	v_cvt_pk_bf16_f32 v102, v106, v107
	v_cvt_pk_bf16_f32 v109, v96, v97
	v_cvt_pk_bf16_f32 v108, v94, v95
	v_cvt_pk_bf16_f32 v107, v100, v101
	v_cvt_pk_bf16_f32 v106, v98, v99
	v_cvt_pk_bf16_f32 v121, v76, v77
	v_cvt_pk_bf16_f32 v120, v74, v75
	v_cvt_pk_bf16_f32 v119, v80, v81
	v_cvt_pk_bf16_f32 v118, v78, v79
	v_pk_fma_f32 v[172:173], v[152:153], v[70:71], v[158:159] op_sel_hi:[0,1,0]
	v_pk_fma_f32 v[94:95], v[152:153], v[72:73], v[158:159] op_sel_hi:[0,1,0]
	v_pk_fma_f32 v[184:185], v[152:153], v[66:67], v[158:159] op_sel_hi:[0,1,0]
	v_pk_fma_f32 v[96:97], v[152:153], v[68:69], v[158:159] op_sel_hi:[0,1,0]
	ds_read_b128 v[66:69], v176
	ds_read_b128 v[70:73], v176 offset:1024
	ds_read_b128 v[74:77], v176 offset:2048
	ds_read_b128 v[78:81], v176 offset:3072
	ds_read_b128 v[98:101], v176 offset:4096
	ds_read_b128 v[126:129], v176 offset:5120
	ds_read_b128 v[134:137], v176 offset:6144
	ds_read_b128 v[142:145], v176 offset:7168
	ds_read_b128 v[166:169], v176 offset:8192
	ds_read_b128 v[192:195], v176 offset:9216
	v_cvt_pk_bf16_f32 v97, v96, v97
	v_cvt_pk_bf16_f32 v96, v184, v185
	v_cvt_pk_bf16_f32 v95, v94, v95
	v_cvt_pk_bf16_f32 v94, v172, v173
	ds_read_b128 v[196:199], v176 offset:10240
	ds_read_b128 v[200:203], v176 offset:11264
	ds_read_b128 v[204:207], v176 offset:12288
	ds_read_b128 v[208:211], v176 offset:13312
	ds_read_b128 v[212:215], v176 offset:14336
	s_waitcnt lgkmcnt(0)
	v_mfma_f32_32x32x16_bf16 v[50:65], v[66:69], v[138:141], v[50:65]
	v_mfma_f32_32x32x16_bf16 v[34:49], v[70:73], v[138:141], v[34:49]
	v_mfma_f32_32x32x16_bf16 v[18:33], v[74:77], v[138:141], v[18:33]
	v_mfma_f32_32x32x16_bf16 v[2:17], v[78:81], v[138:141], v[2:17]
	v_mfma_f32_32x32x16_bf16 v[66:81], v[98:101], v[138:141], 0
	v_mfma_f32_32x32x16_bf16 v[50:65], v[126:129], v[130:133], v[50:65]
	v_mfma_f32_32x32x16_bf16 v[34:49], v[134:137], v[130:133], v[34:49]
	v_mfma_f32_32x32x16_bf16 v[18:33], v[142:145], v[130:133], v[18:33]
	ds_read_b128 v[98:101], v176 offset:15360
	ds_read_b128 v[126:129], v176 offset:16384
	ds_read_b128 v[134:137], v176 offset:17408
	ds_read_b128 v[138:141], v176 offset:18432
	ds_read_b128 v[142:145], v176 offset:19456
	v_mfma_f32_32x32x16_bf16 v[2:17], v[166:169], v[130:133], v[2:17]
	v_mfma_f32_32x32x16_bf16 v[66:81], v[192:195], v[130:133], v[66:81]
	v_mfma_f32_32x32x16_bf16 v[50:65], v[196:199], v[122:125], v[50:65]
	v_mfma_f32_32x32x16_bf16 v[34:49], v[200:203], v[122:125], v[34:49]
	v_mfma_f32_32x32x16_bf16 v[18:33], v[204:207], v[122:125], v[18:33]
	v_mfma_f32_32x32x16_bf16 v[2:17], v[208:211], v[122:125], v[2:17]
	v_mfma_f32_32x32x16_bf16 v[66:81], v[212:215], v[122:125], v[66:81]
	s_mov_b64 s[8:9], 0x1a000
	v_readfirstlane_b32 s3, v186
	s_waitcnt lgkmcnt(0)
	v_mfma_f32_32x32x16_bf16 v[50:65], v[98:101], v[114:117], v[50:65]
	v_lshl_add_u64 v[98:99], v[180:181], 0, s[8:9]
	s_mov_b32 m0, s3
	s_waitcnt vmcnt(8) lgkmcnt(0)
	s_barrier
	global_load_lds_dwordx4 v[98:99], off
	global_load_lds_dwordx4 v[98:99], off offset:1024
	global_load_lds_dwordx4 v[98:99], off offset:2048
	global_load_lds_dwordx4 v[98:99], off offset:3072
	v_mfma_f32_32x32x16_bf16 v[34:49], v[126:129], v[114:117], v[34:49]
	ds_read_b128 v[98:101], v176 offset:20480
	ds_read_b128 v[122:125], v176 offset:21504
	v_mfma_f32_32x32x16_bf16 v[18:33], v[134:137], v[114:117], v[18:33]
	v_mfma_f32_32x32x16_bf16 v[2:17], v[138:141], v[114:117], v[2:17]
	ds_read_b128 v[126:129], v176 offset:22528
	ds_read_b128 v[130:133], v176 offset:23552
	ds_read_b128 v[134:137], v176 offset:24576
	ds_read_b128 v[138:141], v176 offset:25600
	ds_read_b128 v[166:169], v176 offset:26624
	ds_read_b128 v[192:195], v176 offset:27648
	ds_read_b128 v[196:199], v176 offset:28672
	ds_read_b128 v[200:203], v176 offset:29696
	v_mfma_f32_32x32x16_bf16 v[66:81], v[142:145], v[114:117], v[66:81]
	s_waitcnt lgkmcnt(0)
	v_mfma_f32_32x32x16_bf16 v[34:49], v[122:125], v[102:105], v[34:49]
	v_mfma_f32_32x32x16_bf16 v[18:33], v[126:129], v[102:105], v[18:33]
	v_mfma_f32_32x32x16_bf16 v[2:17], v[130:133], v[102:105], v[2:17]
	ds_read_b128 v[114:117], v176 offset:31744
	ds_read_b128 v[122:125], v176 offset:32768
	ds_read_b128 v[126:129], v176 offset:33792
	ds_read_b128 v[130:133], v176 offset:30720
	ds_read_b128 v[142:145], v176 offset:34816
	v_mfma_f32_32x32x16_bf16 v[50:65], v[98:101], v[102:105], v[50:65]
	v_mfma_f32_32x32x16_bf16 v[66:81], v[134:137], v[102:105], v[66:81]
	v_mfma_f32_32x32x16_bf16 v[50:65], v[138:141], v[106:109], v[50:65]
	v_mfma_f32_32x32x16_bf16 v[34:49], v[166:169], v[106:109], v[34:49]
	ds_read_b128 v[102:105], v176 offset:35840
	ds_read_b128 v[134:137], v176 offset:36864
	ds_read_b128 v[138:141], v176 offset:37888
	ds_read_b128 v[166:169], v176 offset:38912
	ds_read_b128 v[98:101], v176 offset:39936
	v_mfma_f32_32x32x16_bf16 v[18:33], v[192:195], v[106:109], v[18:33]
	v_mfma_f32_32x32x16_bf16 v[2:17], v[196:199], v[106:109], v[2:17]
	v_mfma_f32_32x32x16_bf16 v[66:81], v[200:203], v[106:109], v[66:81]
	s_waitcnt lgkmcnt(0)
	v_mfma_f32_32x32x16_bf16 v[50:65], v[130:133], v[118:121], v[50:65]
	v_mfma_f32_32x32x16_bf16 v[34:49], v[114:117], v[118:121], v[34:49]
	v_mfma_f32_32x32x16_bf16 v[18:33], v[122:125], v[118:121], v[18:33]
	v_mfma_f32_32x32x16_bf16 v[2:17], v[126:129], v[118:121], v[2:17]
	v_mfma_f32_32x32x16_bf16 v[66:81], v[142:145], v[118:121], v[66:81]
	s_mov_b64 s[8:9], 0x1e000
	v_readfirstlane_b32 s3, v190
	v_mfma_f32_32x32x16_bf16 v[50:65], v[102:105], v[94:97], v[50:65]
	v_lshl_add_u64 v[102:103], v[180:181], 0, s[8:9]
	s_mov_b32 m0, s3
	s_waitcnt vmcnt(4) lgkmcnt(0)
	s_barrier
	global_load_lds_dwordx4 v[102:103], off
	global_load_lds_dwordx4 v[102:103], off offset:1024
	global_load_lds_dwordx4 v[102:103], off offset:2048
	global_load_lds_dwordx4 v[102:103], off offset:3072
	s_waitcnt vmcnt(4)
	v_mfma_f32_32x32x16_bf16 v[34:49], v[134:137], v[94:97], v[34:49]
	ds_read_b128 v[102:105], v176 offset:40960
	ds_read_b128 v[106:109], v176 offset:41984
	v_mfma_f32_32x32x16_bf16 v[18:33], v[138:141], v[94:97], v[18:33]
	ds_read_b128 v[114:117], v176 offset:43008
	ds_read_b128 v[118:121], v176 offset:44032
	ds_read_b128 v[122:125], v189 offset:58112
	ds_read_b128 v[126:129], v189 offset:58128
	ds_read_b128 v[130:133], v176 offset:45056
	ds_read_b128 v[134:137], v176 offset:46080
	ds_read_b128 v[138:141], v176 offset:47104
	ds_read_b128 v[142:145], v176 offset:48128
	ds_read_b128 v[190:193], v189 offset:58176
	ds_read_b128 v[194:197], v189 offset:58192
	v_mfma_f32_32x32x16_bf16 v[2:17], v[166:169], v[94:97], v[2:17]
	v_lshlrev_b32_e32 v152, 16, v110
	v_and_b32_e32 v153, 0xffff0000, v110
	v_lshlrev_b32_e32 v158, 16, v111
	v_and_b32_e32 v159, 0xffff0000, v111
	v_lshlrev_b32_e32 v110, 16, v112
	v_and_b32_e32 v111, 0xffff0000, v112
	v_lshlrev_b32_e32 v112, 16, v113
	v_and_b32_e32 v113, 0xffff0000, v113
	s_waitcnt lgkmcnt(0)
	v_pk_mul_f32 v[166:167], v[122:123], v[152:153]
	v_pk_mul_f32 v[168:169], v[124:125], v[158:159]
	v_pk_mul_f32 v[128:129], v[128:129], v[112:113]
	v_pk_mul_f32 v[126:127], v[126:127], v[110:111]
	v_cvt_pk_bf16_f32 v113, v128, v129
	v_cvt_pk_bf16_f32 v112, v126, v127
	v_cvt_pk_bf16_f32 v111, v168, v169
	v_cvt_pk_bf16_f32 v110, v166, v167
	v_pk_fma_f32 v[152:153], v[122:123], v[152:153], v[126:127]
	v_pk_fma_f32 v[158:159], v[124:125], v[158:159], v[128:129]
	v_mfma_f32_32x32x16_bf16 v[50:65], v[102:105], v[110:113], v[50:65]
	v_mfma_f32_32x32x16_bf16 v[34:49], v[106:109], v[110:113], v[34:49]
	v_mfma_f32_32x32x16_bf16 v[18:33], v[114:117], v[110:113], v[18:33]
	ds_read_b128 v[102:105], v176 offset:49152
	ds_read_b128 v[106:109], v176 offset:50176
	ds_read_b128 v[114:117], v176 offset:51200
	ds_read_b128 v[122:125], v176 offset:52224
	ds_read_b128 v[126:129], v189 offset:58240
	ds_read_b128 v[166:169], v189 offset:58256
	v_mfma_f32_32x32x16_bf16 v[2:17], v[118:121], v[110:113], v[2:17]
	v_lshlrev_b32_e32 v110, 16, v90
	v_and_b32_e32 v111, 0xffff0000, v90
	v_lshlrev_b32_e32 v112, 16, v91
	v_and_b32_e32 v113, 0xffff0000, v91
	v_lshlrev_b32_e32 v90, 16, v92
	v_and_b32_e32 v91, 0xffff0000, v92
	v_lshlrev_b32_e32 v92, 16, v93
	v_and_b32_e32 v93, 0xffff0000, v93
	v_pk_mul_f32 v[172:173], v[196:197], v[92:93]
	v_pk_mul_f32 v[184:185], v[194:195], v[90:91]
	v_pk_mul_f32 v[118:119], v[190:191], v[110:111]
	v_pk_mul_f32 v[120:121], v[192:193], v[112:113]
	v_pk_fma_f32 v[110:111], v[190:191], v[110:111], v[184:185]
	v_pk_fma_f32 v[112:113], v[192:193], v[112:113], v[172:173]
	v_pk_add_f32 v[110:111], v[152:153], v[110:111]
	v_pk_add_f32 v[112:113], v[158:159], v[112:113]
	v_cvt_pk_bf16_f32 v90, v118, v119
	v_pk_mov_b32 v[118:119], v[110:111], v[112:113] op_sel:[1,0]
	v_mov_b32_e32 v111, v113
	v_cvt_pk_bf16_f32 v93, v172, v173
	v_cvt_pk_bf16_f32 v92, v184, v185
	v_cvt_pk_bf16_f32 v91, v120, v121
	v_pk_add_f32 v[110:111], v[118:119], v[110:111]
	s_nop 0
	v_mfma_f32_32x32x16_bf16 v[50:65], v[130:133], v[90:93], v[50:65]
	v_add_f32_e64 v152, v110, v111
	v_add_f32_e64 v153, v111, v110
	v_mfma_f32_32x32x16_bf16 v[34:49], v[134:137], v[90:93], v[34:49]
	v_mfma_f32_32x32x16_bf16 v[18:33], v[138:141], v[90:93], v[18:33]
	ds_read_b128 v[110:113], v176 offset:53248
	ds_read_b128 v[118:121], v176 offset:54272
	ds_read_b128 v[130:133], v176 offset:55296
	ds_read_b128 v[134:137], v176 offset:56320
	ds_read_b128 v[138:141], v189 offset:58304
	ds_read_b128 v[190:193], v189 offset:58320
	v_mfma_f32_32x32x16_bf16 v[2:17], v[142:145], v[90:93], v[2:17]
	v_lshlrev_b32_e32 v90, 16, v86
	v_and_b32_e32 v91, 0xffff0000, v86
	v_lshlrev_b32_e32 v92, 16, v87
	v_and_b32_e32 v93, 0xffff0000, v87
	v_lshlrev_b32_e32 v86, 16, v88
	v_and_b32_e32 v87, 0xffff0000, v88
	v_lshlrev_b32_e32 v88, 16, v89
	v_and_b32_e32 v89, 0xffff0000, v89
	s_waitcnt lgkmcnt(0)
	v_pk_mul_f32 v[142:143], v[128:129], v[92:93]
	v_pk_mul_f32 v[144:145], v[126:127], v[90:91]
	v_pk_mul_f32 v[158:159], v[166:167], v[86:87]
	v_pk_mul_f32 v[166:167], v[168:169], v[88:89]
	v_cvt_pk_bf16_f32 v88, v158, v159
	v_cvt_pk_bf16_f32 v86, v144, v145
	v_cvt_pk_bf16_f32 v89, v166, v167
	v_cvt_pk_bf16_f32 v87, v142, v143
	v_pk_fma_f32 v[92:93], v[128:129], v[92:93], v[166:167]
	v_pk_fma_f32 v[90:91], v[126:127], v[90:91], v[158:159]
	v_mfma_f32_32x32x16_bf16 v[50:65], v[102:105], v[86:89], v[50:65]
	v_mfma_f32_32x32x16_bf16 v[34:49], v[106:109], v[86:89], v[34:49]
	v_mfma_f32_32x32x16_bf16 v[18:33], v[114:117], v[86:89], v[18:33]
	v_mfma_f32_32x32x16_bf16 v[2:17], v[122:125], v[86:89], v[2:17]
	v_lshlrev_b32_e32 v86, 16, v82
	v_and_b32_e32 v87, 0xffff0000, v82
	v_lshlrev_b32_e32 v88, 16, v83
	v_and_b32_e32 v89, 0xffff0000, v83
	v_lshlrev_b32_e32 v82, 16, v84
	v_and_b32_e32 v83, 0xffff0000, v84
	v_lshlrev_b32_e32 v84, 16, v85
	v_and_b32_e32 v85, 0xffff0000, v85
	v_mfma_f32_32x32x16_bf16 v[66:81], v[98:101], v[94:97], v[66:81]
	v_mul_f32_e64 v102, v140, v88
	v_mul_f32_e64 v103, v141, v89
	v_mul_f32_e64 v104, v138, v86
	v_mul_f32_e64 v105, v139, v87
	v_mul_f32_e64 v106, v190, v82
	v_mul_f32_e64 v107, v191, v83
	v_pk_mul_f32 v[108:109], v[192:193], v[84:85]
	v_cvt_pk_bf16_f32 v84, v106, v107
	v_cvt_pk_bf16_f32 v82, v104, v105
	v_cvt_pk_bf16_f32 v85, v108, v109
	v_cvt_pk_bf16_f32 v83, v102, v103
	s_waitcnt vmcnt(4) lgkmcnt(0)
	s_nop 0
	v_mfma_f32_32x32x16_bf16 v[50:65], v[110:113], v[82:85], v[50:65]
	s_barrier
	v_permlane32_swap_b32_e32 v162, v150
	v_permlane32_swap_b32_e32 v170, v148
	v_mov_b32_e32 v171, v162
	v_mov_b32_e32 v149, v150
	v_mfma_f32_32x32x16_bf16 v[34:49], v[118:121], v[82:85], v[34:49]
	v_add_f32_e64 v70, v170, v148
	v_add_f32_e64 v71, v171, v149
	s_mov_b32 s8, 0x3e3504f3
	v_add_f32_e64 v66, v66, v70
	v_add_f32_e64 v67, v67, v71
	v_or_b32_e32 v182, v182, v188
	v_mul_f32_e32 v74, v51, v51
	v_fmac_f32_e32 v74, v50, v50
	v_fmac_f32_e32 v74, v52, v52
	v_mfma_f32_32x32x16_bf16 v[18:33], v[130:133], v[82:85], v[18:33]
	v_fmac_f32_e32 v74, v53, v53
	v_fmac_f32_e32 v74, v54, v54
	v_fmac_f32_e32 v74, v55, v55
	v_fmac_f32_e32 v74, v56, v56
	v_fmac_f32_e32 v74, v57, v57
	v_fmac_f32_e32 v74, v58, v58
	v_fmac_f32_e32 v74, v59, v59
	v_mfma_f32_32x32x16_bf16 v[2:17], v[134:137], v[82:85], v[2:17]
	ds_read_b128 v[82:85], v147 offset:59904
	v_fmac_f32_e32 v74, v60, v60
	v_fmac_f32_e32 v74, v61, v61
	v_fmac_f32_e32 v74, v62, v62
	v_fmac_f32_e32 v74, v63, v63
	s_waitcnt lgkmcnt(0)
	v_pk_add_f32 v[66:67], v[82:83], v[66:67]
	v_fmac_f32_e32 v74, v64, v64
	v_pk_mul_f32 v[130:131], v[66:67], s[8:9] op_sel_hi:[1,0]
	v_lshlrev_b64 v[66:67], 5, v[182:183]
	v_lshl_add_u64 v[134:135], s[4:5], 0, v[66:67]
	v_add_f32_e32 v66, 0, v50
	v_add_f32_e32 v66, v66, v51
	v_add_f32_e32 v66, v66, v52
	v_add_f32_e32 v66, v66, v53
	v_add_f32_e32 v66, v66, v54
	v_add_f32_e32 v66, v66, v55
	v_add_f32_e32 v66, v66, v56
	v_add_f32_e32 v66, v66, v57
	v_add_f32_e32 v66, v66, v58
	v_add_f32_e32 v66, v66, v59
	v_add_f32_e32 v66, v66, v60
	v_add_f32_e32 v66, v66, v61
	v_add_f32_e32 v66, v66, v62
	v_add_f32_e32 v66, v66, v63
	v_add_f32_e32 v66, v66, v64
	v_add_f32_e32 v66, v66, v65
	v_fmac_f32_e32 v74, v65, v65
	v_add_f32_e32 v66, v66, v34
	v_fmac_f32_e32 v74, v34, v34
	v_add_f32_e32 v66, v66, v35
	v_fmac_f32_e32 v74, v35, v35
	v_add_f32_e32 v66, v66, v36
	v_fmac_f32_e32 v74, v36, v36
	v_add_f32_e32 v66, v66, v37
	v_fmac_f32_e32 v74, v37, v37
	v_add_f32_e32 v66, v66, v38
	v_fmac_f32_e32 v74, v38, v38
	v_add_f32_e32 v66, v66, v39
	v_fmac_f32_e32 v74, v39, v39
	v_add_f32_e32 v66, v66, v40
	v_fmac_f32_e32 v74, v40, v40
	v_add_f32_e32 v66, v66, v41
	v_fmac_f32_e32 v74, v41, v41
	v_add_f32_e32 v66, v66, v42
	v_fmac_f32_e32 v74, v42, v42
	v_add_f32_e32 v66, v66, v43
	v_fmac_f32_e32 v74, v43, v43
	v_add_f32_e32 v66, v66, v44
	v_fmac_f32_e32 v74, v44, v44
	v_add_f32_e32 v66, v66, v45
	v_fmac_f32_e32 v74, v45, v45
	v_add_f32_e32 v66, v66, v46
	v_fmac_f32_e32 v74, v46, v46
	v_add_f32_e32 v66, v66, v47
	v_fmac_f32_e32 v74, v47, v47
	v_add_f32_e32 v66, v66, v48
	v_fmac_f32_e32 v74, v48, v48
	v_add_f32_e32 v66, v66, v49
	v_fmac_f32_e32 v74, v49, v49
	v_add_f32_e32 v66, v66, v18
	v_fmac_f32_e32 v74, v18, v18
	v_add_f32_e32 v66, v66, v19
	v_fmac_f32_e32 v74, v19, v19
	v_add_f32_e32 v66, v66, v20
	v_fmac_f32_e32 v74, v20, v20
	v_add_f32_e32 v66, v66, v21
	v_fmac_f32_e32 v74, v21, v21
	v_add_f32_e32 v66, v66, v22
	v_fmac_f32_e32 v74, v22, v22
	v_add_f32_e32 v66, v66, v23
	v_fmac_f32_e32 v74, v23, v23
	v_add_f32_e32 v66, v66, v24
	v_fmac_f32_e32 v74, v24, v24
	v_add_f32_e32 v66, v66, v25
	v_fmac_f32_e32 v74, v25, v25
	v_add_f32_e32 v66, v66, v26
	v_fmac_f32_e32 v74, v26, v26
	v_add_f32_e32 v66, v66, v27
	v_fmac_f32_e32 v74, v27, v27
	v_add_f32_e32 v66, v66, v28
	v_fmac_f32_e32 v74, v28, v28
	v_add_f32_e32 v66, v66, v29
	v_fmac_f32_e32 v74, v29, v29
	v_add_f32_e32 v66, v66, v30
	v_fmac_f32_e32 v74, v30, v30
	v_add_f32_e32 v66, v66, v31
	v_fmac_f32_e32 v74, v31, v31
	v_add_f32_e32 v66, v66, v32
	v_fmac_f32_e32 v74, v32, v32
	v_add_f32_e32 v66, v66, v33
	v_fmac_f32_e32 v74, v33, v33
	v_add_f32_e32 v66, v66, v2
	v_fmac_f32_e32 v74, v2, v2
	v_pk_fma_f32 v[88:89], v[140:141], v[88:89], v[108:109]
	v_pk_fma_f32 v[86:87], v[138:139], v[86:87], v[106:107]
	v_add_f32_e32 v66, v66, v3
	v_fmac_f32_e32 v74, v3, v3
	v_pk_add_f32 v[86:87], v[90:91], v[86:87]
	v_pk_add_f32 v[88:89], v[92:93], v[88:89]
	v_add_f32_e32 v66, v66, v4
	v_fmac_f32_e32 v74, v4, v4
	v_pk_mov_b32 v[90:91], v[86:87], v[88:89] op_sel:[1,0]
	v_mov_b32_e32 v87, v89
	v_add_f32_e32 v66, v66, v5
	v_fmac_f32_e32 v74, v5, v5
	v_pk_add_f32 v[86:87], v[90:91], v[86:87]
	v_add_f32_e32 v66, v66, v6
	v_fmac_f32_e32 v74, v6, v6
	v_pk_add_f32 v[86:87], v[86:87], v[86:87] op_sel:[0,1] op_sel_hi:[1,0]
	v_add_f32_e32 v66, v66, v7
	v_fmac_f32_e32 v74, v7, v7
	v_permlane32_swap_b32_e32 v146, v86
	v_add_f32_e32 v66, v66, v8
	v_fmac_f32_e32 v74, v8, v8
	v_permlane32_swap_b32_e32 v156, v152
	v_mov_b32_e32 v157, v146
	v_mov_b32_e32 v153, v86
	v_add_f32_e32 v66, v66, v9
	v_fmac_f32_e32 v74, v9, v9
	v_pk_mul_f32 v[72:73], v[10:11], v[10:11]
	v_pk_add_f32 v[70:71], v[156:157], v[152:153]
	v_add_f32_e32 v66, v66, v10
	v_add_f32_e32 v72, v74, v72
	v_pk_add_f32 v[68:69], v[68:69], v[70:71]
	v_add_f32_e32 v75, v66, v11
	v_pk_mul_f32 v[70:71], v[12:13], v[12:13]
	v_add_f32_e32 v72, v72, v73
	v_pk_add_f32 v[68:69], v[84:85], v[68:69]
	v_add_f32_e32 v73, v75, v12
	v_add_f32_e32 v70, v72, v70
	v_pk_mul_f32 v[132:133], v[68:69], s[8:9] op_sel_hi:[1,0]
	v_pk_mul_f32 v[68:69], v[14:15], v[14:15]
	v_add_f32_e32 v73, v73, v13
	v_add_f32_e32 v70, v70, v71
	v_add_f32_e32 v71, v73, v14
	v_add_f32_e32 v68, v70, v68
	v_pk_mul_f32 v[66:67], v[16:17], v[16:17]
	v_add_f32_e32 v71, v71, v15
	v_add_f32_e32 v68, v68, v69
	v_add_f32_e32 v69, v71, v16
	v_add_f32_e32 v66, v68, v66
	v_add_f32_e32 v69, v69, v17
	v_add_f32_e32 v68, v66, v67
	v_mov_b32_e32 v67, v69
	v_mov_b32_e32 v66, v68
	s_nop 0
	v_permlane32_swap_b32_e32 v69, v67
	v_permlane32_swap_b32_e32 v68, v66
	v_pk_add_f32 v[66:67], v[68:69], v[66:67]
	v_mov_b32_e32 v155, v175
	v_pk_mul_f32 v[136:137], v[66:67], s[0:1] op_sel_hi:[1,0]
	v_readfirstlane_b32 s0, v187
	v_fma_f32 v66, -v137, v137, v136
	v_add_f32_e32 v66, 0x3727c5ac, v66
	v_cmp_gt_f32_e32 vcc, s2, v66
	s_mov_b64 s[2:3], 0x22000
	v_mul_f32_e32 v67, 0x4b800000, v66
	v_lshl_add_u64 v[138:139], v[180:181], 0, s[2:3]
	s_mov_b32 m0, s0
	v_cndmask_b32_e32 v136, v66, v67, vcc
	ds_read_b128 v[114:117], v147 offset:58880
	ds_read_b128 v[118:121], v147 offset:58912
	ds_read_b128 v[122:125], v147 offset:58944
	ds_read_b128 v[126:129], v147 offset:58976
	ds_read_b128 v[98:101], v147 offset:59008
	ds_read_b128 v[102:105], v147 offset:59040
	ds_read_b128 v[106:109], v147 offset:59072
	ds_read_b128 v[110:113], v147 offset:59104
	ds_read_b128 v[82:85], v147 offset:59136
	ds_read_b128 v[86:89], v147 offset:59168
	ds_read_b128 v[90:93], v147 offset:59200
	ds_read_b128 v[94:97], v147 offset:59232
	ds_read_b128 v[66:69], v147 offset:59264
	ds_read_b128 v[70:73], v147 offset:59296
	ds_read_b128 v[74:77], v147 offset:59328
	ds_read_b128 v[78:81], v147 offset:59360
	global_load_lds_dwordx4 v[138:139], off
	global_load_lds_dwordx4 v[138:139], off offset:1024
	global_load_lds_dwordx4 v[138:139], off offset:2048
	global_load_lds_dwordx4 v[138:139], off offset:3072
	v_rsq_f32_e32 v136, v136
	v_lshl_add_u64 v[134:135], v[134:135], 0, v[154:155]
	global_store_dwordx4 v[134:135], v[130:133], off nt
	s_nop 1
	v_mul_f32_e32 v130, 0x45800000, v136
	v_cndmask_b32_e32 v162, v136, v130, vcc
	v_mul_f32_e64 v166, v162, -v137
	v_pk_fma_f32 v[134:135], v[162:163], v[50:51], v[166:167] op_sel_hi:[0,1,0]
	v_pk_fma_f32 v[130:131], v[162:163], v[52:53], v[166:167] op_sel_hi:[0,1,0]
	v_pk_fma_f32 v[136:137], v[162:163], v[54:55], v[166:167] op_sel_hi:[0,1,0]
	v_pk_fma_f32 v[132:133], v[162:163], v[56:57], v[166:167] op_sel_hi:[0,1,0]
	v_cvt_pk_bf16_f32 v133, v132, v133
	v_cvt_pk_bf16_f32 v132, v136, v137
	v_cvt_pk_bf16_f32 v131, v130, v131
	v_cvt_pk_bf16_f32 v130, v134, v135
	v_pk_fma_f32 v[138:139], v[162:163], v[58:59], v[166:167] op_sel_hi:[0,1,0]
	v_pk_fma_f32 v[134:135], v[162:163], v[60:61], v[166:167] op_sel_hi:[0,1,0]
	v_pk_fma_f32 v[140:141], v[162:163], v[62:63], v[166:167] op_sel_hi:[0,1,0]
	v_pk_fma_f32 v[136:137], v[162:163], v[64:65], v[166:167] op_sel_hi:[0,1,0]
	v_cvt_pk_bf16_f32 v137, v136, v137
	v_cvt_pk_bf16_f32 v136, v140, v141
	v_cvt_pk_bf16_f32 v135, v134, v135
	v_cvt_pk_bf16_f32 v134, v138, v139
	v_pk_fma_f32 v[142:143], v[162:163], v[34:35], v[166:167] op_sel_hi:[0,1,0]
	v_pk_fma_f32 v[138:139], v[162:163], v[36:37], v[166:167] op_sel_hi:[0,1,0]
	v_pk_fma_f32 v[144:145], v[162:163], v[38:39], v[166:167] op_sel_hi:[0,1,0]
	v_pk_fma_f32 v[140:141], v[162:163], v[40:41], v[166:167] op_sel_hi:[0,1,0]
	v_cvt_pk_bf16_f32 v141, v140, v141
	v_cvt_pk_bf16_f32 v140, v144, v145
	v_cvt_pk_bf16_f32 v139, v138, v139
	v_cvt_pk_bf16_f32 v138, v142, v143
	v_pk_fma_f32 v[146:147], v[162:163], v[42:43], v[166:167] op_sel_hi:[0,1,0]
	v_pk_fma_f32 v[142:143], v[162:163], v[44:45], v[166:167] op_sel_hi:[0,1,0]
	v_pk_fma_f32 v[148:149], v[162:163], v[46:47], v[166:167] op_sel_hi:[0,1,0]
	v_pk_fma_f32 v[144:145], v[162:163], v[48:49], v[166:167] op_sel_hi:[0,1,0]
	v_cvt_pk_bf16_f32 v145, v144, v145
	v_cvt_pk_bf16_f32 v144, v148, v149
	v_cvt_pk_bf16_f32 v143, v142, v143
	v_cvt_pk_bf16_f32 v142, v146, v147
	v_pk_fma_f32 v[150:151], v[162:163], v[18:19], v[166:167] op_sel_hi:[0,1,0]
	v_pk_fma_f32 v[146:147], v[162:163], v[20:21], v[166:167] op_sel_hi:[0,1,0]
	v_pk_fma_f32 v[152:153], v[162:163], v[22:23], v[166:167] op_sel_hi:[0,1,0]
	v_pk_fma_f32 v[148:149], v[162:163], v[24:25], v[166:167] op_sel_hi:[0,1,0]
	v_cvt_pk_bf16_f32 v149, v148, v149
	v_cvt_pk_bf16_f32 v148, v152, v153
	v_cvt_pk_bf16_f32 v147, v146, v147
	v_cvt_pk_bf16_f32 v146, v150, v151
	v_pk_fma_f32 v[156:157], v[162:163], v[26:27], v[166:167] op_sel_hi:[0,1,0]
	v_pk_fma_f32 v[150:151], v[162:163], v[28:29], v[166:167] op_sel_hi:[0,1,0]
	v_pk_fma_f32 v[158:159], v[162:163], v[30:31], v[166:167] op_sel_hi:[0,1,0]
	v_pk_fma_f32 v[152:153], v[162:163], v[32:33], v[166:167] op_sel_hi:[0,1,0]
	v_cvt_pk_bf16_f32 v153, v152, v153
	v_cvt_pk_bf16_f32 v152, v158, v159
	v_cvt_pk_bf16_f32 v151, v150, v151
	v_cvt_pk_bf16_f32 v150, v156, v157
	v_pk_fma_f32 v[168:169], v[162:163], v[2:3], v[166:167] op_sel_hi:[0,1,0]
	v_pk_fma_f32 v[156:157], v[162:163], v[4:5], v[166:167] op_sel_hi:[0,1,0]
	v_pk_fma_f32 v[170:171], v[162:163], v[6:7], v[166:167] op_sel_hi:[0,1,0]
	v_pk_fma_f32 v[158:159], v[162:163], v[8:9], v[166:167] op_sel_hi:[0,1,0]
	v_cvt_pk_bf16_f32 v159, v158, v159
	v_cvt_pk_bf16_f32 v158, v170, v171
	v_cvt_pk_bf16_f32 v157, v156, v157
	v_cvt_pk_bf16_f32 v156, v168, v169
	v_pk_fma_f32 v[212:213], v[162:163], v[10:11], v[166:167] op_sel_hi:[0,1,0]
	v_pk_fma_f32 v[208:209], v[162:163], v[12:13], v[166:167] op_sel_hi:[0,1,0]
	v_pk_fma_f32 v[214:215], v[162:163], v[14:15], v[166:167] op_sel_hi:[0,1,0]
	v_pk_fma_f32 v[210:211], v[162:163], v[16:17], v[166:167] op_sel_hi:[0,1,0]
	ds_read_b128 v[166:169], v176
	ds_read_b128 v[170:173], v176 offset:1024
	ds_read_b128 v[182:185], v176 offset:2048
	ds_read_b128 v[188:191], v176 offset:3072
	ds_read_b128 v[192:195], v176 offset:4096
	ds_read_b128 v[196:199], v176 offset:5120
	ds_read_b128 v[200:203], v176 offset:6144
	ds_read_b128 v[204:207], v176 offset:7168
	v_cvt_pk_bf16_f32 v211, v210, v211
	v_cvt_pk_bf16_f32 v210, v214, v215
	v_cvt_pk_bf16_f32 v209, v208, v209
	v_cvt_pk_bf16_f32 v208, v212, v213
	s_waitcnt lgkmcnt(0)
	v_mfma_f32_32x32x16_bf16 v[114:129], v[166:169], v[130:133], v[114:129]
	v_mfma_f32_32x32x16_bf16 v[98:113], v[170:173], v[130:133], v[98:113]
	v_mfma_f32_32x32x16_bf16 v[82:97], v[182:185], v[130:133], v[82:97]
	ds_read_b128 v[166:169], v176 offset:8192
	ds_read_b128 v[170:173], v176 offset:9216
	ds_read_b128 v[182:185], v176 offset:10240
	ds_read_b128 v[212:215], v176 offset:11264
	v_mfma_f32_32x32x16_bf16 v[66:81], v[188:191], v[130:133], v[66:81]
	v_mfma_f32_32x32x16_bf16 v[114:129], v[192:195], v[134:137], v[114:129]
	v_mfma_f32_32x32x16_bf16 v[98:113], v[196:199], v[134:137], v[98:113]
	ds_read_b128 v[130:133], v176 offset:12288
	ds_read_b128 v[188:191], v176 offset:13312
	ds_read_b128 v[192:195], v176 offset:14336
	ds_read_b128 v[196:199], v176 offset:15360
	v_mfma_f32_32x32x16_bf16 v[82:97], v[200:203], v[134:137], v[82:97]
	v_mfma_f32_32x32x16_bf16 v[66:81], v[204:207], v[134:137], v[66:81]
	s_waitcnt lgkmcnt(0)
	v_mfma_f32_32x32x16_bf16 v[114:129], v[166:169], v[138:141], v[114:129]
	v_mfma_f32_32x32x16_bf16 v[98:113], v[170:173], v[138:141], v[98:113]
	v_mfma_f32_32x32x16_bf16 v[82:97], v[182:185], v[138:141], v[82:97]
	v_mfma_f32_32x32x16_bf16 v[66:81], v[212:215], v[138:141], v[66:81]
	s_mov_b64 s[2:3], 0x26000
	v_readfirstlane_b32 s0, v186
	v_mfma_f32_32x32x16_bf16 v[114:129], v[130:133], v[142:145], v[114:129]
	v_lshl_add_u64 v[130:131], v[180:181], 0, s[2:3]
	s_mov_b32 m0, s0
	s_waitcnt vmcnt(4) lgkmcnt(0)
	s_barrier
	global_load_lds_dwordx4 v[130:131], off
	global_load_lds_dwordx4 v[130:131], off offset:1024
	global_load_lds_dwordx4 v[130:131], off offset:2048
	global_load_lds_dwordx4 v[130:131], off offset:3072
	v_mfma_f32_32x32x16_bf16 v[98:113], v[188:191], v[142:145], v[98:113]
	ds_read_b128 v[130:133], v176 offset:20480
	ds_read_b128 v[134:137], v176 offset:21504
	ds_read_b128 v[138:141], v176 offset:22528
	ds_read_b128 v[166:169], v176 offset:23552
	ds_read_b128 v[170:173], v176 offset:24576
	ds_read_b128 v[180:183], v176 offset:25600
	ds_read_b128 v[184:187], v176 offset:26624
	ds_read_b128 v[188:191], v176 offset:27648
	v_mfma_f32_32x32x16_bf16 v[82:97], v[192:195], v[142:145], v[82:97]
	v_mfma_f32_32x32x16_bf16 v[66:81], v[196:199], v[142:145], v[66:81]
	s_waitcnt lgkmcnt(0)
	v_mfma_f32_32x32x16_bf16 v[114:129], v[130:133], v[146:149], v[114:129]
	v_mfma_f32_32x32x16_bf16 v[98:113], v[134:137], v[146:149], v[98:113]
	v_mfma_f32_32x32x16_bf16 v[82:97], v[138:141], v[146:149], v[82:97]
	ds_read_b128 v[130:133], v176 offset:28672
	ds_read_b128 v[134:137], v176 offset:29696
	ds_read_b128 v[138:141], v176 offset:30720
	ds_read_b128 v[142:145], v176 offset:31744
	v_mfma_f32_32x32x16_bf16 v[66:81], v[166:169], v[146:149], v[66:81]
	v_mfma_f32_32x32x16_bf16 v[114:129], v[170:173], v[150:153], v[114:129]
	v_mfma_f32_32x32x16_bf16 v[98:113], v[180:183], v[150:153], v[98:113]
	ds_read_b128 v[146:149], v176 offset:32768
	ds_read_b128 v[166:169], v176 offset:33792
	ds_read_b128 v[170:173], v176 offset:34816
	ds_read_b128 v[180:183], v176 offset:35840
	v_mfma_f32_32x32x16_bf16 v[82:97], v[184:187], v[150:153], v[82:97]
	v_mfma_f32_32x32x16_bf16 v[66:81], v[188:191], v[150:153], v[66:81]
	s_waitcnt lgkmcnt(0)
	v_mfma_f32_32x32x16_bf16 v[114:129], v[130:133], v[156:159], v[114:129]
	v_mfma_f32_32x32x16_bf16 v[98:113], v[134:137], v[156:159], v[98:113]
	v_mfma_f32_32x32x16_bf16 v[82:97], v[138:141], v[156:159], v[82:97]
	v_mfma_f32_32x32x16_bf16 v[66:81], v[142:145], v[156:159], v[66:81]
	v_mfma_f32_32x32x16_bf16 v[114:129], v[146:149], v[208:211], v[114:129]
	s_waitcnt vmcnt(4) lgkmcnt(0)
	s_barrier
	v_mfma_f32_32x32x16_bf16 v[98:113], v[166:169], v[208:211], v[98:113]
	s_nop 8
	v_mul_f32_e32 v130, 0x3c23d70a, v114
	v_max_f32_e32 v114, v114, v114
	v_mul_f32_e32 v131, 0x3c23d70a, v115
	v_max_f32_e32 v115, v115, v115
	v_max_f32_e32 v114, v114, v130
	v_mul_f32_e32 v130, 0x3c23d70a, v116
	v_max_f32_e32 v116, v116, v116
	v_max_f32_e32 v115, v115, v131
	v_max_f32_e32 v116, v116, v130
	v_mul_f32_e32 v130, 0x3c23d70a, v117
	v_max_f32_e32 v117, v117, v117
	v_max_f32_e32 v117, v117, v130
	v_cvt_pk_bf16_f32 v134, v114, v115
	v_mul_f32_e32 v114, 0x3c23d70a, v122
	v_max_f32_e32 v115, v122, v122
	v_cvt_pk_bf16_f32 v135, v116, v117
	v_max_f32_e32 v114, v115, v114
	v_mul_f32_e32 v115, 0x3c23d70a, v123
	v_max_f32_e32 v116, v123, v123
	v_mfma_f32_32x32x16_bf16 v[82:97], v[170:173], v[208:211], v[82:97]
	v_max_f32_e32 v115, v116, v115
	v_cvt_pk_bf16_f32 v138, v114, v115
	v_mul_f32_e32 v114, 0x3c23d70a, v98
	v_max_f32_e32 v98, v98, v98
	v_max_f32_e32 v98, v98, v114
	v_mul_f32_e32 v114, 0x3c23d70a, v99
	v_max_f32_e32 v99, v99, v99
	v_max_f32_e32 v99, v99, v114
	v_mul_f32_e32 v114, 0x3c23d70a, v100
	v_max_f32_e32 v100, v100, v100
	v_max_f32_e32 v100, v100, v114
	v_mul_f32_e32 v114, 0x3c23d70a, v101
	v_max_f32_e32 v101, v101, v101
	v_max_f32_e32 v101, v101, v114
	v_cvt_pk_bf16_f32 v142, v98, v99
	v_mul_f32_e32 v98, 0x3c23d70a, v106
	v_max_f32_e32 v99, v106, v106
	v_cvt_pk_bf16_f32 v143, v100, v101
	v_max_f32_e32 v98, v99, v98
	v_mul_f32_e32 v99, 0x3c23d70a, v107
	v_max_f32_e32 v100, v107, v107
	v_mfma_f32_32x32x16_bf16 v[66:81], v[180:183], v[208:211], v[66:81]
	v_max_f32_e32 v99, v100, v99
	v_cvt_pk_bf16_f32 v146, v98, v99
	v_mul_f32_e32 v98, 0x3c23d70a, v82
	v_max_f32_e32 v82, v82, v82
	v_max_f32_e32 v82, v82, v98
	v_mul_f32_e32 v98, 0x3c23d70a, v83
	v_max_f32_e32 v83, v83, v83
	v_max_f32_e32 v83, v83, v98
	v_mul_f32_e32 v98, 0x3c23d70a, v84
	v_max_f32_e32 v84, v84, v84
	v_max_f32_e32 v84, v84, v98
	v_mul_f32_e32 v98, 0x3c23d70a, v85
	v_max_f32_e32 v85, v85, v85
	v_max_f32_e32 v85, v85, v98
	v_cvt_pk_bf16_f32 v150, v82, v83
	v_mul_f32_e32 v82, 0x3c23d70a, v90
	v_max_f32_e32 v83, v90, v90
	v_cvt_pk_bf16_f32 v151, v84, v85
	v_max_f32_e32 v82, v83, v82
	v_mul_f32_e32 v83, 0x3c23d70a, v91
	v_max_f32_e32 v84, v91, v91
	v_max_f32_e32 v83, v84, v83
	v_mul_f32_e32 v130, 0x3c23d70a, v118
	v_max_f32_e32 v118, v118, v118
	v_cvt_pk_bf16_f32 v156, v82, v83
	v_mul_f32_e32 v82, 0x3c23d70a, v66
	v_max_f32_e32 v66, v66, v66
	v_max_f32_e32 v118, v118, v130
	v_mul_f32_e32 v130, 0x3c23d70a, v119
	v_max_f32_e32 v119, v119, v119
	v_max_f32_e32 v66, v66, v82
	v_mul_f32_e32 v82, 0x3c23d70a, v67
	v_max_f32_e32 v67, v67, v67
	v_max_f32_e32 v119, v119, v130
	v_mul_f32_e32 v130, 0x3c23d70a, v120
	v_max_f32_e32 v120, v120, v120
	v_mul_f32_e32 v114, 0x3c23d70a, v102
	v_max_f32_e32 v102, v102, v102
	v_mul_f32_e32 v98, 0x3c23d70a, v86
	v_max_f32_e32 v86, v86, v86
	v_max_f32_e32 v67, v67, v82
	v_max_f32_e32 v120, v120, v130
	v_mul_f32_e32 v130, 0x3c23d70a, v121
	v_max_f32_e32 v121, v121, v121
	v_max_f32_e32 v102, v102, v114
	v_mul_f32_e32 v114, 0x3c23d70a, v103
	v_max_f32_e32 v103, v103, v103
	v_max_f32_e32 v86, v86, v98
	v_mul_f32_e32 v98, 0x3c23d70a, v87
	v_max_f32_e32 v87, v87, v87
	v_cvt_pk_bf16_f32 v166, v66, v67
	v_mul_f32_e32 v66, 0x3c23d70a, v74
	v_max_f32_e32 v67, v74, v74
	v_max_f32_e32 v121, v121, v130
	v_mul_f32_e32 v116, 0x3c23d70a, v124
	v_max_f32_e32 v117, v124, v124
	v_max_f32_e32 v103, v103, v114
	v_mul_f32_e32 v114, 0x3c23d70a, v104
	v_max_f32_e32 v104, v104, v104
	v_mul_f32_e32 v100, 0x3c23d70a, v108
	v_max_f32_e32 v101, v108, v108
	v_max_f32_e32 v87, v87, v98
	v_mul_f32_e32 v98, 0x3c23d70a, v88
	v_max_f32_e32 v88, v88, v88
	v_mul_f32_e32 v84, 0x3c23d70a, v92
	v_max_f32_e32 v85, v92, v92
	v_mul_f32_e32 v82, 0x3c23d70a, v68
	v_max_f32_e32 v68, v68, v68
	v_max_f32_e32 v130, v67, v66
	v_mul_f32_e32 v66, 0x3c23d70a, v75
	v_max_f32_e32 v67, v75, v75
	v_cvt_pk_bf16_f32 v136, v118, v119
	v_max_f32_e32 v116, v117, v116
	v_mul_f32_e32 v117, 0x3c23d70a, v125
	v_max_f32_e32 v118, v125, v125
	v_max_f32_e32 v104, v104, v114
	v_mul_f32_e32 v114, 0x3c23d70a, v105
	v_max_f32_e32 v105, v105, v105
	v_cvt_pk_bf16_f32 v144, v102, v103
	v_max_f32_e32 v100, v101, v100
	v_mul_f32_e32 v101, 0x3c23d70a, v109
	v_max_f32_e32 v102, v109, v109
	v_max_f32_e32 v88, v88, v98
	v_mul_f32_e32 v98, 0x3c23d70a, v89
	v_max_f32_e32 v89, v89, v89
	v_cvt_pk_bf16_f32 v152, v86, v87
	v_max_f32_e32 v84, v85, v84
	v_mul_f32_e32 v85, 0x3c23d70a, v93
	v_max_f32_e32 v86, v93, v93
	v_max_f32_e32 v68, v68, v82
	v_mul_f32_e32 v82, 0x3c23d70a, v69
	v_max_f32_e32 v69, v69, v69
	v_max_f32_e32 v155, v67, v66
	v_mul_f32_e32 v66, 0x3c23d70a, v76
	v_max_f32_e32 v67, v76, v76
	v_max_f32_e32 v117, v118, v117
	v_mul_f32_e32 v118, 0x3c23d70a, v126
	v_max_f32_e32 v119, v126, v126
	v_max_f32_e32 v105, v105, v114
	v_max_f32_e32 v101, v102, v101
	v_mul_f32_e32 v102, 0x3c23d70a, v110
	v_max_f32_e32 v103, v110, v110
	v_max_f32_e32 v89, v89, v98
	v_max_f32_e32 v85, v86, v85
	v_mul_f32_e32 v86, 0x3c23d70a, v94
	v_max_f32_e32 v87, v94, v94
	v_max_f32_e32 v69, v69, v82
	v_mul_f32_e32 v82, 0x3c23d70a, v70
	v_max_f32_e32 v70, v70, v70
	v_max_f32_e32 v131, v67, v66
	v_mul_f32_e32 v66, 0x3c23d70a, v77
	v_max_f32_e32 v67, v77, v77
	v_cvt_pk_bf16_f32 v137, v120, v121
	v_max_f32_e32 v118, v119, v118
	v_mul_f32_e32 v119, 0x3c23d70a, v127
	v_max_f32_e32 v120, v127, v127
	v_cvt_pk_bf16_f32 v145, v104, v105
	v_max_f32_e32 v102, v103, v102
	v_mul_f32_e32 v103, 0x3c23d70a, v111
	v_max_f32_e32 v104, v111, v111
	v_cvt_pk_bf16_f32 v153, v88, v89
	v_max_f32_e32 v86, v87, v86
	v_mul_f32_e32 v87, 0x3c23d70a, v95
	v_max_f32_e32 v88, v95, v95
	v_max_f32_e32 v70, v70, v82
	v_mul_f32_e32 v82, 0x3c23d70a, v71
	v_max_f32_e32 v71, v71, v71
	v_max_f32_e32 v162, v67, v66
	v_mul_f32_e32 v66, 0x3c23d70a, v78
	v_max_f32_e32 v67, v78, v78
	v_max_f32_e32 v119, v120, v119
	v_mul_f32_e32 v120, 0x3c23d70a, v128
	v_max_f32_e32 v121, v128, v128
	v_max_f32_e32 v103, v104, v103
	v_mul_f32_e32 v104, 0x3c23d70a, v112
	v_max_f32_e32 v105, v112, v112
	v_max_f32_e32 v87, v88, v87
	v_mul_f32_e32 v88, 0x3c23d70a, v96
	v_max_f32_e32 v89, v96, v96
	v_max_f32_e32 v71, v71, v82
	v_mul_f32_e32 v82, 0x3c23d70a, v72
	v_max_f32_e32 v72, v72, v72
	v_max_f32_e32 v132, v67, v66
	v_mul_f32_e32 v66, 0x3c23d70a, v79
	v_max_f32_e32 v67, v79, v79
	v_max_f32_e32 v120, v121, v120
	v_mul_f32_e32 v121, 0x3c23d70a, v129
	v_max_f32_e32 v122, v129, v129
	v_max_f32_e32 v104, v105, v104
	v_mul_f32_e32 v105, 0x3c23d70a, v113
	v_max_f32_e32 v106, v113, v113
	v_max_f32_e32 v88, v89, v88
	v_mul_f32_e32 v89, 0x3c23d70a, v97
	v_max_f32_e32 v90, v97, v97
	v_max_f32_e32 v72, v72, v82
	v_mul_f32_e32 v82, 0x3c23d70a, v73
	v_max_f32_e32 v73, v73, v73
	v_max_f32_e32 v174, v67, v66
	v_mul_f32_e32 v66, 0x3c23d70a, v80
	v_max_f32_e32 v67, v80, v80
	v_max_f32_e32 v121, v122, v121
	v_max_f32_e32 v105, v106, v105
	v_max_f32_e32 v89, v90, v89
	v_max_f32_e32 v73, v73, v82
	v_max_f32_e32 v133, v67, v66
	v_mul_f32_e32 v66, 0x3c23d70a, v81
	v_max_f32_e32 v67, v81, v81
	v_cvt_pk_bf16_f32 v141, v120, v121
	v_cvt_pk_bf16_f32 v140, v118, v119
	v_cvt_pk_bf16_f32 v139, v116, v117
	v_cvt_pk_bf16_f32 v149, v104, v105
	v_cvt_pk_bf16_f32 v148, v102, v103
	v_cvt_pk_bf16_f32 v147, v100, v101
	v_cvt_pk_bf16_f32 v159, v88, v89
	v_cvt_pk_bf16_f32 v158, v86, v87
	v_cvt_pk_bf16_f32 v157, v84, v85
	v_cvt_pk_bf16_f32 v169, v72, v73
	v_cvt_pk_bf16_f32 v168, v70, v71
	v_cvt_pk_bf16_f32 v167, v68, v69
	v_max_f32_e32 v177, v67, v66
	ds_read_b128 v[114:117], v154 offset:59392
	ds_read_b128 v[118:121], v154 offset:59424
	ds_read_b128 v[122:125], v154 offset:59456
	ds_read_b128 v[126:129], v154 offset:59488
	ds_read_b128 v[98:101], v154 offset:59520
	ds_read_b128 v[102:105], v154 offset:59552
	ds_read_b128 v[106:109], v154 offset:59584
	ds_read_b128 v[110:113], v154 offset:59616
	ds_read_b128 v[82:85], v154 offset:59648
	ds_read_b128 v[86:89], v154 offset:59680
	ds_read_b128 v[90:93], v154 offset:59712
	ds_read_b128 v[94:97], v154 offset:59744
	ds_read_b128 v[66:69], v154 offset:59776
	ds_read_b128 v[70:73], v154 offset:59808
	ds_read_b128 v[74:77], v154 offset:59840
	ds_read_b128 v[78:81], v154 offset:59872
	ds_read_b128 v[170:173], v176 offset:40960
	ds_read_b128 v[180:183], v176 offset:41984
	ds_read_b128 v[184:187], v176 offset:43008
	ds_read_b128 v[188:191], v176 offset:44032
	ds_read_b128 v[192:195], v176 offset:45056
	ds_read_b128 v[196:199], v176 offset:46080
	ds_read_b128 v[200:203], v176 offset:47104
	ds_read_b128 v[204:207], v176 offset:48128
	v_cvt_pk_bf16_f32 v133, v133, v177
	v_cvt_pk_bf16_f32 v132, v132, v174
	v_cvt_pk_bf16_f32 v131, v131, v162
	v_cvt_pk_bf16_f32 v130, v130, v155
	s_waitcnt lgkmcnt(0)
	v_mfma_f32_32x32x16_bf16 v[114:129], v[170:173], v[134:137], v[114:129]
	v_mfma_f32_32x32x16_bf16 v[98:113], v[180:183], v[134:137], v[98:113]
	v_mfma_f32_32x32x16_bf16 v[82:97], v[184:187], v[134:137], v[82:97]
	ds_read_b128 v[170:173], v176 offset:49152
	ds_read_b128 v[180:183], v176 offset:50176
	ds_read_b128 v[184:187], v176 offset:51200
	ds_read_b128 v[208:211], v176 offset:52224
	v_mfma_f32_32x32x16_bf16 v[66:81], v[188:191], v[134:137], v[66:81]
	v_mfma_f32_32x32x16_bf16 v[114:129], v[192:195], v[138:141], v[114:129]
	v_mfma_f32_32x32x16_bf16 v[98:113], v[196:199], v[138:141], v[98:113]
	ds_read_b128 v[134:137], v176 offset:53248
	ds_read_b128 v[188:191], v176 offset:54272
	ds_read_b128 v[192:195], v176 offset:55296
	ds_read_b128 v[196:199], v176 offset:56320
	v_mfma_f32_32x32x16_bf16 v[82:97], v[200:203], v[138:141], v[82:97]
	v_mfma_f32_32x32x16_bf16 v[66:81], v[204:207], v[138:141], v[66:81]
	s_waitcnt lgkmcnt(0)
	v_mfma_f32_32x32x16_bf16 v[114:129], v[170:173], v[142:145], v[114:129]
	v_mfma_f32_32x32x16_bf16 v[98:113], v[180:183], v[142:145], v[98:113]
	v_mfma_f32_32x32x16_bf16 v[82:97], v[184:187], v[142:145], v[82:97]
	v_mfma_f32_32x32x16_bf16 v[66:81], v[208:211], v[142:145], v[66:81]
	v_mfma_f32_32x32x16_bf16 v[114:129], v[134:137], v[146:149], v[114:129]
	s_waitcnt vmcnt(0) lgkmcnt(0)
	s_barrier
	v_mfma_f32_32x32x16_bf16 v[98:113], v[188:191], v[146:149], v[98:113]
	v_mfma_f32_32x32x16_bf16 v[82:97], v[192:195], v[146:149], v[82:97]
	ds_read_b128 v[134:137], v176
	ds_read_b128 v[138:141], v176 offset:1024
	ds_read_b128 v[142:145], v176 offset:2048
	ds_read_b128 v[170:173], v176 offset:3072
	ds_read_b128 v[180:183], v176 offset:4096
	ds_read_b128 v[184:187], v176 offset:5120
	ds_read_b128 v[188:191], v176 offset:6144
	ds_read_b128 v[192:195], v176 offset:7168
	v_mfma_f32_32x32x16_bf16 v[66:81], v[196:199], v[146:149], v[66:81]
	s_waitcnt lgkmcnt(5)
	v_mfma_f32_32x32x16_bf16 v[82:97], v[142:145], v[150:153], v[82:97]
	ds_read_b128 v[142:145], v176 offset:8192
	ds_read_b128 v[146:149], v176 offset:9216
	ds_read_b128 v[196:199], v176 offset:10240
	ds_read_b128 v[200:203], v176 offset:11264
	v_mfma_f32_32x32x16_bf16 v[114:129], v[134:137], v[150:153], v[114:129]
	v_mfma_f32_32x32x16_bf16 v[98:113], v[138:141], v[150:153], v[98:113]
	s_waitcnt lgkmcnt(8)
	v_mfma_f32_32x32x16_bf16 v[66:81], v[170:173], v[150:153], v[66:81]
	ds_read_b128 v[150:153], v176 offset:12288
	ds_read_b128 v[170:173], v176 offset:13312
	ds_read_b128 v[138:141], v176 offset:14336
	ds_read_b128 v[134:137], v176 offset:15360
	s_waitcnt lgkmcnt(11)
	v_mfma_f32_32x32x16_bf16 v[114:129], v[180:183], v[156:159], v[114:129]
	s_waitcnt lgkmcnt(10)
	v_mfma_f32_32x32x16_bf16 v[98:113], v[184:187], v[156:159], v[98:113]
	s_waitcnt lgkmcnt(9)
	v_mfma_f32_32x32x16_bf16 v[82:97], v[188:191], v[156:159], v[82:97]
	s_waitcnt lgkmcnt(8)
	v_mfma_f32_32x32x16_bf16 v[66:81], v[192:195], v[156:159], v[66:81]
	s_waitcnt lgkmcnt(7)
	v_mfma_f32_32x32x16_bf16 v[114:129], v[142:145], v[166:169], v[114:129]
	s_waitcnt lgkmcnt(6)
	v_mfma_f32_32x32x16_bf16 v[98:113], v[146:149], v[166:169], v[98:113]
	s_waitcnt lgkmcnt(5)
	v_mfma_f32_32x32x16_bf16 v[82:97], v[196:199], v[166:169], v[82:97]
	s_waitcnt lgkmcnt(4)
	v_mfma_f32_32x32x16_bf16 v[66:81], v[200:203], v[166:169], v[66:81]
	s_waitcnt lgkmcnt(3)
	v_mfma_f32_32x32x16_bf16 v[114:129], v[150:153], v[130:133], v[114:129]
	v_and_b32_e32 v0, 7, v0
	v_lshlrev_b32_e32 v174, 4, v0
	v_or_b32_e32 v144, v1, v174
	v_mad_u32_u24 v145, v161, s1, v144
	v_lshl_add_u64 v[142:143], s[6:7], 0, v[178:179]
	s_nop 6
	v_mul_f32_e32 v0, 0x3c23d70a, v114
	v_max_f32_e32 v1, v114, v114
	v_max_f32_e32 v0, v1, v0
	v_mul_f32_e32 v1, 0x3c23d70a, v115
	v_max_f32_e32 v114, v115, v115
	v_max_f32_e32 v1, v114, v1
	v_pk_add_f32 v[50:51], v[50:51], v[0:1]
	v_mul_f32_e32 v0, 0x3c23d70a, v116
	v_max_f32_e32 v1, v116, v116
	v_max_f32_e32 v0, v1, v0
	v_mul_f32_e32 v1, 0x3c23d70a, v117
	v_max_f32_e32 v114, v117, v117
	v_max_f32_e32 v1, v114, v1
	v_pk_add_f32 v[52:53], v[52:53], v[0:1]
	v_mul_f32_e32 v0, 0x3c23d70a, v118
	v_max_f32_e32 v1, v118, v118
	ds_write_b128 v160, v[50:53] offset:61440
	v_max_f32_e32 v0, v1, v0
	v_mul_f32_e32 v1, 0x3c23d70a, v119
	v_max_f32_e32 v50, v119, v119
	v_max_f32_e32 v1, v50, v1
	v_pk_add_f32 v[50:51], v[54:55], v[0:1]
	v_mul_f32_e32 v0, 0x3c23d70a, v120
	v_max_f32_e32 v1, v120, v120
	v_max_f32_e32 v0, v1, v0
	v_mul_f32_e32 v1, 0x3c23d70a, v121
	v_max_f32_e32 v52, v121, v121
	v_max_f32_e32 v1, v52, v1
	v_pk_add_f32 v[52:53], v[56:57], v[0:1]
	v_mul_f32_e32 v0, 0x3c23d70a, v122
	v_max_f32_e32 v1, v122, v122
	ds_write_b128 v160, v[50:53] offset:61472
	v_max_f32_e32 v0, v1, v0
	v_mul_f32_e32 v1, 0x3c23d70a, v123
	v_max_f32_e32 v50, v123, v123
	v_max_f32_e32 v1, v50, v1
	v_pk_add_f32 v[50:51], v[58:59], v[0:1]
	v_mul_f32_e32 v0, 0x3c23d70a, v124
	v_max_f32_e32 v1, v124, v124
	v_max_f32_e32 v0, v1, v0
	v_mul_f32_e32 v1, 0x3c23d70a, v125
	v_max_f32_e32 v52, v125, v125
	v_max_f32_e32 v1, v52, v1
	v_pk_add_f32 v[52:53], v[60:61], v[0:1]
	v_mul_f32_e32 v0, 0x3c23d70a, v126
	v_max_f32_e32 v1, v126, v126
	ds_write_b128 v160, v[50:53] offset:61504
	v_max_f32_e32 v0, v1, v0
	v_mul_f32_e32 v1, 0x3c23d70a, v127
	v_max_f32_e32 v50, v127, v127
	v_max_f32_e32 v1, v50, v1
	v_pk_add_f32 v[50:51], v[62:63], v[0:1]
	v_mul_f32_e32 v0, 0x3c23d70a, v128
	v_max_f32_e32 v1, v128, v128
	v_max_f32_e32 v0, v1, v0
	v_mul_f32_e32 v1, 0x3c23d70a, v129
	v_max_f32_e32 v52, v129, v129
	v_max_f32_e32 v1, v52, v1
	v_pk_add_f32 v[52:53], v[64:65], v[0:1]
	ds_write_b128 v160, v[50:53] offset:61536
	ds_read_b128 v[50:53], v145 offset:61440
	v_add_u32_e32 v62, v144, v165
	ds_read_b128 v[54:57], v62 offset:61440
	v_lshl_add_u64 v[142:143], v[142:143], 0, v[174:175]
	v_lshlrev_b32_e32 v174, 9, v161
	s_waitcnt lgkmcnt(8)
	v_mfma_f32_32x32x16_bf16 v[98:113], v[170:173], v[130:133], v[98:113]
	v_lshl_add_u64 v[0:1], v[142:143], 0, v[174:175]
	s_waitcnt lgkmcnt(1)
	global_store_dwordx4 v[0:1], v[50:53], off nt
	v_add_u32_e32 v63, v144, v164
	v_add_u32_e32 v64, v144, v163
	v_or_b32_e32 v50, 0x1000, v174
	v_mov_b32_e32 v51, v175
	v_lshl_add_u64 v[50:51], v[142:143], 0, v[50:51]
	ds_read_b128 v[58:61], v64 offset:61440
	s_waitcnt lgkmcnt(1)
	global_store_dwordx4 v[50:51], v[54:57], off nt
	ds_read_b128 v[54:57], v63 offset:61440
	v_or_b32_e32 v52, 0x2000, v174
	v_mov_b32_e32 v53, v175
	v_lshl_add_u64 v[52:53], v[142:143], 0, v[52:53]
	v_or_b32_e32 v174, 0x3000, v174
	s_waitcnt lgkmcnt(0)
	global_store_dwordx4 v[52:53], v[54:57], off nt
	v_mfma_f32_32x32x16_bf16 v[82:97], v[138:141], v[130:133], v[82:97]
	s_nop 0
	v_lshl_add_u64 v[54:55], v[142:143], 0, v[174:175]
	v_mul_f32_e32 v56, 0x3c23d70a, v98
	v_max_f32_e32 v57, v98, v98
	global_store_dwordx4 v[54:55], v[58:61], off nt
	v_max_f32_e32 v56, v57, v56
	v_mul_f32_e32 v57, 0x3c23d70a, v99
	v_max_f32_e32 v58, v99, v99
	v_max_f32_e32 v57, v58, v57
	v_pk_add_f32 v[34:35], v[34:35], v[56:57]
	v_mul_f32_e32 v56, 0x3c23d70a, v100
	v_max_f32_e32 v57, v100, v100
	v_max_f32_e32 v56, v57, v56
	v_mul_f32_e32 v57, 0x3c23d70a, v101
	v_max_f32_e32 v58, v101, v101
	v_max_f32_e32 v57, v58, v57
	v_pk_add_f32 v[36:37], v[36:37], v[56:57]
	ds_write_b128 v160, v[34:37] offset:61440
	v_mul_f32_e32 v34, 0x3c23d70a, v102
	v_max_f32_e32 v35, v102, v102
	v_max_f32_e32 v34, v35, v34
	v_mul_f32_e32 v35, 0x3c23d70a, v103
	v_max_f32_e32 v36, v103, v103
	v_max_f32_e32 v35, v36, v35
	v_mul_f32_e32 v36, 0x3c23d70a, v104
	v_max_f32_e32 v37, v104, v104
	v_pk_add_f32 v[34:35], v[38:39], v[34:35]
	v_max_f32_e32 v36, v37, v36
	v_mul_f32_e32 v37, 0x3c23d70a, v105
	v_max_f32_e32 v38, v105, v105
	v_max_f32_e32 v37, v38, v37
	v_pk_add_f32 v[36:37], v[40:41], v[36:37]
	ds_write_b128 v160, v[34:37] offset:61472
	v_mul_f32_e32 v34, 0x3c23d70a, v106
	v_max_f32_e32 v35, v106, v106
	v_max_f32_e32 v34, v35, v34
	v_mul_f32_e32 v35, 0x3c23d70a, v107
	v_max_f32_e32 v36, v107, v107
	v_max_f32_e32 v35, v36, v35
	v_mul_f32_e32 v36, 0x3c23d70a, v108
	v_max_f32_e32 v37, v108, v108
	v_max_f32_e32 v36, v37, v36
	v_mul_f32_e32 v37, 0x3c23d70a, v109
	v_max_f32_e32 v38, v109, v109
	v_max_f32_e32 v37, v38, v37
	v_pk_add_f32 v[34:35], v[42:43], v[34:35]
	v_pk_add_f32 v[36:37], v[44:45], v[36:37]
	ds_write_b128 v160, v[34:37] offset:61504
	v_mul_f32_e32 v34, 0x3c23d70a, v110
	v_max_f32_e32 v35, v110, v110
	v_max_f32_e32 v34, v35, v34
	v_mul_f32_e32 v35, 0x3c23d70a, v111
	v_max_f32_e32 v36, v111, v111
	v_max_f32_e32 v35, v36, v35
	v_mul_f32_e32 v36, 0x3c23d70a, v112
	v_max_f32_e32 v37, v112, v112
	v_max_f32_e32 v36, v37, v36
	v_mul_f32_e32 v37, 0x3c23d70a, v113
	v_max_f32_e32 v38, v113, v113
	v_max_f32_e32 v37, v38, v37
	v_pk_add_f32 v[34:35], v[46:47], v[34:35]
	v_pk_add_f32 v[36:37], v[48:49], v[36:37]
	ds_write_b128 v160, v[34:37] offset:61536
	ds_read_b128 v[34:37], v145 offset:61440
	ds_read_b128 v[38:41], v62 offset:61440
	ds_read_b128 v[42:45], v63 offset:61440
	ds_read_b128 v[46:49], v64 offset:61440
	s_waitcnt lgkmcnt(3)
	global_store_dwordx4 v[0:1], v[34:37], off offset:128 nt
	s_waitcnt lgkmcnt(2)
	global_store_dwordx4 v[50:51], v[38:41], off offset:128 nt
	s_waitcnt lgkmcnt(1)
	global_store_dwordx4 v[52:53], v[42:45], off offset:128 nt
	s_waitcnt lgkmcnt(0)
	global_store_dwordx4 v[54:55], v[46:49], off offset:128 nt
	v_mul_f32_e32 v34, 0x3c23d70a, v82
	v_max_f32_e32 v35, v82, v82
	v_max_f32_e32 v34, v35, v34
	v_mul_f32_e32 v35, 0x3c23d70a, v83
	v_max_f32_e32 v36, v83, v83
	v_max_f32_e32 v35, v36, v35
	v_pk_add_f32 v[18:19], v[18:19], v[34:35]
	v_mul_f32_e32 v34, 0x3c23d70a, v84
	v_max_f32_e32 v35, v84, v84
	v_max_f32_e32 v34, v35, v34
	v_mul_f32_e32 v35, 0x3c23d70a, v85
	v_max_f32_e32 v36, v85, v85
	v_max_f32_e32 v35, v36, v35
	v_pk_add_f32 v[20:21], v[20:21], v[34:35]
	ds_write_b128 v160, v[18:21] offset:61440
	v_mul_f32_e32 v18, 0x3c23d70a, v86
	v_max_f32_e32 v19, v86, v86
	v_max_f32_e32 v18, v19, v18
	v_mul_f32_e32 v19, 0x3c23d70a, v87
	v_max_f32_e32 v20, v87, v87
	v_max_f32_e32 v19, v20, v19
	v_mul_f32_e32 v20, 0x3c23d70a, v88
	v_max_f32_e32 v21, v88, v88
	v_pk_add_f32 v[18:19], v[22:23], v[18:19]
	v_max_f32_e32 v20, v21, v20
	v_mul_f32_e32 v21, 0x3c23d70a, v89
	v_max_f32_e32 v22, v89, v89
	v_max_f32_e32 v21, v22, v21
	v_pk_add_f32 v[20:21], v[24:25], v[20:21]
	ds_write_b128 v160, v[18:21] offset:61472
	v_mul_f32_e32 v18, 0x3c23d70a, v90
	v_max_f32_e32 v19, v90, v90
	v_max_f32_e32 v18, v19, v18
	v_mul_f32_e32 v19, 0x3c23d70a, v91
	v_max_f32_e32 v20, v91, v91
	v_max_f32_e32 v19, v20, v19
	v_mul_f32_e32 v20, 0x3c23d70a, v92
	v_max_f32_e32 v21, v92, v92
	v_max_f32_e32 v20, v21, v20
	v_mul_f32_e32 v21, 0x3c23d70a, v93
	v_max_f32_e32 v22, v93, v93
	v_max_f32_e32 v21, v22, v21
	v_pk_add_f32 v[18:19], v[26:27], v[18:19]
	v_pk_add_f32 v[20:21], v[28:29], v[20:21]
	ds_write_b128 v160, v[18:21] offset:61504
	v_mul_f32_e32 v18, 0x3c23d70a, v94
	v_max_f32_e32 v19, v94, v94
	v_max_f32_e32 v18, v19, v18
	v_mul_f32_e32 v19, 0x3c23d70a, v95
	v_max_f32_e32 v20, v95, v95
	v_max_f32_e32 v19, v20, v19
	v_mul_f32_e32 v20, 0x3c23d70a, v96
	v_max_f32_e32 v21, v96, v96
	v_max_f32_e32 v20, v21, v20
	v_mul_f32_e32 v21, 0x3c23d70a, v97
	v_max_f32_e32 v22, v97, v97
	v_mfma_f32_32x32x16_bf16 v[66:81], v[134:137], v[130:133], v[66:81]
	v_max_f32_e32 v21, v22, v21
	v_add_f32_e64 v18, v30, v18
	v_add_f32_e64 v19, v31, v19
	v_add_f32_e64 v20, v32, v20
	v_add_f32_e64 v21, v33, v21
	ds_write_b128 v160, v[18:21] offset:61536
	ds_read_b128 v[18:21], v145 offset:61440
	ds_read_b128 v[22:25], v62 offset:61440
	ds_read_b128 v[26:29], v63 offset:61440
	ds_read_b128 v[30:33], v64 offset:61440
	s_waitcnt lgkmcnt(3)
	global_store_dwordx4 v[0:1], v[18:21], off offset:256 nt
	s_waitcnt lgkmcnt(2)
	global_store_dwordx4 v[50:51], v[22:25], off offset:256 nt
	s_waitcnt lgkmcnt(1)
	global_store_dwordx4 v[52:53], v[26:29], off offset:256 nt
	s_waitcnt lgkmcnt(0)
	global_store_dwordx4 v[54:55], v[30:33], off offset:256 nt
	v_mul_f32_e32 v18, 0x3c23d70a, v66
	v_max_f32_e32 v19, v66, v66
	v_max_f32_e32 v18, v19, v18
	v_mul_f32_e32 v19, 0x3c23d70a, v67
	v_max_f32_e32 v20, v67, v67
	v_max_f32_e32 v19, v20, v19
	v_pk_add_f32 v[2:3], v[2:3], v[18:19]
	v_mul_f32_e32 v18, 0x3c23d70a, v68
	v_max_f32_e32 v19, v68, v68
	v_max_f32_e32 v18, v19, v18
	v_mul_f32_e32 v19, 0x3c23d70a, v69
	v_max_f32_e32 v20, v69, v69
	v_max_f32_e32 v19, v20, v19
	v_pk_add_f32 v[4:5], v[4:5], v[18:19]
	ds_write_b128 v160, v[2:5] offset:61440
	v_mul_f32_e32 v2, 0x3c23d70a, v70
	v_max_f32_e32 v3, v70, v70
	v_max_f32_e32 v2, v3, v2
	v_mul_f32_e32 v3, 0x3c23d70a, v71
	v_max_f32_e32 v4, v71, v71
	v_max_f32_e32 v3, v4, v3
	v_mul_f32_e32 v4, 0x3c23d70a, v72
	v_max_f32_e32 v5, v72, v72
	v_pk_add_f32 v[2:3], v[6:7], v[2:3]
	v_max_f32_e32 v4, v5, v4
	v_mul_f32_e32 v5, 0x3c23d70a, v73
	v_max_f32_e32 v6, v73, v73
	v_max_f32_e32 v5, v6, v5
	v_pk_add_f32 v[4:5], v[8:9], v[4:5]
	ds_write_b128 v160, v[2:5] offset:61472
	v_mul_f32_e32 v2, 0x3c23d70a, v74
	v_max_f32_e32 v3, v74, v74
	v_max_f32_e32 v2, v3, v2
	v_mul_f32_e32 v3, 0x3c23d70a, v75
	v_max_f32_e32 v4, v75, v75
	v_max_f32_e32 v3, v4, v3
	v_mul_f32_e32 v4, 0x3c23d70a, v76
	v_max_f32_e32 v5, v76, v76
	v_max_f32_e32 v4, v5, v4
	v_mul_f32_e32 v5, 0x3c23d70a, v77
	v_max_f32_e32 v6, v77, v77
	v_max_f32_e32 v5, v6, v5
	v_pk_add_f32 v[2:3], v[10:11], v[2:3]
	v_pk_add_f32 v[4:5], v[12:13], v[4:5]
	ds_write_b128 v160, v[2:5] offset:61504
	v_mul_f32_e32 v2, 0x3c23d70a, v78
	v_max_f32_e32 v3, v78, v78
	v_max_f32_e32 v2, v3, v2
	v_mul_f32_e32 v3, 0x3c23d70a, v79
	v_max_f32_e32 v4, v79, v79
	v_max_f32_e32 v3, v4, v3
	v_mul_f32_e32 v4, 0x3c23d70a, v80
	v_max_f32_e32 v5, v80, v80
	v_max_f32_e32 v4, v5, v4
	v_mul_f32_e32 v5, 0x3c23d70a, v81
	v_max_f32_e32 v6, v81, v81
	v_max_f32_e32 v5, v6, v5
	v_pk_add_f32 v[2:3], v[14:15], v[2:3]
	v_pk_add_f32 v[4:5], v[16:17], v[4:5]
	ds_write_b128 v160, v[2:5] offset:61536
	ds_read_b128 v[2:5], v145 offset:61440
	ds_read_b128 v[6:9], v62 offset:61440
	ds_read_b128 v[10:13], v63 offset:61440
	ds_read_b128 v[14:17], v64 offset:61440
	s_waitcnt lgkmcnt(3)
	global_store_dwordx4 v[0:1], v[2:5], off offset:384 nt
	s_waitcnt lgkmcnt(2)
	global_store_dwordx4 v[50:51], v[6:9], off offset:384 nt
	s_waitcnt lgkmcnt(1)
	global_store_dwordx4 v[52:53], v[10:13], off offset:384 nt
	s_waitcnt lgkmcnt(0)
	global_store_dwordx4 v[54:55], v[14:17], off offset:384 nt
	s_endpgm

_Z16node_post_kernelPKfS0_PKtS0_S2_S0_S0_S0_S0_S0_Pf:
	s_load_dwordx8 s[12:19], s[0:1], 0x10
	s_load_dwordx8 s[20:27], s[0:1], 0x30
	s_lshr_b32 s28, s2, 3
	v_lshlrev_b32_e32 v162, 4, v0
	v_and_b32_e32 v163, 0xff0, v162
	v_add_u32_e32 v163, 0x2000, v163
	v_and_b32_e32 v168, 0xff, v0
	v_lshlrev_b32_e32 v168, 2, v168
	v_lshlrev_b32_e32 v169, 2, v0
	s_mul_i32 s29, s28, 0x3000
	s_lshr_b32 s32, s2, 7
	s_lshl_b32 s32, s32, 17
	s_and_b32 s33, s28, 15
	s_lshl_b32 s33, s33, 13
	s_add_u32 s32, s32, s33
	s_lshl_b32 s33, s2, 11
	s_waitcnt lgkmcnt(0)
	s_add_u32 s30, s16, s29
	s_addc_u32 s31, s17, 0
	s_add_u32 s34, s12, s32
	s_addc_u32 s35, s13, 0
	s_add_u32 s36, s14, s33
	s_addc_u32 s37, s15, 0
	global_load_dwordx4 v[164:167], v162, s[34:35]
	global_load_dwordx4 v[164:167], v162, s[30:31]
	global_load_dwordx4 v[164:167], v163, s[30:31]
	global_load_dword v164, v169, s[36:37]
	global_load_dword v164, v168, s[18:19]
	global_load_dword v164, v168, s[20:21]
	global_load_dword v164, v168, s[22:23]
	global_load_dword v164, v168, s[24:25]
	global_load_dword v164, v168, s[26:27]
	v_and_b32_e32 v170, 0x7f, v0
	v_min_u32_e32 v170, 0x5f, v170
	v_lshlrev_b32_e32 v170, 12, v170
	v_and_b32_e32 v171, 31, v0
	v_lshlrev_b32_e32 v171, 12, v171
	s_lshr_b32 s38, s2, 7
	s_lshl_b32 s38, s38, 17
	s_add_u32 s38, s12, s38
	s_addc_u32 s39, s13, 0
	global_load_dword v164, v170, s[16:17]
	global_load_dword v164, v171, s[38:39]
	s_load_dwordx4 s[4:7], s[0:1], 0x0
	s_load_dwordx2 s[10:11], s[0:1], 0x10
	s_lshl_b32 s8, s2, 1
	s_bfe_i32 s2, s2, 0x180007
	v_bfe_u32 v19, v0, 6, 1
	s_ashr_i32 s3, s2, 31
	v_or_b32_e32 v2, s8, v19
	s_lshl_b64 s[2:3], s[2:3], 17
	v_ashrrev_i32_e32 v3, 31, v2
	s_waitcnt lgkmcnt(0)
	s_add_u32 s2, s10, s2
	v_lshlrev_b64 v[2:3], 13, v[2:3]
	v_and_b32_e32 v144, 63, v0
	s_addc_u32 s3, s11, s3
	v_lshl_add_u64 v[2:3], s[4:5], 0, v[2:3]
	s_and_b32 s4, s8, 0xffffff00
	v_lshrrev_b32_e32 v1, 6, v0
	v_or_b32_e32 v8, s4, v144
	v_mov_b32_e32 v18, 0
	v_and_b32_e32 v134, 6, v1
	v_ashrrev_i32_e32 v9, 31, v8
	s_ashr_i32 s4, s4, 31
	v_lshlrev_b32_e32 v4, 2, v134
	v_mov_b32_e32 v5, v18
	v_lshl_add_u64 v[10:11], v[8:9], 2, s[6:7]
	v_mov_b32_e32 v9, s4
	v_lshl_add_u64 v[2:3], v[2:3], 0, v[4:5]
	v_lshlrev_b32_e32 v4, 5, v144
	v_lshl_add_u64 v[8:9], v[8:9], 2, s[6:7]
	global_load_dword v38, v[10:11], off
	global_load_dword v39, v[8:9], off offset:256
	v_or_b32_e32 v10, 0x800, v4
	v_mov_b32_e32 v11, v18
	v_lshl_add_u64 v[10:11], v[2:3], 0, v[10:11]
	v_lshl_add_u64 v[6:7], v[2:3], 0, v[4:5]
	global_load_dwordx2 v[20:21], v[10:11], off
	v_or_b32_e32 v10, 0x1000, v4
	v_mov_b32_e32 v11, v18
	global_load_dwordx2 v[6:7], v[6:7], off
	v_lshl_add_u64 v[10:11], v[2:3], 0, v[10:11]
	global_load_dwordx2 v[22:23], v[10:11], off
	global_load_dword v40, v[8:9], off offset:512
	v_or_b32_e32 v4, 0x1800, v4
	v_lshl_add_u64 v[2:3], v[2:3], 0, v[4:5]
	global_load_dword v41, v[8:9], off offset:768
	global_load_dwordx2 v[4:5], v[2:3], off
	v_lshl_or_b32 v24, v1, 10, v144
	v_lshlrev_b32_e32 v142, 4, v24
	v_mov_b32_e32 v143, v18
	v_lshl_add_u64 v[2:3], s[2:3], 0, v[142:143]
	s_movk_i32 s6, 0x1000
	s_load_dwordx2 s[4:5], s[0:1], 0x20
	v_add_co_u32_e32 v8, vcc, s6, v2
	s_movk_i32 s7, 0x2000
	s_nop 0
	v_addc_co_u32_e32 v9, vcc, 0, v3, vcc
	global_load_dwordx4 v[34:37], v[8:9], off
	global_load_dwordx4 v[26:29], v[8:9], off offset:1024
	global_load_dwordx4 v[14:17], v[8:9], off offset:2048
	global_load_dwordx4 v[10:13], v[8:9], off offset:3072
	v_or_b32_e32 v8, 0x200, v24
	v_add_co_u32_e32 v24, vcc, s7, v2
	s_movk_i32 s9, 0x3000
	s_nop 0
	v_addc_co_u32_e32 v25, vcc, 0, v3, vcc
	v_add_co_u32_e32 v30, vcc, s9, v2
	v_lshlrev_b32_e32 v145, 4, v8
	s_nop 0
	v_addc_co_u32_e32 v31, vcc, 0, v3, vcc
	s_waitcnt lgkmcnt(0)
	v_lshl_add_u64 v[2:3], s[4:5], 0, v[142:143]
	v_add_co_u32_e32 v32, vcc, s6, v2
	s_mov_b32 s6, 0xff7fffff
	s_nop 0
	v_addc_co_u32_e32 v33, vcc, 0, v3, vcc
	v_add_co_u32_e32 v46, vcc, s7, v2
	v_lshlrev_b32_e32 v19, 12, v19
	s_nop 0
	v_addc_co_u32_e32 v47, vcc, 0, v3, vcc
	v_add_co_u32_e32 v78, vcc, s9, v2
	v_mov_b32_e32 v2, 0xff7fffff
	s_nop 0
	v_addc_co_u32_e32 v79, vcc, 0, v3, vcc
	v_lshlrev_b32_e32 v134, 9, v134
	v_and_b32_e32 v152, 15, v0
	s_waitcnt vmcnt(11)
	v_cmp_neq_f32_e32 vcc, 0, v38
	s_waitcnt vmcnt(8)
	s_nop 0
	v_cndmask_b32_e32 v3, v2, v6, vcc
	v_cndmask_b32_e32 v6, v2, v7, vcc
	v_cmp_neq_f32_e32 vcc, 0, v39
	s_nop 1
	v_cndmask_b32_e32 v7, v2, v20, vcc
	v_cndmask_b32_e32 v8, v2, v21, vcc
	s_waitcnt vmcnt(6)
	v_cmp_neq_f32_e32 vcc, 0, v40
	v_max3_f32 v9, v3, s6, v7
	v_max3_f32 v20, v6, s6, v8
	v_cndmask_b32_e32 v21, v2, v22, vcc
	v_cndmask_b32_e32 v22, v2, v23, vcc
	s_waitcnt vmcnt(5)
	v_cmp_neq_f32_e32 vcc, 0, v41
	s_waitcnt vmcnt(4)
	s_nop 0
	v_cndmask_b32_e32 v4, v2, v4, vcc
	v_cndmask_b32_e32 v2, v2, v5, vcc
	v_max3_f32 v5, v9, v21, v4
	v_max3_f32 v9, v20, v22, v2
	s_nop 0
	v_mov_b32_dpp v20, v5 quad_perm:[1,0,3,2] row_mask:0xf bank_mask:0xf bound_ctrl:1
	v_max_f32_e32 v20, v20, v20
	v_max_f32_e32 v5, v5, v20
	s_nop 1
	v_mov_b32_dpp v20, v5 quad_perm:[2,3,0,1] row_mask:0xf bank_mask:0xf bound_ctrl:1
	v_max_f32_e32 v20, v20, v20
	v_max_f32_e32 v5, v5, v20
	s_nop 1
	v_mov_b32_dpp v20, v5 row_half_mirror row_mask:0xf bank_mask:0xf bound_ctrl:1
	v_max_f32_e32 v20, v20, v20
	v_max_f32_e32 v5, v5, v20
	s_nop 1
	v_mov_b32_dpp v20, v5 row_mirror row_mask:0xf bank_mask:0xf bound_ctrl:1
	v_max_f32_e32 v20, v20, v20
	v_max_f32_e32 v5, v5, v20
	v_mov_b32_e32 v20, v5
	s_nop 1
	v_permlane16_swap_b32_e32 v5, v20
	v_max_f32_e32 v20, v20, v20
	v_max_f32_e32 v5, v5, v5
	v_max_f32_e32 v5, v5, v20
	v_mov_b32_e32 v20, v5
	s_nop 1
	v_permlane32_swap_b32_e32 v5, v20
	v_max_f32_e32 v20, v20, v20
	v_max_f32_e32 v5, v5, v5
	v_max_f32_e32 v5, v5, v20
	v_mov_b32_dpp v20, v9 quad_perm:[1,0,3,2] row_mask:0xf bank_mask:0xf bound_ctrl:1
	v_max_f32_e32 v20, v20, v20
	v_max_f32_e32 v9, v9, v20
	v_sub_f32_e32 v3, v3, v5
	v_mul_f32_e32 v3, 0x3fb8aa3b, v3
	v_mov_b32_dpp v20, v9 quad_perm:[2,3,0,1] row_mask:0xf bank_mask:0xf bound_ctrl:1
	v_max_f32_e32 v20, v20, v20
	v_max_f32_e32 v9, v9, v20
	v_sub_f32_e32 v4, v4, v5
	v_mul_f32_e32 v4, 0x3fb8aa3b, v4
	v_mov_b32_dpp v20, v9 row_half_mirror row_mask:0xf bank_mask:0xf bound_ctrl:1
	v_max_f32_e32 v20, v20, v20
	v_max_f32_e32 v9, v9, v20
	v_exp_f32_e32 v139, v4
	s_nop 0
	v_mov_b32_dpp v20, v9 row_mirror row_mask:0xf bank_mask:0xf bound_ctrl:1
	v_max_f32_e32 v20, v20, v20
	v_max_f32_e32 v9, v9, v20
	v_mov_b32_e32 v20, v9
	s_nop 1
	v_permlane16_swap_b32_e32 v9, v20
	v_max_f32_e32 v20, v20, v20
	v_max_f32_e32 v9, v9, v9
	v_max_f32_e32 v9, v9, v20
	v_mov_b32_e32 v20, v9
	s_nop 1
	v_permlane32_swap_b32_e32 v9, v20
	v_max_f32_e32 v20, v20, v20
	v_max_f32_e32 v9, v9, v9
	v_max_f32_e32 v9, v9, v20
	v_exp_f32_e32 v20, v3
	v_sub_f32_e32 v3, v6, v9
	v_mul_f32_e32 v3, 0x3fb8aa3b, v3
	v_exp_f32_e32 v135, v3
	v_sub_f32_e32 v3, v7, v5
	v_mul_f32_e32 v3, 0x3fb8aa3b, v3
	v_sub_f32_e32 v7, v21, v5
	v_exp_f32_e32 v136, v3
	v_mul_f32_e32 v7, 0x3fb8aa3b, v7
	v_sub_f32_e32 v3, v8, v9
	v_exp_f32_e32 v21, v7
	v_mul_f32_e32 v3, 0x3fb8aa3b, v3
	v_exp_f32_e32 v137, v3
	v_add_f32_e32 v3, 0, v20
	v_sub_f32_e32 v2, v2, v9
	v_add_f32_e32 v3, v3, v136
	v_mul_f32_e32 v2, 0x3fb8aa3b, v2
	v_exp_f32_e32 v140, v2
	v_add_f32_e32 v2, v3, v21
	v_add_f32_e32 v2, v2, v139
	v_sub_f32_e32 v7, v22, v9
	v_mul_f32_e32 v7, 0x3fb8aa3b, v7
	v_add_f32_dpp v2, v2, v2 quad_perm:[1,0,3,2] row_mask:0xf bank_mask:0xf bound_ctrl:1
	v_exp_f32_e32 v138, v7
	v_add_f32_e32 v6, 0, v135
	v_add_f32_dpp v2, v2, v2 quad_perm:[2,3,0,1] row_mask:0xf bank_mask:0xf bound_ctrl:1
	v_add_f32_e32 v6, v6, v137
	v_add_f32_e32 v3, v6, v138
	v_add_f32_dpp v2, v2, v2 row_half_mirror row_mask:0xf bank_mask:0xf bound_ctrl:1
	v_add_f32_e32 v3, v3, v140
	s_nop 0
	v_add_f32_dpp v2, v2, v2 row_mirror row_mask:0xf bank_mask:0xf bound_ctrl:1
	v_mov_b32_e32 v4, v2
	s_nop 1
	v_permlane16_swap_b32_e32 v2, v4
	v_add_f32_e32 v2, v2, v4
	v_mov_b32_e32 v4, v2
	s_nop 1
	v_permlane32_swap_b32_e32 v2, v4
	v_add_f32_e32 v141, v2, v4
	s_nop 0
	v_add_f32_dpp v2, v3, v3 quad_perm:[1,0,3,2] row_mask:0xf bank_mask:0xf bound_ctrl:1
	v_div_scale_f32 v143, s[6:7], v141, v141, 1.0
	s_nop 0
	v_add_f32_dpp v2, v2, v2 quad_perm:[2,3,0,1] row_mask:0xf bank_mask:0xf bound_ctrl:1
	v_rcp_f32_e32 v146, v143
	v_div_scale_f32 v148, vcc, 1.0, v141, 1.0
	v_add_f32_dpp v2, v2, v2 row_half_mirror row_mask:0xf bank_mask:0xf bound_ctrl:1
	s_nop 1
	v_add_f32_dpp v2, v2, v2 row_mirror row_mask:0xf bank_mask:0xf bound_ctrl:1
	v_mov_b32_e32 v3, v2
	s_nop 1
	v_permlane16_swap_b32_e32 v2, v3
	v_add_f32_e32 v2, v2, v3
	v_mov_b32_e32 v3, v2
	s_nop 1
	v_permlane32_swap_b32_e32 v2, v3
	v_add_f32_e32 v147, v2, v3
	v_fma_f32 v2, -v143, v146, 1.0
	v_fmac_f32_e32 v146, v2, v146
	global_load_dwordx4 v[90:93], v[24:25], off offset:1024
	global_load_dwordx4 v[82:85], v[24:25], off offset:2048
	global_load_dwordx4 v[74:77], v[24:25], off offset:3072
	global_load_dwordx4 v[66:69], v[30:31], off
	global_load_dwordx4 v[58:61], v[30:31], off offset:1024
	global_load_dwordx4 v[50:53], v[30:31], off offset:2048
	global_load_dwordx4 v[42:45], v[30:31], off offset:3072
	global_load_dwordx4 v[54:57], v[32:33], off
	global_load_dwordx4 v[38:41], v[32:33], off offset:1024
	global_load_dwordx4 v[6:9], v[32:33], off offset:2048
	global_load_dwordx4 v[2:5], v[32:33], off offset:3072
	global_load_dwordx4 v[102:105], v[46:47], off offset:1024
	global_load_dwordx4 v[86:89], v[46:47], off offset:2048
	global_load_dwordx4 v[70:73], v[46:47], off offset:3072
	global_load_dwordx4 v[62:65], v[78:79], off
	s_nop 0
	global_load_dwordx4 v[46:49], v[78:79], off offset:1024
	global_load_dwordx4 v[30:33], v[78:79], off offset:2048
	global_load_dwordx4 v[22:25], v[78:79], off offset:3072
	global_load_dwordx4 v[122:125], v142, s[2:3]
	global_load_dwordx4 v[114:117], v142, s[2:3] offset:1024
	global_load_dwordx4 v[106:109], v142, s[2:3] offset:2048
	global_load_dwordx4 v[98:101], v142, s[2:3] offset:3072
	global_load_dwordx4 v[126:129], v142, s[4:5]
	global_load_dwordx4 v[110:113], v142, s[4:5] offset:1024
	global_load_dwordx4 v[94:97], v142, s[4:5] offset:2048
	global_load_dwordx4 v[78:81], v142, s[4:5] offset:3072
	global_load_dwordx4 v[130:133], v145, s[2:3]
	global_load_dwordx4 v[118:121], v145, s[4:5]
	v_mul_f32_e32 v149, v148, v146
	v_fma_f32 v150, -v143, v149, v148
	v_fmac_f32_e32 v149, v150, v146
	v_fma_f32 v143, -v143, v149, v148
	v_div_scale_f32 v148, s[2:3], v147, v147, 1.0
	v_rcp_f32_e32 v150, v148
	v_div_fmas_f32 v143, v143, v146, v149
	v_div_fixup_f32 v141, v143, v141, 1.0
	v_mul_f32_e32 v20, v141, v20
	v_fma_f32 v143, -v148, v150, 1.0
	v_fmac_f32_e32 v150, v143, v150
	v_div_scale_f32 v143, vcc, 1.0, v147, 1.0
	v_mul_f32_e32 v146, v143, v150
	v_fma_f32 v149, -v148, v146, v143
	v_fmac_f32_e32 v146, v149, v150
	v_fma_f32 v143, -v148, v146, v143
	v_div_fmas_f32 v143, v143, v150, v146
	v_div_fixup_f32 v143, v143, v147, 1.0
	v_lshlrev_b32_e32 v146, 1, v144
	v_lshlrev_b32_e32 v147, 9, v1
	v_bfe_u32 v148, v20, 16, 1
	s_movk_i32 s2, 0x7fff
	v_add3_u32 v20, v20, v148, s2
	v_or3_b32 v148, v147, v19, v146
	v_or3_b32 v19, v19, v134, v146
	ds_write_b16_d16_hi v19, v20
	v_mul_f32_e32 v20, v143, v135
	v_bfe_u32 v134, v20, 16, 1
	v_add3_u32 v20, v20, v134, s2
	v_or_b32_e32 v134, 0x200, v148
	ds_write_b16_d16_hi v134, v20
	v_mul_f32_e32 v20, v141, v136
	v_bfe_u32 v134, v20, 16, 1
	v_add3_u32 v20, v20, v134, s2
	ds_write_b16_d16_hi v19, v20 offset:128
	v_mul_f32_e32 v20, v143, v137
	v_bfe_u32 v134, v20, 16, 1
	v_add3_u32 v20, v20, v134, s2
	v_or_b32_e32 v134, 0x280, v148
	ds_write_b16_d16_hi v134, v20
	v_mul_f32_e32 v20, v141, v21
	v_bfe_u32 v21, v20, 16, 1
	v_add3_u32 v20, v20, v21, s2
	ds_write_b16_d16_hi v19, v20 offset:256
	v_mul_f32_e32 v20, v143, v138
	v_bfe_u32 v21, v20, 16, 1
	v_add3_u32 v20, v20, v21, s2
	v_or_b32_e32 v21, 0x300, v148
	ds_write_b16_d16_hi v21, v20
	v_mul_f32_e32 v20, v141, v139
	v_bfe_u32 v21, v20, 16, 1
	v_add3_u32 v20, v20, v21, s2
	ds_write_b16_d16_hi v19, v20 offset:384
	v_mul_f32_e32 v19, v143, v140
	v_bfe_u32 v20, v19, 16, 1
	v_add3_u32 v19, v19, v20, s2
	v_or_b32_e32 v20, 0x380, v148
	ds_write_b16_d16_hi v20, v19
	v_lshrrev_b32_e32 v20, 1, v0
	v_and_b32_e32 v20, 24, v20
	v_lshlrev_b32_e32 v19, 12, v152
	v_lshlrev_b32_e32 v153, 1, v20
	v_or3_b32 v143, v147, v19, v153
	v_cmp_gt_u32_e64 s[2:3], 2, v152
	v_mov_b32_e32 v138, 0
	v_mov_b32_e32 v139, 0
	v_mov_b32_e32 v140, 0
	v_mov_b32_e32 v141, 0
	s_waitcnt lgkmcnt(0)
	s_barrier
	s_and_saveexec_b64 s[6:7], s[2:3]
	ds_read_b128 v[138:141], v143
	s_or_b64 exec, exec, s[6:7]
	s_waitcnt vmcnt(9) lgkmcnt(0)
	v_mfma_f32_16x16x32_bf16 v[134:137], v[122:125], v[138:141], 0
	v_mov_b32_e32 v19, 0
	v_mov_b32_e32 v20, 0
	v_mov_b32_e32 v21, 0
	s_waitcnt vmcnt(1)
	v_mfma_f32_16x16x32_bf16 v[130:133], v[130:133], v[138:141], 0
	s_and_saveexec_b64 s[6:7], s[2:3]
	ds_read_b128 v[18:21], v143 offset:64
	s_or_b64 exec, exec, s[6:7]
	s_waitcnt lgkmcnt(0)
	v_mfma_f32_16x16x32_bf16 v[134:137], v[114:117], v[18:21], v[134:137]
	v_mov_b32_e32 v122, 0
	v_mov_b32_e32 v114, 0
	v_mov_b32_e32 v115, 0
	v_mfma_f32_16x16x32_bf16 v[18:21], v[90:93], v[18:21], v[130:133]
	v_mov_b32_e32 v116, 0
	v_mov_b32_e32 v117, 0
	s_and_saveexec_b64 s[6:7], s[2:3]
	ds_read_b128 v[114:117], v143 offset:128
	s_or_b64 exec, exec, s[6:7]
	s_waitcnt lgkmcnt(0)
	v_mfma_f32_16x16x32_bf16 v[90:93], v[106:109], v[114:117], v[134:137]
	v_mov_b32_e32 v123, 0
	v_mov_b32_e32 v124, 0
	v_mov_b32_e32 v125, 0
	v_mfma_f32_16x16x32_bf16 v[106:109], v[82:85], v[114:117], v[18:21]
	s_and_saveexec_b64 s[6:7], s[2:3]
	ds_read_b128 v[122:125], v143 offset:192
	s_or_b64 exec, exec, s[6:7]
	s_waitcnt lgkmcnt(0)
	v_mfma_f32_16x16x32_bf16 v[98:101], v[98:101], v[122:125], v[90:93]
	v_mov_b32_e32 v18, 0
	v_mov_b32_e32 v82, 0
	v_mov_b32_e32 v83, 0
	v_mfma_f32_16x16x32_bf16 v[90:93], v[74:77], v[122:125], v[106:109]
	v_mov_b32_e32 v84, 0
	v_mov_b32_e32 v85, 0
	s_and_saveexec_b64 s[6:7], s[2:3]
	ds_read_b128 v[82:85], v143 offset:256
	s_or_b64 exec, exec, s[6:7]
	s_waitcnt lgkmcnt(0)
	v_mfma_f32_16x16x32_bf16 v[74:77], v[34:37], v[82:85], v[98:101]
	v_mov_b32_e32 v19, 0
	v_mov_b32_e32 v20, 0
	v_mov_b32_e32 v21, 0
	v_mfma_f32_16x16x32_bf16 v[66:69], v[66:69], v[82:85], v[90:93]
	s_and_saveexec_b64 s[6:7], s[2:3]
	ds_read_b128 v[18:21], v143 offset:320
	s_or_b64 exec, exec, s[6:7]
	s_waitcnt lgkmcnt(0)
	v_mfma_f32_16x16x32_bf16 v[74:77], v[26:29], v[18:21], v[74:77]
	v_mov_b32_e32 v34, 0
	v_mov_b32_e32 v26, 0
	v_mov_b32_e32 v27, 0
	v_mfma_f32_16x16x32_bf16 v[18:21], v[58:61], v[18:21], v[66:69]
	v_mov_b32_e32 v28, 0
	v_mov_b32_e32 v29, 0
	s_and_saveexec_b64 s[6:7], s[2:3]
	ds_read_b128 v[26:29], v143 offset:384
	s_or_b64 exec, exec, s[6:7]
	s_waitcnt lgkmcnt(0)
	v_mfma_f32_16x16x32_bf16 v[14:17], v[14:17], v[26:29], v[74:77]
	v_mov_b32_e32 v35, 0
	v_mov_b32_e32 v36, 0
	v_mov_b32_e32 v37, 0
	v_mfma_f32_16x16x32_bf16 v[18:21], v[50:53], v[26:29], v[18:21]
	s_and_saveexec_b64 s[6:7], s[2:3]
	ds_read_b128 v[34:37], v143 offset:448
	s_or_b64 exec, exec, s[6:7]
	s_waitcnt lgkmcnt(0)
	v_mfma_f32_16x16x32_bf16 v[14:17], v[10:13], v[34:37], v[14:17]
	v_lshrrev_b32_e32 v155, 4, v144
	v_mfma_f32_16x16x32_bf16 v[10:13], v[42:45], v[34:37], v[18:21]
	s_and_saveexec_b64 s[6:7], s[2:3]
	s_cbranch_execz .LBB2_18
	s_nop 0
	v_lshlrev_b32_e32 v18, 9, v152
	v_and_b32_e32 v19, 0x1c0, v0
	v_lshlrev_b32_e32 v20, 3, v155
	v_or3_b32 v18, v18, v19, v20
	v_mov_b32_e32 v19, 1
	v_and_b32_sdwa v20, v16, v19 dst_sel:DWORD dst_unused:UNUSED_PAD src0_sel:WORD_1 src1_sel:DWORD
	s_movk_i32 s9, 0x7fff
	v_and_b32_sdwa v21, v14, v19 dst_sel:DWORD dst_unused:UNUSED_PAD src0_sel:WORD_1 src1_sel:DWORD
	v_add3_u32 v16, v16, v20, s9
	v_and_b32_sdwa v20, v17, v19 dst_sel:DWORD dst_unused:UNUSED_PAD src0_sel:WORD_1 src1_sel:DWORD
	v_add3_u32 v14, v14, v21, s9
	v_and_b32_sdwa v21, v15, v19 dst_sel:DWORD dst_unused:UNUSED_PAD src0_sel:WORD_1 src1_sel:DWORD
	v_add3_u32 v17, v17, v20, s9
	v_add3_u32 v15, v15, v21, s9
	v_and_b32_e32 v17, 0xffff0000, v17
	v_and_b32_e32 v20, 0xffff0000, v15
	v_or_b32_sdwa v15, v17, v16 dst_sel:DWORD dst_unused:UNUSED_PAD src0_sel:DWORD src1_sel:WORD_1
	v_and_b32_sdwa v16, v12, v19 dst_sel:DWORD dst_unused:UNUSED_PAD src0_sel:WORD_1 src1_sel:DWORD
	v_and_b32_sdwa v17, v10, v19 dst_sel:DWORD dst_unused:UNUSED_PAD src0_sel:WORD_1 src1_sel:DWORD
	v_add3_u32 v10, v10, v17, s9
	v_add3_u32 v12, v12, v16, s9
	v_and_b32_sdwa v16, v13, v19 dst_sel:DWORD dst_unused:UNUSED_PAD src0_sel:WORD_1 src1_sel:DWORD
	v_and_b32_sdwa v17, v11, v19 dst_sel:DWORD dst_unused:UNUSED_PAD src0_sel:WORD_1 src1_sel:DWORD
	v_add3_u32 v13, v13, v16, s9
	v_add3_u32 v11, v11, v17, s9
	v_and_b32_e32 v13, 0xffff0000, v13
	v_and_b32_e32 v16, 0xffff0000, v11
	v_or_b32_sdwa v14, v20, v14 dst_sel:DWORD dst_unused:UNUSED_PAD src0_sel:DWORD src1_sel:WORD_1
	v_or_b32_sdwa v11, v13, v12 dst_sel:DWORD dst_unused:UNUSED_PAD src0_sel:DWORD src1_sel:WORD_1
	v_or_b32_sdwa v10, v16, v10 dst_sel:DWORD dst_unused:UNUSED_PAD src0_sel:DWORD src1_sel:WORD_1
	v_add_u32_e32 v12, 0x2800, v18
	ds_write2_b64 v12, v[14:15], v[10:11] offset1:4

	.amdhsa_kernel _Z16node_post_kernelPKfS0_PKtS0_S2_S0_S0_S0_S0_S0_Pf
		.amdhsa_group_segment_fixed_size 12288
		.amdhsa_private_segment_fixed_size 0
		.amdhsa_kernarg_size 88
		.amdhsa_user_sgpr_count 2
		.amdhsa_user_sgpr_dispatch_ptr 0
		.amdhsa_user_sgpr_queue_ptr 0
		.amdhsa_user_sgpr_kernarg_segment_ptr 1
		.amdhsa_user_sgpr_dispatch_id 0
		.amdhsa_user_sgpr_kernarg_preload_length 0
		.amdhsa_user_sgpr_kernarg_preload_offset 0
		.amdhsa_user_sgpr_private_segment_size 0
		.amdhsa_uses_dynamic_stack 0
		.amdhsa_enable_private_segment 0
		.amdhsa_system_sgpr_workgroup_id_x 1
		.amdhsa_system_sgpr_workgroup_id_y 0
		.amdhsa_system_sgpr_workgroup_id_z 0
		.amdhsa_system_sgpr_workgroup_info 0
		.amdhsa_system_vgpr_workitem_id 0
		.amdhsa_next_free_vgpr 172
		.amdhsa_next_free_sgpr 40
		.amdhsa_accum_offset 172
		.amdhsa_reserve_vcc 1
		.amdhsa_float_round_mode_32 0
		.amdhsa_float_round_mode_16_64 0
		.amdhsa_float_denorm_mode_32 3
		.amdhsa_float_denorm_mode_16_64 3
		.amdhsa_dx10_clamp 1
		.amdhsa_ieee_mode 1
		.amdhsa_fp16_overflow 0
		.amdhsa_tg_split 0
		.amdhsa_exception_fp_ieee_invalid_op 0
		.amdhsa_exception_fp_denorm_src 0
		.amdhsa_exception_fp_ieee_div_zero 0
		.amdhsa_exception_fp_ieee_overflow 0
		.amdhsa_exception_fp_ieee_underflow 0
		.amdhsa_exception_fp_ieee_inexact 0
		.amdhsa_exception_int_div_zero 0
	.end_amdhsa_kernel

amdhsa.kernels:
  - .agpr_count:     0
    .args:
      - .actual_access:  read_only
        .address_space:  global
        .offset:         0
        .size:           8
        .value_kind:     global_buffer
      - .actual_access:  read_only
        .address_space:  global
        .offset:         8
        .size:           8
        .value_kind:     global_buffer
      - .actual_access:  read_only
        .address_space:  global
        .offset:         16
        .size:           8
        .value_kind:     global_buffer
      - .actual_access:  read_only
        .address_space:  global
        .offset:         24
        .size:           8
        .value_kind:     global_buffer
      - .actual_access:  read_only
        .address_space:  global
        .offset:         32
        .size:           8
        .value_kind:     global_buffer
      - .actual_access:  read_only
        .address_space:  global
        .offset:         40
        .size:           8
        .value_kind:     global_buffer
      - .actual_access:  read_only
        .address_space:  global
        .offset:         48
        .size:           8
        .value_kind:     global_buffer
      - .actual_access:  read_only
        .address_space:  global
        .offset:         56
        .size:           8
        .value_kind:     global_buffer
      - .actual_access:  read_only
        .address_space:  global
        .offset:         64
        .size:           8
        .value_kind:     global_buffer
      - .actual_access:  read_only
        .address_space:  global
        .offset:         72
        .size:           8
        .value_kind:     global_buffer
      - .actual_access:  read_only
        .address_space:  global
        .offset:         80
        .size:           8
        .value_kind:     global_buffer
      - .actual_access:  write_only
        .address_space:  global
        .offset:         88
        .size:           8
        .value_kind:     global_buffer
      - .actual_access:  write_only
        .address_space:  global
        .offset:         96
        .size:           8
        .value_kind:     global_buffer
      - .actual_access:  read_only
        .address_space:  global
        .offset:         104
        .size:           8
        .value_kind:     global_buffer
      - .actual_access:  read_only
        .address_space:  global
        .offset:         112
        .size:           8
        .value_kind:     global_buffer
      - .actual_access:  read_only
        .address_space:  global
        .offset:         120
        .size:           8
        .value_kind:     global_buffer
      - .actual_access:  read_only
        .address_space:  global
        .offset:         128
        .size:           8
        .value_kind:     global_buffer
      - .actual_access:  read_only
        .address_space:  global
        .offset:         136
        .size:           8
        .value_kind:     global_buffer
      - .actual_access:  read_only
        .address_space:  global
        .offset:         144
        .size:           8
        .value_kind:     global_buffer
      - .actual_access:  write_only
        .address_space:  global
        .offset:         152
        .size:           8
        .value_kind:     global_buffer
      - .actual_access:  write_only
        .address_space:  global
        .offset:         160
        .size:           8
        .value_kind:     global_buffer
      - .actual_access:  write_only
        .address_space:  global
        .offset:         168
        .size:           8
        .value_kind:     global_buffer
      - .actual_access:  read_only
        .address_space:  global
        .offset:         176
        .size:           8
        .value_kind:     global_buffer
      - .actual_access:  read_only
        .address_space:  global
        .offset:         184
        .size:           8
        .value_kind:     global_buffer
      - .actual_access:  read_only
        .address_space:  global
        .offset:         192
        .size:           8
        .value_kind:     global_buffer
      - .actual_access:  write_only
        .address_space:  global
        .offset:         200
        .size:           8
        .value_kind:     global_buffer
    .group_segment_fixed_size: 40960
    .kernarg_segment_align: 8
    .kernarg_segment_size: 208
    .language:       OpenCL C
    .language_version:
      - 2
      - 0
    .max_flat_workgroup_size: 256
    .name:           _Z10pre_kernelPKfS0_S0_S0_S0_S0_S0_S0_S0_S0_S0_PtPfS0_S0_S0_S0_S0_S0_S2_S2_S2_S0_S0_S0_S1_
    .private_segment_fixed_size: 0
    .sgpr_count:     106
    .sgpr_spill_count: 0
    .symbol:         _Z10pre_kernelPKfS0_S0_S0_S0_S0_S0_S0_S0_S0_S0_PtPfS0_S0_S0_S0_S0_S0_S2_S2_S2_S0_S0_S0_S1_.kd
    .uniform_work_group_size: 1
    .uses_dynamic_stack: false
    .vgpr_count:     128
    .vgpr_spill_count: 0
    .wavefront_size: 64
  - .agpr_count:     0
    .args:
      - .actual_access:  read_only
        .address_space:  global
        .offset:         0
        .size:           8
        .value_kind:     global_buffer
      - .address_space:  global
        .offset:         8
        .size:           8
        .value_kind:     global_buffer
      - .address_space:  global
        .offset:         16
        .size:           8
        .value_kind:     global_buffer
      - .address_space:  global
        .offset:         24
        .size:           8
        .value_kind:     global_buffer
      - .address_space:  global
        .offset:         32
        .size:           8
        .value_kind:     global_buffer
      - .actual_access:  write_only
        .address_space:  global
        .offset:         40
        .size:           8
        .value_kind:     global_buffer
      - .actual_access:  write_only
        .address_space:  global
        .offset:         48
        .size:           8
        .value_kind:     global_buffer
    .group_segment_fixed_size: 79872
    .kernarg_segment_align: 8
    .kernarg_segment_size: 56
    .language:       OpenCL C
    .language_version:
      - 2
      - 0
    .max_flat_workgroup_size: 256
    .name:           _Z11edge_kernelPKfPK15HIP_vector_typeIjLj4EES0_S0_S4_PfS5_
    .private_segment_fixed_size: 0
    .sgpr_count:     26
    .sgpr_spill_count: 0
    .symbol:         _Z11edge_kernelPKfPK15HIP_vector_typeIjLj4EES0_S0_S4_PfS5_.kd
    .uniform_work_group_size: 1
    .uses_dynamic_stack: false
    .vgpr_count:     256
    .vgpr_spill_count: 0
    .wavefront_size: 64
  - .agpr_count:     0
    .args:
      - .actual_access:  read_only
        .address_space:  global
        .offset:         0
        .size:           8
        .value_kind:     global_buffer
      - .actual_access:  read_only
        .address_space:  global
        .offset:         8
        .size:           8
        .value_kind:     global_buffer
      - .actual_access:  read_only
        .address_space:  global
        .offset:         16
        .size:           8
        .value_kind:     global_buffer
      - .actual_access:  read_only
        .address_space:  global
        .offset:         24
        .size:           8
        .value_kind:     global_buffer
      - .actual_access:  read_only
        .address_space:  global
        .offset:         32
        .size:           8
        .value_kind:     global_buffer
      - .actual_access:  read_only
        .address_space:  global
        .offset:         40
        .size:           8
        .value_kind:     global_buffer
      - .actual_access:  read_only
        .address_space:  global
        .offset:         48
        .size:           8
        .value_kind:     global_buffer
      - .actual_access:  read_only
        .address_space:  global
        .offset:         56
        .size:           8
        .value_kind:     global_buffer
      - .actual_access:  read_only
        .address_space:  global
        .offset:         64
        .size:           8
        .value_kind:     global_buffer
      - .actual_access:  read_only
        .address_space:  global
        .offset:         72
        .size:           8
        .value_kind:     global_buffer
      - .actual_access:  write_only
        .address_space:  global
        .offset:         80
        .size:           8
        .value_kind:     global_buffer
    .group_segment_fixed_size: 12288
    .kernarg_segment_align: 8
    .kernarg_segment_size: 88
    .language:       OpenCL C
    .language_version:
      - 2
      - 0
    .max_flat_workgroup_size: 512
    .name:           _Z16node_post_kernelPKfS0_PKtS0_S2_S0_S0_S0_S0_S0_Pf
    .private_segment_fixed_size: 0
    .sgpr_count:     46
    .sgpr_spill_count: 0
    .symbol:         _Z16node_post_kernelPKfS0_PKtS0_S2_S0_S0_S0_S0_S0_Pf.kd
    .uniform_work_group_size: 1
    .uses_dynamic_stack: false
    .vgpr_count:     172
    .vgpr_spill_count: 0
    .wavefront_size: 64
